# speedup vs baseline: 1.0113x; 1.0005x over previous
_Z5k_fftPKtPtPKDv2_f:
	s_load_dwordx2 s[6:7], s[0:1], 0x10
	s_load_dwordx2 s[8:9], s[0:1], 0x0
	v_and_b32_e32 v1, 0xf0, v0
	v_and_b32_e32 v18, 15, v0
	v_mul_u32_u24_e32 v1, v1, v18
	v_lshlrev_b32_e32 v1, 3, v1
	s_waitcnt lgkmcnt(0)
	global_load_dwordx2 v[86:87], v1, s[6:7]
	s_lshr_b32 s4, s2, 3
	s_and_b32 s3, s2, 7
	s_and_b32 s4, s4, 0x1ffffff8
	s_or_b32 s4, s4, s3
	s_bfe_u32 s16, s2, 0x30003
	s_lshl_b32 s3, s4, 3
	s_or_b32 s3, s3, s16
	s_mov_b32 s11, 0
	s_lshr_b32 s10, s3, 1
	s_lshl_b64 s[10:11], s[10:11], 14
	s_add_u32 s3, s8, s10
	s_addc_u32 s8, s9, s11
	s_lshr_b32 s2, s2, 2
	s_and_b32 s2, s2, 2
	s_add_u32 s2, s3, s2
	v_mov_b32_e32 v3, 0
	v_lshlrev_b32_e32 v2, 2, v0
	s_addc_u32 s3, s8, 0
	s_movk_i32 s5, 0x1000
	v_lshl_add_u64 v[6:7], s[2:3], 0, v[2:3]
	v_add_co_u32_e32 v8, vcc, s5, v6
	s_movk_i32 s12, 0x2000
	s_nop 0
	v_addc_co_u32_e32 v9, vcc, 0, v7, vcc
	v_add_co_u32_e32 v10, vcc, s12, v6
	s_movk_i32 s13, 0x3000
	s_add_u32 s8, s2, 0x1000000
	v_addc_co_u32_e32 v11, vcc, 0, v7, vcc
	s_addc_u32 s9, s3, 0
	s_add_u32 s20, s2, 0x2000000
	s_addc_u32 s21, s3, 0
	v_lshlrev_b32_e32 v89, 2, v0
	v_or_b32_e32 v90, 0x1000, v89
	v_or_b32_e32 v91, 0x2000, v89
	v_or_b32_e32 v92, 0x3000, v89
	v_add_co_u32_e32 v6, vcc, s13, v6
	v_lshl_add_u64 v[12:13], s[8:9], 0, v[2:3]
	s_nop 0
	v_addc_co_u32_e32 v7, vcc, 0, v7, vcc
	v_add_co_u32_e32 v14, vcc, s5, v12
	v_lshlrev_b32_e32 v1, 3, v0
	s_nop 0
	v_addc_co_u32_e32 v15, vcc, 0, v13, vcc
	v_add_co_u32_e32 v16, vcc, s12, v12
	v_or_b32_e32 v19, 0x1000, v2
	s_nop 0
	v_addc_co_u32_e32 v17, vcc, 0, v13, vcc
	v_add_co_u32_e32 v12, vcc, s13, v12
	v_or_b32_e32 v20, 0x2000, v2
	v_or_b32_e32 v21, 0x3000, v2
	v_addc_co_u32_e32 v13, vcc, 0, v13, vcc
	v_mul_u32_u24_e32 v3, 3, v0
	s_movk_i32 s5, 0x888
	v_lshlrev_b32_e32 v3, 3, v3
	s_mov_b32 s10, 0x3ec3ef15
	s_mov_b32 s11, 0xbf6c835e
	s_mov_b32 s14, s11
	s_mov_b32 s15, s10
	s_mov_b32 s12, 0xbf3504f3
	s_mov_b32 s13, s12
	v_mov_b32_e32 v88, v0
	global_load_ushort v32, v2, s[2:3] nt
	global_load_ushort v33, v2, s[8:9] nt
	global_load_ushort v34, v2, s[2:3] offset:1024 nt
	global_load_ushort v35, v2, s[8:9] offset:1024 nt
	global_load_ushort v36, v2, s[2:3] offset:2048 nt
	global_load_ushort v37, v2, s[8:9] offset:2048 nt
	global_load_ushort v38, v2, s[8:9] offset:3072 nt
	global_load_ushort v39, v2, s[2:3] offset:3072 nt
	global_load_ushort v40, v19, s[2:3] nt
	global_load_ushort v41, v19, s[8:9] nt
	global_load_ushort v42, v[8:9], off offset:1024 nt
	global_load_ushort v43, v[14:15], off offset:1024 nt
	global_load_ushort v44, v[8:9], off offset:2048 nt
	global_load_ushort v45, v[14:15], off offset:2048 nt
	global_load_ushort v46, v[14:15], off offset:3072 nt
	global_load_ushort v47, v[8:9], off offset:3072 nt
	global_load_ushort v48, v20, s[2:3] nt
	global_load_ushort v49, v20, s[8:9] nt
	global_load_ushort v50, v[10:11], off offset:1024 nt
	global_load_ushort v51, v[16:17], off offset:1024 nt
	global_load_ushort v52, v[10:11], off offset:2048 nt
	global_load_ushort v53, v[16:17], off offset:2048 nt
	global_load_ushort v54, v[16:17], off offset:3072 nt
	global_load_ushort v55, v[10:11], off offset:3072 nt
	global_load_ushort v56, v21, s[2:3] nt
	global_load_ushort v57, v21, s[8:9] nt
	global_load_ushort v58, v[6:7], off offset:1024 nt
	global_load_ushort v59, v[12:13], off offset:1024 nt
	global_load_ushort v60, v[6:7], off offset:2048 nt
	global_load_ushort v61, v[12:13], off offset:2048 nt
	global_load_ushort v62, v[12:13], off offset:3072 nt
	global_load_ushort v63, v[6:7], off offset:3072 nt
	v_mul_u32_u24_e32 v5, 5, v0
	v_mul_u32_u24_e32 v6, 6, v0
	v_mul_u32_u24_e32 v7, 7, v0
	v_mul_u32_u24_e32 v9, 9, v0
	v_mul_u32_u24_e32 v10, 10, v0
	v_lshrrev_b32_e32 v16, 1, v0
	v_lshlrev_b32_e32 v2, 4, v0
	v_lshlrev_b32_e32 v4, 5, v0
	v_lshlrev_b32_e32 v8, 6, v0
	v_mul_u32_u24_e32 v11, 11, v0
	v_mul_u32_u24_e32 v12, 12, v0
	v_mul_u32_u24_e32 v13, 13, v0
	v_mul_u32_u24_e32 v14, 14, v0
	v_mul_u32_u24_e32 v15, 15, v0
	v_lshlrev_b32_e32 v5, 3, v5
	v_lshlrev_b32_e32 v6, 3, v6
	v_lshlrev_b32_e32 v7, 3, v7
	v_lshlrev_b32_e32 v9, 3, v9
	v_lshlrev_b32_e32 v64, 3, v10
	v_and_b32_e32 v10, 0x78, v16
	v_lshlrev_b32_e32 v65, 3, v11
	v_lshlrev_b32_e32 v66, 3, v12
	v_lshlrev_b32_e32 v67, 3, v13
	v_lshlrev_b32_e32 v68, 3, v14
	v_lshlrev_b32_e32 v69, 3, v15
	v_mad_u32_u24 v96, v18, s5, v10
	global_load_dwordx2 v[30:31], v1, s[6:7]
	global_load_dwordx2 v[28:29], v2, s[6:7]
	global_load_dwordx2 v[24:25], v4, s[6:7]
	global_load_dwordx2 v[22:23], v8, s[6:7]
	global_load_ushort v112, v89, s[20:21]
	global_load_ushort v113, v89, s[20:21] offset:1024
	global_load_ushort v114, v89, s[20:21] offset:2048
	global_load_ushort v115, v89, s[20:21] offset:3072
	global_load_ushort v116, v90, s[20:21]
	global_load_ushort v117, v90, s[20:21] offset:1024
	global_load_ushort v118, v90, s[20:21] offset:2048
	global_load_ushort v119, v90, s[20:21] offset:3072
	global_load_ushort v120, v91, s[20:21]
	global_load_ushort v121, v91, s[20:21] offset:1024
	global_load_ushort v122, v91, s[20:21] offset:2048
	global_load_ushort v123, v91, s[20:21] offset:3072
	global_load_ushort v124, v92, s[20:21]
	global_load_ushort v125, v92, s[20:21] offset:1024
	global_load_ushort v126, v92, s[20:21] offset:2048
	global_load_ushort v127, v92, s[20:21] offset:3072
	s_nop 0
	s_mov_b32 s6, 0x3f6c835e
	s_mov_b32 s7, 0xbec3ef15
	s_mov_b32 s8, 0x3f3504f3
	s_mov_b32 s9, s8
	s_waitcnt vmcnt(50)
	v_lshl_or_b32 v85, v33, 16, v32
	v_cvt_f32_fp8_e32 v32, v85
	s_waitcnt vmcnt(48)
	v_lshl_or_b32 v84, v35, 16, v34
	v_cvt_f32_fp8_sdwa v33, v85 src0_sel:BYTE_2
	s_waitcnt vmcnt(46)
	v_lshl_or_b32 v83, v37, 16, v36
	v_cvt_f32_fp8_e32 v34, v84
	v_cvt_f32_fp8_sdwa v35, v84 src0_sel:BYTE_2
	s_waitcnt vmcnt(44)
	v_lshl_or_b32 v82, v38, 16, v39
	s_waitcnt vmcnt(42)
	v_lshl_or_b32 v81, v41, 16, v40
	v_cvt_f32_fp8_e32 v40, v81
	s_waitcnt vmcnt(40)
	v_lshl_or_b32 v80, v43, 16, v42
	v_cvt_f32_fp8_sdwa v41, v81 src0_sel:BYTE_2
	s_waitcnt vmcnt(38)
	v_lshl_or_b32 v79, v45, 16, v44
	v_cvt_f32_fp8_e32 v42, v80
	v_cvt_f32_fp8_sdwa v43, v80 src0_sel:BYTE_2
	v_cvt_f32_fp8_e32 v36, v83
	v_cvt_f32_fp8_sdwa v37, v83 src0_sel:BYTE_2
	s_waitcnt vmcnt(36)
	v_lshl_or_b32 v78, v46, 16, v47
	v_cvt_f32_fp8_e32 v44, v79
	s_waitcnt vmcnt(34)
	v_lshl_or_b32 v77, v49, 16, v48
	v_cvt_f32_fp8_e32 v48, v77
	s_waitcnt vmcnt(32)
	v_lshl_or_b32 v76, v51, 16, v50
	v_cvt_f32_fp8_sdwa v49, v77 src0_sel:BYTE_2
	s_waitcnt vmcnt(30)
	v_lshl_or_b32 v75, v53, 16, v52
	v_cvt_f32_fp8_e32 v50, v76
	v_cvt_f32_fp8_sdwa v51, v76 src0_sel:BYTE_2
	s_waitcnt vmcnt(28)
	v_lshl_or_b32 v74, v54, 16, v55
	s_waitcnt vmcnt(26)
	v_lshl_or_b32 v73, v57, 16, v56
	v_cvt_f32_fp8_e32 v56, v73
	s_waitcnt vmcnt(24)
	v_lshl_or_b32 v72, v59, 16, v58
	v_cvt_f32_fp8_sdwa v57, v73 src0_sel:BYTE_2
	s_waitcnt vmcnt(22)
	v_lshl_or_b32 v71, v61, 16, v60
	v_cvt_f32_fp8_e32 v58, v72
	v_cvt_f32_fp8_sdwa v59, v72 src0_sel:BYTE_2
	v_cvt_f32_fp8_sdwa v45, v79 src0_sel:BYTE_2
	v_cvt_f32_fp8_e32 v52, v75
	v_cvt_f32_fp8_sdwa v53, v75 src0_sel:BYTE_2
	v_cvt_f32_fp8_e32 v60, v71
	v_cvt_f32_fp8_sdwa v61, v71 src0_sel:BYTE_2
	s_waitcnt vmcnt(20)
	v_lshl_or_b32 v70, v62, 16, v63
	v_cvt_f32_fp8_e32 v38, v82
	v_cvt_f32_fp8_sdwa v39, v82 src0_sel:BYTE_2
	v_cvt_f32_fp8_e32 v46, v78
	v_cvt_f32_fp8_sdwa v47, v78 src0_sel:BYTE_2
	v_cvt_f32_fp8_e32 v54, v74
	v_cvt_f32_fp8_sdwa v55, v74 src0_sel:BYTE_2
	v_cvt_f32_fp8_e32 v62, v70
	v_cvt_f32_fp8_sdwa v63, v70 src0_sel:BYTE_2
	v_pk_add_f32 v[64:65], v[32:33], v[48:49]
	v_pk_add_f32 v[32:33], v[32:33], v[48:49] neg_lo:[0,1] neg_hi:[0,1]
	v_pk_add_f32 v[48:49], v[40:41], v[56:57]
	v_pk_add_f32 v[40:41], v[40:41], v[56:57] neg_lo:[0,1] neg_hi:[0,1]
	v_pk_add_f32 v[56:57], v[64:65], v[48:49]
	v_pk_add_f32 v[48:49], v[64:65], v[48:49] neg_lo:[0,1] neg_hi:[0,1]
	v_pk_add_f32 v[64:65], v[32:33], v[40:41] op_sel:[0,1] op_sel_hi:[1,0] neg_hi:[0,1]
	v_pk_add_f32 v[32:33], v[32:33], v[40:41] op_sel:[0,1] op_sel_hi:[1,0] neg_lo:[0,1]
	v_pk_add_f32 v[40:41], v[34:35], v[50:51]
	v_pk_add_f32 v[34:35], v[34:35], v[50:51] neg_lo:[0,1] neg_hi:[0,1]
	v_pk_add_f32 v[50:51], v[42:43], v[58:59]
	v_pk_add_f32 v[42:43], v[42:43], v[58:59] neg_lo:[0,1] neg_hi:[0,1]
	v_pk_add_f32 v[58:59], v[40:41], v[50:51]
	v_pk_add_f32 v[40:41], v[40:41], v[50:51] neg_lo:[0,1] neg_hi:[0,1]
	v_pk_add_f32 v[50:51], v[34:35], v[42:43] op_sel:[0,1] op_sel_hi:[1,0] neg_hi:[0,1]
	v_pk_add_f32 v[34:35], v[34:35], v[42:43] op_sel:[0,1] op_sel_hi:[1,0] neg_lo:[0,1]
	v_pk_add_f32 v[42:43], v[36:37], v[52:53]
	v_pk_add_f32 v[36:37], v[36:37], v[52:53] neg_lo:[0,1] neg_hi:[0,1]
	v_pk_add_f32 v[52:53], v[44:45], v[60:61]
	v_pk_add_f32 v[44:45], v[44:45], v[60:61] neg_lo:[0,1] neg_hi:[0,1]
	v_pk_add_f32 v[60:61], v[42:43], v[52:53]
	v_pk_add_f32 v[42:43], v[42:43], v[52:53] neg_lo:[0,1] neg_hi:[0,1]
	v_pk_add_f32 v[52:53], v[36:37], v[44:45] op_sel:[0,1] op_sel_hi:[1,0] neg_hi:[0,1]
	v_pk_add_f32 v[36:37], v[36:37], v[44:45] op_sel:[0,1] op_sel_hi:[1,0] neg_lo:[0,1]
	v_pk_add_f32 v[44:45], v[38:39], v[54:55]
	v_pk_add_f32 v[38:39], v[38:39], v[54:55] neg_lo:[0,1] neg_hi:[0,1]
	v_pk_add_f32 v[54:55], v[46:47], v[62:63]
	v_pk_add_f32 v[46:47], v[46:47], v[62:63] neg_lo:[0,1] neg_hi:[0,1]
	v_pk_add_f32 v[62:63], v[44:45], v[54:55]
	v_pk_add_f32 v[44:45], v[44:45], v[54:55] neg_lo:[0,1] neg_hi:[0,1]
	v_pk_add_f32 v[54:55], v[38:39], v[46:47] op_sel:[0,1] op_sel_hi:[1,0] neg_hi:[0,1]
	v_pk_add_f32 v[38:39], v[38:39], v[46:47] op_sel:[0,1] op_sel_hi:[1,0] neg_lo:[0,1]
	v_pk_mul_f32 v[46:47], v[50:51], s[6:7] op_sel:[0,0] op_sel_hi:[0,1]
	v_pk_fma_f32 v[46:47], v[50:51], s[6:7], v[46:47] op_sel:[1,1,0] op_sel_hi:[1,0,1] neg_lo:[0,1,0]
	v_pk_mul_f32 v[50:51], v[34:35], s[10:11] op_sel:[0,0] op_sel_hi:[0,1]
	v_pk_fma_f32 v[50:51], v[34:35], s[10:11], v[50:51] op_sel:[1,1,0] op_sel_hi:[1,0,1] neg_lo:[0,1,0]
	v_pk_add_f32 v[34:35], v[52:53], v[52:53] op_sel:[0,1] op_sel_hi:[1,0] neg_hi:[0,1]
	v_pk_add_f32 v[40:41], v[40:41], v[40:41] op_sel:[0,1] op_sel_hi:[1,0] neg_hi:[0,1]
	s_nop 0
	v_pk_mul_f32 v[52:53], v[54:55], s[10:11] op_sel:[0,0] op_sel_hi:[0,1]
	v_pk_fma_f32 v[52:53], v[54:55], s[10:11], v[52:53] op_sel:[1,1,0] op_sel_hi:[1,0,1] neg_lo:[0,1,0]
	v_pk_mul_f32 v[54:55], v[38:39], s[14:15] op_sel:[0,0] op_sel_hi:[0,1]
	v_pk_fma_f32 v[54:55], v[38:39], s[14:15], v[54:55] op_sel:[1,1,0] op_sel_hi:[1,0,1] neg_lo:[0,1,0]
	v_pk_add_f32 v[38:39], v[56:57], v[60:61]
	v_pk_mul_f32 v[34:35], v[34:35], s[8:9]
	v_pk_add_f32 v[56:57], v[56:57], v[60:61] neg_lo:[0,1] neg_hi:[0,1]
	v_pk_add_f32 v[60:61], v[58:59], v[62:63]
	v_pk_add_f32 v[58:59], v[58:59], v[62:63] neg_lo:[0,1] neg_hi:[0,1]
	v_pk_mul_f32 v[40:41], v[40:41], s[8:9]
	v_pk_add_f32 v[36:37], v[36:37], v[36:37] op_sel:[0,1] op_sel_hi:[1,0] neg_lo:[0,1]
	v_pk_add_f32 v[44:45], v[44:45], v[44:45] op_sel:[0,1] op_sel_hi:[1,0] neg_lo:[0,1]
	v_pk_add_f32 v[62:63], v[38:39], v[60:61]
	v_pk_add_f32 v[38:39], v[38:39], v[60:61] neg_lo:[0,1] neg_hi:[0,1]
	v_pk_add_f32 v[60:61], v[56:57], v[58:59] op_sel:[0,1] op_sel_hi:[1,0] neg_hi:[0,1]
	v_pk_add_f32 v[56:57], v[56:57], v[58:59] op_sel:[0,1] op_sel_hi:[1,0] neg_lo:[0,1]
	v_pk_add_f32 v[58:59], v[64:65], v[34:35]
	v_pk_add_f32 v[34:35], v[64:65], v[34:35] neg_lo:[0,1] neg_hi:[0,1]
	v_pk_add_f32 v[64:65], v[46:47], v[52:53]
	v_pk_add_f32 v[46:47], v[46:47], v[52:53] neg_lo:[0,1] neg_hi:[0,1]
	v_pk_mul_f32 v[36:37], v[36:37], s[12:13]
	v_pk_mul_f32 v[44:45], v[44:45], s[12:13]
	v_pk_add_f32 v[52:53], v[58:59], v[64:65]
	v_pk_add_f32 v[58:59], v[58:59], v[64:65] neg_lo:[0,1] neg_hi:[0,1]
	v_pk_add_f32 v[64:65], v[34:35], v[46:47] op_sel:[0,1] op_sel_hi:[1,0] neg_hi:[0,1]
	v_pk_add_f32 v[34:35], v[34:35], v[46:47] op_sel:[0,1] op_sel_hi:[1,0] neg_lo:[0,1]
	v_pk_add_f32 v[46:47], v[48:49], v[42:43] op_sel:[0,1] op_sel_hi:[1,0] neg_hi:[0,1]
	v_pk_add_f32 v[42:43], v[48:49], v[42:43] op_sel:[0,1] op_sel_hi:[1,0] neg_lo:[0,1]
	v_pk_add_f32 v[48:49], v[40:41], v[44:45]
	v_pk_add_f32 v[40:41], v[40:41], v[44:45] neg_lo:[0,1] neg_hi:[0,1]
	v_pk_add_f32 v[44:45], v[48:49], v[46:47]
	v_pk_add_f32 v[46:47], v[46:47], v[48:49] neg_lo:[0,1] neg_hi:[0,1]
	v_pk_add_f32 v[48:49], v[42:43], v[40:41] op_sel:[0,1] op_sel_hi:[1,0] neg_hi:[0,1]
	v_pk_add_f32 v[40:41], v[42:43], v[40:41] op_sel:[0,1] op_sel_hi:[1,0] neg_lo:[0,1]
	v_pk_add_f32 v[42:43], v[32:33], v[36:37]
	v_pk_add_f32 v[32:33], v[32:33], v[36:37] neg_lo:[0,1] neg_hi:[0,1]
	v_pk_add_f32 v[36:37], v[50:51], v[54:55]
	v_pk_add_f32 v[50:51], v[50:51], v[54:55] neg_lo:[0,1] neg_hi:[0,1]
	v_pk_add_f32 v[54:55], v[42:43], v[36:37]
	v_pk_add_f32 v[36:37], v[42:43], v[36:37] neg_lo:[0,1] neg_hi:[0,1]
	v_pk_add_f32 v[42:43], v[32:33], v[50:51] op_sel:[0,1] op_sel_hi:[1,0] neg_hi:[0,1]
	v_pk_add_f32 v[32:33], v[32:33], v[50:51] op_sel:[0,1] op_sel_hi:[1,0] neg_lo:[0,1]
	s_waitcnt vmcnt(16)
	v_pk_mul_f32 v[26:27], v[30:31], v[28:29] op_sel:[0,0] op_sel_hi:[0,1]
	v_pk_fma_f32 v[26:27], v[30:31], v[28:29], v[26:27] op_sel:[1,1,0] op_sel_hi:[1,0,1] neg_lo:[0,1,0]
	v_pk_mul_f32 v[20:21], v[30:31], v[24:25] op_sel:[0,0] op_sel_hi:[0,1]
	v_pk_fma_f32 v[20:21], v[30:31], v[24:25], v[20:21] op_sel:[1,1,0] op_sel_hi:[1,0,1] neg_lo:[0,1,0]
	v_pk_mul_f32 v[16:17], v[28:29], v[24:25] op_sel:[0,0] op_sel_hi:[0,1]
	v_pk_fma_f32 v[16:17], v[28:29], v[24:25], v[16:17] op_sel:[1,1,0] op_sel_hi:[1,0,1] neg_lo:[0,1,0]
	v_pk_mul_f32 v[18:19], v[30:31], v[22:23] op_sel:[0,0] op_sel_hi:[0,1]
	v_pk_fma_f32 v[18:19], v[30:31], v[22:23], v[18:19] op_sel:[1,1,0] op_sel_hi:[1,0,1] neg_lo:[0,1,0]
	v_pk_mul_f32 v[12:13], v[28:29], v[22:23] op_sel:[0,0] op_sel_hi:[0,1]
	v_pk_fma_f32 v[12:13], v[28:29], v[22:23], v[12:13] op_sel:[1,1,0] op_sel_hi:[1,0,1] neg_lo:[0,1,0]
	v_pk_mul_f32 v[6:7], v[24:25], v[22:23] op_sel:[0,0] op_sel_hi:[0,1]
	v_pk_fma_f32 v[6:7], v[24:25], v[22:23], v[6:7] op_sel:[1,1,0] op_sel_hi:[1,0,1] neg_lo:[0,1,0]
	v_pk_mul_f32 v[10:11], v[26:27], v[24:25] op_sel:[0,0] op_sel_hi:[0,1]
	v_pk_fma_f32 v[10:11], v[26:27], v[24:25], v[10:11] op_sel:[1,1,0] op_sel_hi:[1,0,1] neg_lo:[0,1,0]
	v_pk_mul_f32 v[14:15], v[26:27], v[22:23] op_sel:[0,0] op_sel_hi:[0,1]
	v_pk_fma_f32 v[14:15], v[26:27], v[22:23], v[14:15] op_sel:[1,1,0] op_sel_hi:[1,0,1] neg_lo:[0,1,0]
	v_pk_mul_f32 v[8:9], v[20:21], v[22:23] op_sel:[0,0] op_sel_hi:[0,1]
	v_pk_fma_f32 v[8:9], v[20:21], v[22:23], v[8:9] op_sel:[1,1,0] op_sel_hi:[1,0,1] neg_lo:[0,1,0]
	v_pk_mul_f32 v[4:5], v[16:17], v[22:23] op_sel:[0,0] op_sel_hi:[0,1]
	v_pk_fma_f32 v[4:5], v[16:17], v[22:23], v[4:5] op_sel:[1,1,0] op_sel_hi:[1,0,1] neg_lo:[0,1,0]
	v_pk_mul_f32 v[2:3], v[10:11], v[22:23] op_sel:[0,0] op_sel_hi:[0,1]
	v_pk_fma_f32 v[2:3], v[10:11], v[22:23], v[2:3] op_sel:[1,1,0] op_sel_hi:[1,0,1] neg_lo:[0,1,0]
	v_pk_mul_f32 v[50:51], v[52:53], v[30:31] op_sel:[0,0] op_sel_hi:[0,1]
	v_pk_fma_f32 v[50:51], v[52:53], v[30:31], v[50:51] op_sel:[1,1,0] op_sel_hi:[1,0,1] neg_lo:[0,1,0]
	ds_write_b64 v1, v[50:51] offset:2184
	v_pk_mul_f32 v[50:51], v[44:45], v[28:29] op_sel:[0,0] op_sel_hi:[0,1]
	v_pk_fma_f32 v[50:51], v[44:45], v[28:29], v[50:51] op_sel:[1,1,0] op_sel_hi:[1,0,1] neg_lo:[0,1,0]
	v_pk_mul_f32 v[44:45], v[54:55], v[26:27] op_sel:[0,0] op_sel_hi:[0,1]
	v_pk_fma_f32 v[44:45], v[54:55], v[26:27], v[44:45] op_sel:[1,1,0] op_sel_hi:[1,0,1] neg_lo:[0,1,0]
	ds_write_b64 v1, v[44:45] offset:6552
	v_pk_mul_f32 v[44:45], v[60:61], v[24:25] op_sel:[0,0] op_sel_hi:[0,1]
	v_pk_fma_f32 v[44:45], v[60:61], v[24:25], v[44:45] op_sel:[1,1,0] op_sel_hi:[1,0,1] neg_lo:[0,1,0]
	ds_write_b64 v1, v[44:45] offset:8736
	v_pk_mul_f32 v[44:45], v[64:65], v[20:21] op_sel:[0,0] op_sel_hi:[0,1]
	v_pk_fma_f32 v[44:45], v[64:65], v[20:21], v[44:45] op_sel:[1,1,0] op_sel_hi:[1,0,1] neg_lo:[0,1,0]
	ds_write_b64 v1, v[44:45] offset:10920
	v_pk_mul_f32 v[44:45], v[48:49], v[16:17] op_sel:[0,0] op_sel_hi:[0,1]
	v_pk_fma_f32 v[44:45], v[48:49], v[16:17], v[44:45] op_sel:[1,1,0] op_sel_hi:[1,0,1] neg_lo:[0,1,0]
	ds_write_b64 v1, v[44:45] offset:13104
	v_pk_mul_f32 v[44:45], v[42:43], v[10:11] op_sel:[0,0] op_sel_hi:[0,1]
	v_pk_fma_f32 v[44:45], v[42:43], v[10:11], v[44:45] op_sel:[1,1,0] op_sel_hi:[1,0,1] neg_lo:[0,1,0]
	v_pk_mul_f32 v[42:43], v[38:39], v[22:23] op_sel:[0,0] op_sel_hi:[0,1]
	v_pk_fma_f32 v[42:43], v[38:39], v[22:23], v[42:43] op_sel:[1,1,0] op_sel_hi:[1,0,1] neg_lo:[0,1,0]
	v_pk_mul_f32 v[38:39], v[58:59], v[18:19] op_sel:[0,0] op_sel_hi:[0,1]
	v_pk_fma_f32 v[38:39], v[58:59], v[18:19], v[38:39] op_sel:[1,1,0] op_sel_hi:[1,0,1] neg_lo:[0,1,0]
	ds_write_b64 v1, v[38:39] offset:19656
	v_pk_mul_f32 v[38:39], v[46:47], v[12:13] op_sel:[0,0] op_sel_hi:[0,1]
	v_pk_fma_f32 v[38:39], v[46:47], v[12:13], v[38:39] op_sel:[1,1,0] op_sel_hi:[1,0,1] neg_lo:[0,1,0]
	ds_write_b64 v1, v[38:39] offset:21840
	v_pk_mul_f32 v[38:39], v[36:37], v[14:15] op_sel:[0,0] op_sel_hi:[0,1]
	v_pk_fma_f32 v[38:39], v[36:37], v[14:15], v[38:39] op_sel:[1,1,0] op_sel_hi:[1,0,1] neg_lo:[0,1,0]
	v_pk_mul_f32 v[36:37], v[56:57], v[6:7] op_sel:[0,0] op_sel_hi:[0,1]
	v_pk_fma_f32 v[36:37], v[56:57], v[6:7], v[36:37] op_sel:[1,1,0] op_sel_hi:[1,0,1] neg_lo:[0,1,0]
	ds_write_b64 v1, v[36:37] offset:26208
	v_pk_mul_f32 v[36:37], v[34:35], v[8:9] op_sel:[0,0] op_sel_hi:[0,1]
	v_pk_fma_f32 v[36:37], v[34:35], v[8:9], v[36:37] op_sel:[1,1,0] op_sel_hi:[1,0,1] neg_lo:[0,1,0]
	v_pk_mul_f32 v[34:35], v[40:41], v[4:5] op_sel:[0,0] op_sel_hi:[0,1]
	v_pk_fma_f32 v[34:35], v[40:41], v[4:5], v[34:35] op_sel:[1,1,0] op_sel_hi:[1,0,1] neg_lo:[0,1,0]
	ds_write_b64 v1, v[34:35] offset:30576
	v_pk_mul_f32 v[34:35], v[32:33], v[2:3] op_sel:[0,0] op_sel_hi:[0,1]
	v_pk_fma_f32 v[34:35], v[32:33], v[2:3], v[34:35] op_sel:[1,1,0] op_sel_hi:[1,0,1] neg_lo:[0,1,0]
	ds_write_b64 v1, v[62:63]
	ds_write_b64 v1, v[50:51] offset:4368
	ds_write_b64 v1, v[44:45] offset:15288
	ds_write_b64 v1, v[42:43] offset:17472
	ds_write_b64 v1, v[38:39] offset:24024
	ds_write_b64 v1, v[36:37] offset:28392
	ds_write_b64 v1, v[34:35] offset:32760
	ds_write_b64 v1, v[86:87] offset:34816
	s_waitcnt lgkmcnt(0)
	s_barrier
	ds_read2_b64 v[32:35], v96 offset1:16
	ds_read2_b64 v[36:39], v96 offset0:32 offset1:48
	ds_read2_b64 v[40:43], v96 offset0:64 offset1:80
	ds_read2_b64 v[44:47], v96 offset0:128 offset1:144
	ds_read2_b64 v[48:51], v96 offset0:96 offset1:112
	ds_read2_b64 v[52:55], v96 offset0:192 offset1:208
	ds_read2_b64 v[56:59], v96 offset0:160 offset1:176
	ds_read2_b64 v[60:63], v96 offset0:224 offset1:240
	s_waitcnt lgkmcnt(4)
	v_pk_add_f32 v[64:65], v[32:33], v[44:45]
	v_pk_add_f32 v[32:33], v[32:33], v[44:45] neg_lo:[0,1] neg_hi:[0,1]
	s_waitcnt lgkmcnt(2)
	v_pk_add_f32 v[44:45], v[40:41], v[52:53]
	v_pk_add_f32 v[40:41], v[40:41], v[52:53] neg_lo:[0,1] neg_hi:[0,1]
	v_pk_add_f32 v[52:53], v[64:65], v[44:45]
	v_pk_add_f32 v[44:45], v[64:65], v[44:45] neg_lo:[0,1] neg_hi:[0,1]
	v_pk_add_f32 v[64:65], v[32:33], v[40:41] op_sel:[0,1] op_sel_hi:[1,0] neg_hi:[0,1]
	v_pk_add_f32 v[32:33], v[32:33], v[40:41] op_sel:[0,1] op_sel_hi:[1,0] neg_lo:[0,1]
	v_pk_add_f32 v[40:41], v[34:35], v[46:47]
	v_pk_add_f32 v[34:35], v[34:35], v[46:47] neg_lo:[0,1] neg_hi:[0,1]
	v_pk_add_f32 v[46:47], v[42:43], v[54:55]
	v_pk_add_f32 v[42:43], v[42:43], v[54:55] neg_lo:[0,1] neg_hi:[0,1]
	v_pk_add_f32 v[54:55], v[40:41], v[46:47]
	v_pk_add_f32 v[40:41], v[40:41], v[46:47] neg_lo:[0,1] neg_hi:[0,1]
	v_pk_add_f32 v[46:47], v[34:35], v[42:43] op_sel:[0,1] op_sel_hi:[1,0] neg_hi:[0,1]
	v_pk_add_f32 v[34:35], v[34:35], v[42:43] op_sel:[0,1] op_sel_hi:[1,0] neg_lo:[0,1]
	s_waitcnt lgkmcnt(1)
	v_pk_add_f32 v[42:43], v[36:37], v[56:57]
	v_pk_add_f32 v[36:37], v[36:37], v[56:57] neg_lo:[0,1] neg_hi:[0,1]
	s_waitcnt lgkmcnt(0)
	v_pk_add_f32 v[56:57], v[48:49], v[60:61]
	v_pk_add_f32 v[48:49], v[48:49], v[60:61] neg_lo:[0,1] neg_hi:[0,1]
	v_pk_add_f32 v[60:61], v[42:43], v[56:57]
	v_pk_add_f32 v[42:43], v[42:43], v[56:57] neg_lo:[0,1] neg_hi:[0,1]
	v_pk_add_f32 v[56:57], v[36:37], v[48:49] op_sel:[0,1] op_sel_hi:[1,0] neg_hi:[0,1]
	v_pk_add_f32 v[36:37], v[36:37], v[48:49] op_sel:[0,1] op_sel_hi:[1,0] neg_lo:[0,1]
	v_pk_add_f32 v[48:49], v[38:39], v[58:59]
	v_pk_add_f32 v[38:39], v[38:39], v[58:59] neg_lo:[0,1] neg_hi:[0,1]
	v_pk_add_f32 v[58:59], v[50:51], v[62:63]
	v_pk_add_f32 v[50:51], v[50:51], v[62:63] neg_lo:[0,1] neg_hi:[0,1]
	v_pk_add_f32 v[62:63], v[48:49], v[58:59]
	v_pk_add_f32 v[48:49], v[48:49], v[58:59] neg_lo:[0,1] neg_hi:[0,1]
	v_pk_add_f32 v[58:59], v[38:39], v[50:51] op_sel:[0,1] op_sel_hi:[1,0] neg_hi:[0,1]
	v_pk_add_f32 v[38:39], v[38:39], v[50:51] op_sel:[0,1] op_sel_hi:[1,0] neg_lo:[0,1]
	v_pk_mul_f32 v[50:51], v[46:47], s[6:7] op_sel:[0,0] op_sel_hi:[0,1]
	v_pk_fma_f32 v[50:51], v[46:47], s[6:7], v[50:51] op_sel:[1,1,0] op_sel_hi:[1,0,1] neg_lo:[0,1,0]
	v_pk_mul_f32 v[46:47], v[34:35], s[10:11] op_sel:[0,0] op_sel_hi:[0,1]
	v_pk_fma_f32 v[46:47], v[34:35], s[10:11], v[46:47] op_sel:[1,1,0] op_sel_hi:[1,0,1] neg_lo:[0,1,0]
	v_pk_add_f32 v[34:35], v[56:57], v[56:57] op_sel:[0,1] op_sel_hi:[1,0] neg_hi:[0,1]
	v_pk_add_f32 v[40:41], v[40:41], v[40:41] op_sel:[0,1] op_sel_hi:[1,0] neg_hi:[0,1]
	s_nop 0
	v_pk_mul_f32 v[56:57], v[58:59], s[10:11] op_sel:[0,0] op_sel_hi:[0,1]
	v_pk_fma_f32 v[56:57], v[58:59], s[10:11], v[56:57] op_sel:[1,1,0] op_sel_hi:[1,0,1] neg_lo:[0,1,0]
	v_pk_mul_f32 v[58:59], v[38:39], s[14:15] op_sel:[0,0] op_sel_hi:[0,1]
	v_pk_fma_f32 v[58:59], v[38:39], s[14:15], v[58:59] op_sel:[1,1,0] op_sel_hi:[1,0,1] neg_lo:[0,1,0]
	v_pk_add_f32 v[38:39], v[52:53], v[60:61]
	v_pk_mul_f32 v[34:35], v[34:35], s[8:9]
	v_pk_add_f32 v[52:53], v[52:53], v[60:61] neg_lo:[0,1] neg_hi:[0,1]
	v_pk_add_f32 v[60:61], v[54:55], v[62:63]
	v_pk_add_f32 v[54:55], v[54:55], v[62:63] neg_lo:[0,1] neg_hi:[0,1]
	v_pk_add_f32 v[36:37], v[36:37], v[36:37] op_sel:[0,1] op_sel_hi:[1,0] neg_lo:[0,1]
	v_pk_add_f32 v[48:49], v[48:49], v[48:49] op_sel:[0,1] op_sel_hi:[1,0] neg_lo:[0,1]
	v_pk_add_f32 v[62:63], v[38:39], v[60:61]
	v_pk_add_f32 v[60:61], v[38:39], v[60:61] neg_lo:[0,1] neg_hi:[0,1]
	v_pk_add_f32 v[66:67], v[52:53], v[54:55] op_sel:[0,1] op_sel_hi:[1,0] neg_hi:[0,1]
	v_pk_add_f32 v[52:53], v[52:53], v[54:55] op_sel:[0,1] op_sel_hi:[1,0] neg_lo:[0,1]
	v_pk_add_f32 v[38:39], v[64:65], v[34:35]
	v_pk_add_f32 v[34:35], v[64:65], v[34:35] neg_lo:[0,1] neg_hi:[0,1]
	v_pk_add_f32 v[54:55], v[50:51], v[56:57]
	v_pk_add_f32 v[50:51], v[50:51], v[56:57] neg_lo:[0,1] neg_hi:[0,1]
	v_pk_mul_f32 v[40:41], v[40:41], s[8:9]
	v_pk_mul_f32 v[36:37], v[36:37], s[12:13]
	v_pk_mul_f32 v[48:49], v[48:49], s[12:13]
	v_pk_add_f32 v[56:57], v[38:39], v[54:55]
	v_pk_add_f32 v[54:55], v[38:39], v[54:55] neg_lo:[0,1] neg_hi:[0,1]
	v_pk_add_f32 v[64:65], v[34:35], v[50:51] op_sel:[0,1] op_sel_hi:[1,0] neg_hi:[0,1]
	v_pk_add_f32 v[50:51], v[34:35], v[50:51] op_sel:[0,1] op_sel_hi:[1,0] neg_lo:[0,1]
	v_pk_add_f32 v[34:35], v[44:45], v[42:43] op_sel:[0,1] op_sel_hi:[1,0] neg_hi:[0,1]
	v_pk_add_f32 v[38:39], v[44:45], v[42:43] op_sel:[0,1] op_sel_hi:[1,0] neg_lo:[0,1]
	v_pk_add_f32 v[42:43], v[40:41], v[48:49]
	v_pk_add_f32 v[40:41], v[40:41], v[48:49] neg_lo:[0,1] neg_hi:[0,1]
	v_pk_add_f32 v[44:45], v[42:43], v[34:35]
	v_pk_add_f32 v[42:43], v[34:35], v[42:43] neg_lo:[0,1] neg_hi:[0,1]
	v_pk_add_f32 v[34:35], v[32:33], v[36:37]
	v_pk_add_f32 v[36:37], v[32:33], v[36:37] neg_lo:[0,1] neg_hi:[0,1]
	v_pk_add_f32 v[32:33], v[46:47], v[58:59]
	v_pk_add_f32 v[48:49], v[38:39], v[40:41] op_sel:[0,1] op_sel_hi:[1,0] neg_hi:[0,1]
	v_pk_add_f32 v[40:41], v[38:39], v[40:41] op_sel:[0,1] op_sel_hi:[1,0] neg_lo:[0,1]
	v_pk_add_f32 v[38:39], v[46:47], v[58:59] neg_lo:[0,1] neg_hi:[0,1]
	v_pk_add_f32 v[46:47], v[34:35], v[32:33]
	v_pk_add_f32 v[58:59], v[34:35], v[32:33] neg_lo:[0,1] neg_hi:[0,1]
	v_pk_add_f32 v[68:69], v[36:37], v[38:39] op_sel:[0,1] op_sel_hi:[1,0] neg_hi:[0,1]
	v_pk_add_f32 v[86:87], v[36:37], v[38:39] op_sel:[0,1] op_sel_hi:[1,0] neg_lo:[0,1]
	s_nop 0
	v_ashrrev_i32_e32 v32, 4, v88
	v_lshlrev_b32_e32 v90, 3, v32
	v_add_u32_e32 v91, 0x8800, v90
	v_and_b32_e32 v36, 15, v88
	ds_read2_b64 v[32:35], v91 offset0:16 offset1:32
	v_mad_u32_u24 v92, v36, s5, v90
	ds_read2_b64 v[36:39], v91 offset0:48 offset1:64
	s_waitcnt lgkmcnt(1)
	v_pk_mul_f32 v[88:89], v[56:57], v[32:33] op_sel:[0,0] op_sel_hi:[0,1]
	v_pk_fma_f32 v[88:89], v[56:57], v[32:33], v[88:89] op_sel:[1,1,0] op_sel_hi:[1,0,1] neg_lo:[0,1,0]
	v_pk_mul_f32 v[56:57], v[44:45], v[34:35] op_sel:[0,0] op_sel_hi:[0,1]
	v_pk_fma_f32 v[56:57], v[44:45], v[34:35], v[56:57] op_sel:[1,1,0] op_sel_hi:[1,0,1] neg_lo:[0,1,0]
	s_waitcnt lgkmcnt(0)
	v_pk_mul_f32 v[44:45], v[46:47], v[36:37] op_sel:[0,0] op_sel_hi:[0,1]
	v_pk_fma_f32 v[44:45], v[46:47], v[36:37], v[44:45] op_sel:[1,1,0] op_sel_hi:[1,0,1] neg_lo:[0,1,0]
	ds_write2_b64 v92, v[56:57], v[44:45] offset0:32 offset1:48
	v_pk_mul_f32 v[44:45], v[66:67], v[38:39] op_sel:[0,0] op_sel_hi:[0,1]
	v_pk_fma_f32 v[44:45], v[66:67], v[38:39], v[44:45] op_sel:[1,1,0] op_sel_hi:[1,0,1] neg_lo:[0,1,0]
	ds_read2_b64 v[32:35], v91 offset0:80 offset1:96
	s_waitcnt lgkmcnt(0)
	v_pk_mul_f32 v[46:47], v[64:65], v[32:33] op_sel:[0,0] op_sel_hi:[0,1]
	v_pk_fma_f32 v[46:47], v[64:65], v[32:33], v[46:47] op_sel:[1,1,0] op_sel_hi:[1,0,1] neg_lo:[0,1,0]
	ds_write2_b64 v92, v[44:45], v[46:47] offset0:64 offset1:80
	v_pk_mul_f32 v[44:45], v[48:49], v[34:35] op_sel:[0,0] op_sel_hi:[0,1]
	v_pk_fma_f32 v[44:45], v[48:49], v[34:35], v[44:45] op_sel:[1,1,0] op_sel_hi:[1,0,1] neg_lo:[0,1,0]
	ds_read2_b64 v[36:39], v91 offset0:112 offset1:128
	ds_read2_b64 v[32:35], v91 offset0:144 offset1:160
	s_waitcnt lgkmcnt(1)
	v_pk_mul_f32 v[46:47], v[68:69], v[36:37] op_sel:[0,0] op_sel_hi:[0,1]
	v_pk_fma_f32 v[46:47], v[68:69], v[36:37], v[46:47] op_sel:[1,1,0] op_sel_hi:[1,0,1] neg_lo:[0,1,0]
	ds_write2_b64 v92, v[44:45], v[46:47] offset0:96 offset1:112
	v_pk_mul_f32 v[44:45], v[60:61], v[38:39] op_sel:[0,0] op_sel_hi:[0,1]
	v_pk_fma_f32 v[44:45], v[60:61], v[38:39], v[44:45] op_sel:[1,1,0] op_sel_hi:[1,0,1] neg_lo:[0,1,0]
	ds_read2_b64 v[36:39], v91 offset0:176 offset1:192
	s_waitcnt lgkmcnt(2)
	v_pk_mul_f32 v[46:47], v[54:55], v[32:33] op_sel:[0,0] op_sel_hi:[0,1]
	v_pk_fma_f32 v[46:47], v[54:55], v[32:33], v[46:47] op_sel:[1,1,0] op_sel_hi:[1,0,1] neg_lo:[0,1,0]
	ds_write2_b64 v92, v[44:45], v[46:47] offset0:128 offset1:144
	v_pk_mul_f32 v[44:45], v[42:43], v[34:35] op_sel:[0,0] op_sel_hi:[0,1]
	v_pk_fma_f32 v[44:45], v[42:43], v[34:35], v[44:45] op_sel:[1,1,0] op_sel_hi:[1,0,1] neg_lo:[0,1,0]
	ds_read2_b64 v[32:35], v91 offset0:208 offset1:224
	s_waitcnt lgkmcnt(2)
	v_pk_mul_f32 v[42:43], v[58:59], v[36:37] op_sel:[0,0] op_sel_hi:[0,1]
	v_pk_fma_f32 v[42:43], v[58:59], v[36:37], v[42:43] op_sel:[1,1,0] op_sel_hi:[1,0,1] neg_lo:[0,1,0]
	ds_write2_b64 v92, v[44:45], v[42:43] offset0:160 offset1:176
	v_pk_mul_f32 v[42:43], v[52:53], v[38:39] op_sel:[0,0] op_sel_hi:[0,1]
	v_pk_fma_f32 v[42:43], v[52:53], v[38:39], v[42:43] op_sel:[1,1,0] op_sel_hi:[1,0,1] neg_lo:[0,1,0]
	s_waitcnt lgkmcnt(1)
	v_pk_mul_f32 v[38:39], v[50:51], v[32:33] op_sel:[0,0] op_sel_hi:[0,1]
	v_pk_fma_f32 v[38:39], v[50:51], v[32:33], v[38:39] op_sel:[1,1,0] op_sel_hi:[1,0,1] neg_lo:[0,1,0]
	v_pk_mul_f32 v[32:33], v[40:41], v[34:35] op_sel:[0,0] op_sel_hi:[0,1]
	v_pk_fma_f32 v[32:33], v[40:41], v[34:35], v[32:33] op_sel:[1,1,0] op_sel_hi:[1,0,1] neg_lo:[0,1,0]
	ds_read_b64 v[36:37], v90 offset:36736
	s_waitcnt lgkmcnt(0)
	v_pk_mul_f32 v[34:35], v[86:87], v[36:37] op_sel:[0,0] op_sel_hi:[0,1]
	v_pk_fma_f32 v[34:35], v[86:87], v[36:37], v[34:35] op_sel:[1,1,0] op_sel_hi:[1,0,1] neg_lo:[0,1,0]
	ds_write2_b64 v92, v[32:33], v[34:35] offset0:224 offset1:240
	v_mov_b32_e32 v32, v0
	ds_write2_b64 v92, v[62:63], v[88:89] offset1:16
	ds_write2_b64 v92, v[42:43], v[38:39] offset0:192 offset1:208
	s_waitcnt lgkmcnt(0)
	s_barrier
	s_nop 0
	v_and_b32_e32 v33, 15, v32
	v_and_b32_e32 v32, 0x1ffffff0, v32
	v_lshlrev_b32_e32 v32, 3, v32
	v_mad_u32_u24 v60, v33, s5, v32
	ds_read2_b64 v[32:35], v60 offset1:1
	ds_read2_b64 v[36:39], v60 offset0:2 offset1:3
	ds_read2_b64 v[40:43], v60 offset0:8 offset1:9
	ds_read2_b64 v[44:47], v60 offset0:4 offset1:5
	ds_read2_b64 v[48:51], v60 offset0:6 offset1:7
	ds_read2_b64 v[52:55], v60 offset0:12 offset1:13
	ds_read2_b64 v[56:59], v60 offset0:10 offset1:11
	ds_read2_b64 v[60:63], v60 offset0:14 offset1:15
	s_waitcnt lgkmcnt(5)
	v_pk_add_f32 v[64:65], v[32:33], v[40:41]
	v_pk_add_f32 v[32:33], v[32:33], v[40:41] neg_lo:[0,1] neg_hi:[0,1]
	s_waitcnt lgkmcnt(2)
	v_pk_add_f32 v[40:41], v[44:45], v[52:53]
	v_pk_add_f32 v[44:45], v[44:45], v[52:53] neg_lo:[0,1] neg_hi:[0,1]
	v_pk_add_f32 v[52:53], v[64:65], v[40:41]
	v_pk_add_f32 v[40:41], v[64:65], v[40:41] neg_lo:[0,1] neg_hi:[0,1]
	v_pk_add_f32 v[64:65], v[32:33], v[44:45] op_sel:[0,1] op_sel_hi:[1,0] neg_hi:[0,1]
	v_pk_add_f32 v[66:67], v[32:33], v[44:45] op_sel:[0,1] op_sel_hi:[1,0] neg_lo:[0,1]
	v_pk_add_f32 v[32:33], v[34:35], v[42:43]
	v_pk_add_f32 v[34:35], v[34:35], v[42:43] neg_lo:[0,1] neg_hi:[0,1]
	v_pk_add_f32 v[42:43], v[46:47], v[54:55]
	v_pk_add_f32 v[44:45], v[46:47], v[54:55] neg_lo:[0,1] neg_hi:[0,1]
	v_pk_add_f32 v[46:47], v[32:33], v[42:43]
	v_pk_add_f32 v[32:33], v[32:33], v[42:43] neg_lo:[0,1] neg_hi:[0,1]
	v_pk_add_f32 v[42:43], v[34:35], v[44:45] op_sel:[0,1] op_sel_hi:[1,0] neg_hi:[0,1]
	v_pk_add_f32 v[34:35], v[34:35], v[44:45] op_sel:[0,1] op_sel_hi:[1,0] neg_lo:[0,1]
	s_waitcnt lgkmcnt(1)
	v_pk_add_f32 v[44:45], v[36:37], v[56:57]
	s_waitcnt lgkmcnt(0)
	v_pk_add_f32 v[54:55], v[48:49], v[60:61]
	v_pk_add_f32 v[32:33], v[32:33], v[32:33] op_sel:[0,1] op_sel_hi:[1,0] neg_hi:[0,1]
	v_pk_add_f32 v[36:37], v[36:37], v[56:57] neg_lo:[0,1] neg_hi:[0,1]
	v_pk_add_f32 v[48:49], v[48:49], v[60:61] neg_lo:[0,1] neg_hi:[0,1]
	v_pk_add_f32 v[56:57], v[44:45], v[54:55]
	v_pk_add_f32 v[54:55], v[44:45], v[54:55] neg_lo:[0,1] neg_hi:[0,1]
	v_pk_add_f32 v[44:45], v[36:37], v[48:49] op_sel:[0,1] op_sel_hi:[1,0] neg_hi:[0,1]
	v_pk_mul_f32 v[68:69], v[32:33], s[8:9]
	v_pk_add_f32 v[36:37], v[36:37], v[48:49] op_sel:[0,1] op_sel_hi:[1,0] neg_lo:[0,1]
	v_pk_add_f32 v[48:49], v[38:39], v[58:59]
	v_pk_add_f32 v[32:33], v[44:45], v[44:45] op_sel:[0,1] op_sel_hi:[1,0] neg_hi:[0,1]
	v_pk_add_f32 v[38:39], v[38:39], v[58:59] neg_lo:[0,1] neg_hi:[0,1]
	v_pk_add_f32 v[58:59], v[50:51], v[62:63]
	v_pk_mul_f32 v[86:87], v[34:35], s[10:11] op_sel:[0,0] op_sel_hi:[0,1]
	v_pk_fma_f32 v[86:87], v[34:35], s[10:11], v[86:87] op_sel:[1,1,0] op_sel_hi:[1,0,1] neg_lo:[0,1,0]
	v_pk_mul_f32 v[34:35], v[32:33], s[8:9]
	v_pk_add_f32 v[32:33], v[36:37], v[36:37] op_sel:[0,1] op_sel_hi:[1,0] neg_lo:[0,1]
	v_pk_add_f32 v[50:51], v[50:51], v[62:63] neg_lo:[0,1] neg_hi:[0,1]
	v_pk_add_f32 v[60:61], v[48:49], v[58:59]
	v_pk_add_f32 v[48:49], v[48:49], v[58:59] neg_lo:[0,1] neg_hi:[0,1]
	v_pk_add_f32 v[58:59], v[38:39], v[50:51] op_sel:[0,1] op_sel_hi:[1,0] neg_hi:[0,1]
	v_pk_add_f32 v[38:39], v[38:39], v[50:51] op_sel:[0,1] op_sel_hi:[1,0] neg_lo:[0,1]
	v_pk_mul_f32 v[88:89], v[32:33], s[12:13]
	v_pk_add_f32 v[36:37], v[46:47], v[60:61]
	v_pk_add_f32 v[32:33], v[48:49], v[48:49] op_sel:[0,1] op_sel_hi:[1,0] neg_lo:[0,1]
	v_pk_mul_f32 v[44:45], v[58:59], s[10:11] op_sel:[0,0] op_sel_hi:[0,1]
	v_pk_fma_f32 v[44:45], v[58:59], s[10:11], v[44:45] op_sel:[1,1,0] op_sel_hi:[1,0,1] neg_lo:[0,1,0]
	v_pk_mul_f32 v[58:59], v[38:39], s[14:15] op_sel:[0,0] op_sel_hi:[0,1]
	v_pk_fma_f32 v[58:59], v[38:39], s[14:15], v[58:59] op_sel:[1,1,0] op_sel_hi:[1,0,1] neg_lo:[0,1,0]
	v_pk_add_f32 v[38:39], v[52:53], v[56:57] neg_lo:[0,1] neg_hi:[0,1]
	v_pk_mul_f32 v[48:49], v[32:33], s[12:13]
	v_pk_add_f32 v[32:33], v[52:53], v[56:57]
	v_pk_add_f32 v[46:47], v[46:47], v[60:61] neg_lo:[0,1] neg_hi:[0,1]
	v_pk_mul_f32 v[62:63], v[42:43], s[6:7] op_sel:[0,0] op_sel_hi:[0,1]
	v_pk_fma_f32 v[62:63], v[42:43], s[6:7], v[62:63] op_sel:[1,1,0] op_sel_hi:[1,0,1] neg_lo:[0,1,0]
	v_pk_add_f32 v[50:51], v[32:33], v[36:37]
	v_pk_add_f32 v[36:37], v[32:33], v[36:37] neg_lo:[0,1] neg_hi:[0,1]
	v_pk_add_f32 v[42:43], v[38:39], v[46:47] op_sel:[0,1] op_sel_hi:[1,0] neg_hi:[0,1]
	v_pk_add_f32 v[32:33], v[38:39], v[46:47] op_sel:[0,1] op_sel_hi:[1,0] neg_lo:[0,1]
	v_pk_add_f32 v[38:39], v[64:65], v[34:35]
	v_pk_add_f32 v[34:35], v[64:65], v[34:35] neg_lo:[0,1] neg_hi:[0,1]
	v_pk_add_f32 v[46:47], v[62:63], v[44:45]
	v_pk_add_f32 v[56:57], v[62:63], v[44:45] neg_lo:[0,1] neg_hi:[0,1]
	v_pk_add_f32 v[52:53], v[38:39], v[46:47]
	v_pk_add_f32 v[38:39], v[38:39], v[46:47] neg_lo:[0,1] neg_hi:[0,1]
	v_pk_add_f32 v[44:45], v[34:35], v[56:57] op_sel:[0,1] op_sel_hi:[1,0] neg_hi:[0,1]
	v_pk_add_f32 v[34:35], v[34:35], v[56:57] op_sel:[0,1] op_sel_hi:[1,0] neg_lo:[0,1]
	v_pk_add_f32 v[46:47], v[40:41], v[54:55] op_sel:[0,1] op_sel_hi:[1,0] neg_hi:[0,1]
	v_pk_add_f32 v[56:57], v[40:41], v[54:55] op_sel:[0,1] op_sel_hi:[1,0] neg_lo:[0,1]
	v_pk_add_f32 v[40:41], v[68:69], v[48:49]
	v_pk_add_f32 v[60:61], v[68:69], v[48:49] neg_lo:[0,1] neg_hi:[0,1]
	v_pk_add_f32 v[54:55], v[40:41], v[46:47]
	v_pk_add_f32 v[40:41], v[46:47], v[40:41] neg_lo:[0,1] neg_hi:[0,1]
	v_pk_add_f32 v[46:47], v[66:67], v[88:89]
	v_pk_add_f32 v[62:63], v[86:87], v[58:59]
	v_pk_add_f32 v[58:59], v[86:87], v[58:59] neg_lo:[0,1] neg_hi:[0,1]
	v_pk_add_f32 v[48:49], v[56:57], v[60:61] op_sel:[0,1] op_sel_hi:[1,0] neg_hi:[0,1]
	v_pk_add_f32 v[64:65], v[56:57], v[60:61] op_sel:[0,1] op_sel_hi:[1,0] neg_lo:[0,1]
	v_pk_add_f32 v[60:61], v[66:67], v[88:89] neg_lo:[0,1] neg_hi:[0,1]
	v_pk_add_f32 v[56:57], v[46:47], v[62:63]
	v_pk_add_f32 v[68:69], v[46:47], v[62:63] neg_lo:[0,1] neg_hi:[0,1]
	v_pk_add_f32 v[46:47], v[60:61], v[58:59] op_sel:[0,1] op_sel_hi:[1,0] neg_hi:[0,1]
	v_pk_add_f32 v[66:67], v[60:61], v[58:59] op_sel:[0,1] op_sel_hi:[1,0] neg_lo:[0,1]
	v_mov_b32_e32 v58, v0
	s_nop 0
	v_and_b32_e32 v59, -16, v58
	v_and_b32_e32 v60, 15, v58
	v_lshlrev_b32_e32 v61, 3, v59
	v_mad_u32_u24 v61, v60, s5, v61
	v_cmp_ne_u32_e32 vcc, 0, v60
	ds_write2_b64 v61, v[50:51], v[52:53] offset1:1
	ds_write2_b64 v61, v[54:55], v[56:57] offset0:2 offset1:3
	ds_write2_b64 v61, v[42:43], v[44:45] offset0:4 offset1:5
	ds_write2_b64 v61, v[48:49], v[46:47] offset0:6 offset1:7
	ds_write2_b64 v61, v[36:37], v[38:39] offset0:8 offset1:9
	ds_write2_b64 v61, v[40:41], v[68:69] offset0:10 offset1:11
	ds_write2_b64 v61, v[32:33], v[34:35] offset0:12 offset1:13
	ds_write2_b64 v61, v[64:65], v[66:67] offset0:14 offset1:15
	s_waitcnt lgkmcnt(0)
	s_barrier
	s_and_saveexec_b64 s[6:7], vcc
	s_xor_b64 s[6:7], exec, s[6:7]
	v_sub_u32_e32 v60, 16, v60
	v_mul_u32_u24_e32 v60, 0x111, v60
	v_sub_u32_e32 v59, v60, v59
	v_add_u32_e32 v61, 0xf0, v59
	s_andn2_saveexec_b64 s[6:7], s[6:7]
	v_sub_u32_e32 v59, 0x100, v58
	v_cmp_lt_u32_e32 vcc, 15, v58
	s_nop 1
	v_cndmask_b32_e32 v61, 1, v59, vcc
	s_or_b64 exec, exec, s[6:7]
	v_mov_b32_e32 v59, 0
	v_lshlrev_b32_e32 v92, 3, v61
	ds_read_b64 v[90:91], v59
	ds_read2_b64 v[60:63], v92 offset0:14 offset1:15
	ds_read2_b64 v[86:89], v92 offset0:12 offset1:13
	v_cmp_eq_u32_e32 vcc, 0, v58
	v_cvt_f32_fp8_sdwa v93, v74 src0_sel:BYTE_3
	v_cvt_f32_fp8_sdwa v94, v72 src0_sel:BYTE_1
	s_waitcnt lgkmcnt(1)
	v_cndmask_b32_e32 v59, v63, v91, vcc
	v_cndmask_b32_e32 v58, v62, v90, vcc
	v_pk_add_f32 v[90:91], v[50:51], v[58:59] neg_hi:[0,1]
	v_pk_add_f32 v[50:51], v[50:51], v[58:59] neg_lo:[0,1]
	v_cvt_f32_fp8_sdwa v95, v72 src0_sel:BYTE_3
	v_pk_mul_f32 v[62:63], v[90:91], v[50:51] op_sel:[0,0] op_sel_hi:[0,1]
	v_pk_fma_f32 v[62:63], v[90:91], v[50:51], v[62:63] op_sel:[1,1,0] op_sel_hi:[1,0,1] neg_hi:[0,1,0]
	v_pk_add_f32 v[50:51], v[52:53], v[60:61] neg_hi:[0,1]
	v_pk_add_f32 v[52:53], v[52:53], v[60:61] neg_lo:[0,1]
	v_cvt_f32_fp8_sdwa v72, v71 src0_sel:BYTE_1
	v_pk_mul_f32 v[60:61], v[50:51], v[52:53] op_sel:[0,0] op_sel_hi:[0,1]
	v_pk_fma_f32 v[60:61], v[50:51], v[52:53], v[60:61] op_sel:[1,1,0] op_sel_hi:[1,0,1] neg_hi:[0,1,0]
	s_waitcnt lgkmcnt(0)
	v_pk_add_f32 v[50:51], v[54:55], v[88:89] neg_hi:[0,1]
	v_pk_add_f32 v[52:53], v[54:55], v[88:89] neg_lo:[0,1]
	v_pk_add_f32 v[54:55], v[56:57], v[86:87] neg_hi:[0,1]
	v_pk_add_f32 v[86:87], v[56:57], v[86:87] neg_lo:[0,1]
	v_cvt_f32_fp8_sdwa v98, v70 src0_sel:BYTE_1
	v_pk_mul_f32 v[58:59], v[50:51], v[52:53] op_sel:[0,0] op_sel_hi:[0,1]
	v_pk_fma_f32 v[58:59], v[50:51], v[52:53], v[58:59] op_sel:[1,1,0] op_sel_hi:[1,0,1] neg_hi:[0,1,0]
	ds_read2_b64 v[50:53], v92 offset0:10 offset1:11
	v_pk_mul_f32 v[56:57], v[54:55], v[86:87] op_sel:[0,0] op_sel_hi:[0,1]
	v_pk_fma_f32 v[56:57], v[54:55], v[86:87], v[56:57] op_sel:[1,1,0] op_sel_hi:[1,0,1] neg_hi:[0,1,0]
	ds_read2_b64 v[86:89], v92 offset0:8 offset1:9
	s_waitcnt lgkmcnt(1)
	v_pk_add_f32 v[90:91], v[42:43], v[52:53] neg_hi:[0,1]
	v_pk_add_f32 v[42:43], v[42:43], v[52:53] neg_lo:[0,1]
	v_cvt_f32_fp8_sdwa v99, v70 src0_sel:BYTE_3
	v_pk_mul_f32 v[54:55], v[90:91], v[42:43] op_sel:[0,0] op_sel_hi:[0,1]
	v_pk_fma_f32 v[54:55], v[90:91], v[42:43], v[54:55] op_sel:[1,1,0] op_sel_hi:[1,0,1] neg_hi:[0,1,0]
	v_pk_add_f32 v[42:43], v[44:45], v[50:51] neg_hi:[0,1]
	v_pk_add_f32 v[44:45], v[44:45], v[50:51] neg_lo:[0,1]
	s_mov_b32 s6, 0x3f6c835e
	v_pk_mul_f32 v[52:53], v[42:43], v[44:45] op_sel:[0,0] op_sel_hi:[0,1]
	v_pk_fma_f32 v[52:53], v[42:43], v[44:45], v[52:53] op_sel:[1,1,0] op_sel_hi:[1,0,1] neg_hi:[0,1,0]
	s_waitcnt lgkmcnt(0)
	v_pk_add_f32 v[42:43], v[48:49], v[88:89] neg_hi:[0,1]
	v_pk_add_f32 v[44:45], v[48:49], v[88:89] neg_lo:[0,1]
	v_pk_add_f32 v[88:89], v[46:47], v[86:87] neg_hi:[0,1]
	v_pk_add_f32 v[46:47], v[46:47], v[86:87] neg_lo:[0,1]
	s_mov_b32 s7, 0xbec3ef15
	v_pk_mul_f32 v[50:51], v[42:43], v[44:45] op_sel:[0,0] op_sel_hi:[0,1]
	v_pk_fma_f32 v[50:51], v[42:43], v[44:45], v[50:51] op_sel:[1,1,0] op_sel_hi:[1,0,1] neg_hi:[0,1,0]
	ds_read2_b64 v[42:45], v92 offset0:6 offset1:7
	v_pk_mul_f32 v[48:49], v[88:89], v[46:47] op_sel:[0,0] op_sel_hi:[0,1]
	v_pk_fma_f32 v[48:49], v[88:89], v[46:47], v[48:49] op_sel:[1,1,0] op_sel_hi:[1,0,1] neg_hi:[0,1,0]
	ds_read2_b64 v[86:89], v92 offset0:4 offset1:5
	s_waitcnt lgkmcnt(1)
	v_pk_add_f32 v[90:91], v[36:37], v[44:45] neg_hi:[0,1]
	v_pk_add_f32 v[36:37], v[36:37], v[44:45] neg_lo:[0,1]
	s_mov_b32 s9, s8
	v_pk_mul_f32 v[46:47], v[90:91], v[36:37] op_sel:[0,0] op_sel_hi:[0,1]
	v_pk_fma_f32 v[46:47], v[90:91], v[36:37], v[46:47] op_sel:[1,1,0] op_sel_hi:[1,0,1] neg_hi:[0,1,0]
	v_pk_add_f32 v[36:37], v[38:39], v[42:43] neg_hi:[0,1]
	v_pk_add_f32 v[38:39], v[38:39], v[42:43] neg_lo:[0,1]
	v_cvt_f32_fp8_sdwa v90, v76 src0_sel:BYTE_1
	v_pk_mul_f32 v[44:45], v[36:37], v[38:39] op_sel:[0,0] op_sel_hi:[0,1]
	v_pk_fma_f32 v[44:45], v[36:37], v[38:39], v[44:45] op_sel:[1,1,0] op_sel_hi:[1,0,1] neg_hi:[0,1,0]
	s_waitcnt lgkmcnt(0)
	v_pk_add_f32 v[36:37], v[40:41], v[88:89] neg_hi:[0,1]
	v_pk_add_f32 v[38:39], v[40:41], v[88:89] neg_lo:[0,1]
	v_pk_add_f32 v[88:89], v[68:69], v[86:87] neg_hi:[0,1]
	v_pk_add_f32 v[68:69], v[68:69], v[86:87] neg_lo:[0,1]
	v_cvt_f32_fp8_sdwa v91, v76 src0_sel:BYTE_3
	v_pk_mul_f32 v[42:43], v[36:37], v[38:39] op_sel:[0,0] op_sel_hi:[0,1]
	v_pk_fma_f32 v[42:43], v[36:37], v[38:39], v[42:43] op_sel:[1,1,0] op_sel_hi:[1,0,1] neg_hi:[0,1,0]
	ds_read2_b64 v[36:39], v92 offset0:2 offset1:3
	v_pk_mul_f32 v[40:41], v[88:89], v[68:69] op_sel:[0,0] op_sel_hi:[0,1]
	v_pk_fma_f32 v[40:41], v[88:89], v[68:69], v[40:41] op_sel:[1,1,0] op_sel_hi:[1,0,1] neg_hi:[0,1,0]
	ds_read2_b64 v[86:89], v92 offset1:1
	s_waitcnt lgkmcnt(1)
	v_pk_add_f32 v[68:69], v[32:33], v[38:39] neg_hi:[0,1]
	v_pk_add_f32 v[32:33], v[32:33], v[38:39] neg_lo:[0,1]
	v_cvt_f32_fp8_sdwa v76, v75 src0_sel:BYTE_1
	v_pk_mul_f32 v[38:39], v[68:69], v[32:33] op_sel:[0,0] op_sel_hi:[0,1]
	v_pk_fma_f32 v[38:39], v[68:69], v[32:33], v[38:39] op_sel:[1,1,0] op_sel_hi:[1,0,1] neg_hi:[0,1,0]
	v_pk_add_f32 v[32:33], v[34:35], v[36:37] neg_hi:[0,1]
	v_pk_add_f32 v[34:35], v[34:35], v[36:37] neg_lo:[0,1]
	v_cvt_f32_fp8_sdwa v68, v83 src0_sel:BYTE_1
	v_pk_mul_f32 v[36:37], v[32:33], v[34:35] op_sel:[0,0] op_sel_hi:[0,1]
	v_pk_fma_f32 v[36:37], v[32:33], v[34:35], v[36:37] op_sel:[1,1,0] op_sel_hi:[1,0,1] neg_hi:[0,1,0]
	s_waitcnt lgkmcnt(0)
	v_pk_add_f32 v[32:33], v[64:65], v[88:89] neg_hi:[0,1]
	v_pk_add_f32 v[64:65], v[64:65], v[88:89] neg_lo:[0,1]
	v_cvt_f32_fp8_sdwa v69, v83 src0_sel:BYTE_3
	v_pk_mul_f32 v[34:35], v[32:33], v[64:65] op_sel:[0,0] op_sel_hi:[0,1]
	v_pk_fma_f32 v[34:35], v[32:33], v[64:65], v[34:35] op_sel:[1,1,0] op_sel_hi:[1,0,1] neg_hi:[0,1,0]
	v_pk_add_f32 v[64:65], v[66:67], v[86:87] neg_hi:[0,1]
	v_pk_add_f32 v[66:67], v[66:67], v[86:87] neg_lo:[0,1]
	v_cvt_f32_fp8_sdwa v83, v81 src0_sel:BYTE_3
	v_pk_mul_f32 v[32:33], v[64:65], v[66:67] op_sel:[0,0] op_sel_hi:[0,1]
	v_pk_fma_f32 v[32:33], v[64:65], v[66:67], v[32:33] op_sel:[1,1,0] op_sel_hi:[1,0,1] neg_hi:[0,1,0]
	v_cvt_f32_fp8_sdwa v64, v85 src0_sel:BYTE_1
	v_cvt_f32_fp8_sdwa v65, v85 src0_sel:BYTE_3
	v_cvt_f32_fp8_sdwa v66, v84 src0_sel:BYTE_1
	v_cvt_f32_fp8_sdwa v67, v84 src0_sel:BYTE_3
	v_cvt_f32_fp8_sdwa v84, v82 src0_sel:BYTE_1
	v_cvt_f32_fp8_sdwa v85, v82 src0_sel:BYTE_3
	v_cvt_f32_fp8_sdwa v82, v81 src0_sel:BYTE_1
	v_cvt_f32_fp8_sdwa v86, v80 src0_sel:BYTE_1
	v_cvt_f32_fp8_sdwa v87, v80 src0_sel:BYTE_3
	v_cvt_f32_fp8_sdwa v80, v79 src0_sel:BYTE_1
	v_cvt_f32_fp8_sdwa v81, v79 src0_sel:BYTE_3
	v_cvt_f32_fp8_sdwa v88, v78 src0_sel:BYTE_1
	v_cvt_f32_fp8_sdwa v89, v78 src0_sel:BYTE_3
	v_cvt_f32_fp8_sdwa v78, v77 src0_sel:BYTE_1
	v_cvt_f32_fp8_sdwa v79, v77 src0_sel:BYTE_3
	v_cvt_f32_fp8_sdwa v77, v75 src0_sel:BYTE_3
	v_cvt_f32_fp8_sdwa v92, v74 src0_sel:BYTE_1
	v_cvt_f32_fp8_sdwa v74, v73 src0_sel:BYTE_1
	v_cvt_f32_fp8_sdwa v75, v73 src0_sel:BYTE_3
	v_cvt_f32_fp8_sdwa v73, v71 src0_sel:BYTE_3
	v_pk_add_f32 v[70:71], v[64:65], v[78:79]
	v_pk_add_f32 v[64:65], v[64:65], v[78:79] neg_lo:[0,1] neg_hi:[0,1]
	v_pk_add_f32 v[78:79], v[82:83], v[74:75]
	v_pk_add_f32 v[74:75], v[82:83], v[74:75] neg_lo:[0,1] neg_hi:[0,1]
	v_pk_add_f32 v[82:83], v[70:71], v[78:79]
	v_pk_add_f32 v[70:71], v[70:71], v[78:79] neg_lo:[0,1] neg_hi:[0,1]
	v_pk_add_f32 v[78:79], v[64:65], v[74:75] op_sel:[0,1] op_sel_hi:[1,0] neg_hi:[0,1]
	v_pk_add_f32 v[64:65], v[64:65], v[74:75] op_sel:[0,1] op_sel_hi:[1,0] neg_lo:[0,1]
	v_pk_add_f32 v[74:75], v[66:67], v[90:91]
	v_pk_add_f32 v[66:67], v[66:67], v[90:91] neg_lo:[0,1] neg_hi:[0,1]
	v_pk_add_f32 v[90:91], v[86:87], v[94:95]
	v_pk_add_f32 v[86:87], v[86:87], v[94:95] neg_lo:[0,1] neg_hi:[0,1]
	v_pk_add_f32 v[94:95], v[74:75], v[90:91]
	v_pk_add_f32 v[74:75], v[74:75], v[90:91] neg_lo:[0,1] neg_hi:[0,1]
	v_pk_add_f32 v[90:91], v[66:67], v[86:87] op_sel:[0,1] op_sel_hi:[1,0] neg_hi:[0,1]
	v_pk_add_f32 v[66:67], v[66:67], v[86:87] op_sel:[0,1] op_sel_hi:[1,0] neg_lo:[0,1]
	v_pk_add_f32 v[86:87], v[68:69], v[76:77]
	v_pk_add_f32 v[68:69], v[68:69], v[76:77] neg_lo:[0,1] neg_hi:[0,1]
	v_pk_add_f32 v[76:77], v[80:81], v[72:73]
	v_pk_add_f32 v[72:73], v[80:81], v[72:73] neg_lo:[0,1] neg_hi:[0,1]
	v_pk_add_f32 v[80:81], v[86:87], v[76:77]
	v_pk_add_f32 v[76:77], v[86:87], v[76:77] neg_lo:[0,1] neg_hi:[0,1]
	v_pk_add_f32 v[86:87], v[68:69], v[72:73] op_sel:[0,1] op_sel_hi:[1,0] neg_hi:[0,1]
	v_pk_add_f32 v[68:69], v[68:69], v[72:73] op_sel:[0,1] op_sel_hi:[1,0] neg_lo:[0,1]
	v_pk_add_f32 v[72:73], v[84:85], v[92:93]
	v_pk_add_f32 v[84:85], v[84:85], v[92:93] neg_lo:[0,1] neg_hi:[0,1]
	v_pk_add_f32 v[92:93], v[88:89], v[98:99]
	v_pk_add_f32 v[88:89], v[88:89], v[98:99] neg_lo:[0,1] neg_hi:[0,1]
	v_pk_add_f32 v[98:99], v[72:73], v[92:93]
	v_pk_add_f32 v[72:73], v[72:73], v[92:93] neg_lo:[0,1] neg_hi:[0,1]
	v_pk_add_f32 v[92:93], v[84:85], v[88:89] op_sel:[0,1] op_sel_hi:[1,0] neg_hi:[0,1]
	v_pk_add_f32 v[84:85], v[84:85], v[88:89] op_sel:[0,1] op_sel_hi:[1,0] neg_lo:[0,1]
	v_pk_mul_f32 v[88:89], v[90:91], s[6:7] op_sel:[0,0] op_sel_hi:[0,1]
	v_pk_fma_f32 v[88:89], v[90:91], s[6:7], v[88:89] op_sel:[1,1,0] op_sel_hi:[1,0,1] neg_lo:[0,1,0]
	v_pk_mul_f32 v[90:91], v[66:67], s[10:11] op_sel:[0,0] op_sel_hi:[0,1]
	v_pk_fma_f32 v[90:91], v[66:67], s[10:11], v[90:91] op_sel:[1,1,0] op_sel_hi:[1,0,1] neg_lo:[0,1,0]
	v_pk_add_f32 v[66:67], v[86:87], v[86:87] op_sel:[0,1] op_sel_hi:[1,0] neg_hi:[0,1]
	s_nop 0
	v_pk_add_f32 v[72:73], v[72:73], v[72:73] op_sel:[0,1] op_sel_hi:[1,0] neg_lo:[0,1]
	v_pk_mul_f32 v[86:87], v[92:93], s[10:11] op_sel:[0,0] op_sel_hi:[0,1]
	v_pk_fma_f32 v[86:87], v[92:93], s[10:11], v[86:87] op_sel:[1,1,0] op_sel_hi:[1,0,1] neg_lo:[0,1,0]
	s_mov_b32 s14, s11
	v_pk_mul_f32 v[66:67], v[66:67], s[8:9]
	s_mov_b32 s15, s10
	v_pk_mul_f32 v[92:93], v[84:85], s[14:15] op_sel:[0,0] op_sel_hi:[0,1]
	v_pk_fma_f32 v[92:93], v[84:85], s[14:15], v[92:93] op_sel:[1,1,0] op_sel_hi:[1,0,1] neg_lo:[0,1,0]
	v_pk_add_f32 v[84:85], v[82:83], v[80:81]
	v_pk_add_f32 v[80:81], v[82:83], v[80:81] neg_lo:[0,1] neg_hi:[0,1]
	v_pk_add_f32 v[82:83], v[94:95], v[98:99]
	v_pk_add_f32 v[94:95], v[94:95], v[98:99] neg_lo:[0,1] neg_hi:[0,1]
	v_pk_add_f32 v[74:75], v[74:75], v[74:75] op_sel:[0,1] op_sel_hi:[1,0] neg_hi:[0,1]
	v_pk_add_f32 v[68:69], v[68:69], v[68:69] op_sel:[0,1] op_sel_hi:[1,0] neg_lo:[0,1]
	s_mov_b32 s13, s12
	v_pk_mul_f32 v[72:73], v[72:73], s[12:13]
	v_pk_add_f32 v[98:99], v[84:85], v[82:83]
	v_pk_add_f32 v[82:83], v[84:85], v[82:83] neg_lo:[0,1] neg_hi:[0,1]
	v_pk_add_f32 v[84:85], v[80:81], v[94:95] op_sel:[0,1] op_sel_hi:[1,0] neg_hi:[0,1]
	v_pk_add_f32 v[80:81], v[80:81], v[94:95] op_sel:[0,1] op_sel_hi:[1,0] neg_lo:[0,1]
	v_pk_add_f32 v[94:95], v[78:79], v[66:67]
	v_pk_add_f32 v[66:67], v[78:79], v[66:67] neg_lo:[0,1] neg_hi:[0,1]
	v_pk_add_f32 v[78:79], v[88:89], v[86:87]
	v_pk_add_f32 v[86:87], v[88:89], v[86:87] neg_lo:[0,1] neg_hi:[0,1]
	v_pk_mul_f32 v[74:75], v[74:75], s[8:9]
	v_pk_mul_f32 v[68:69], v[68:69], s[12:13]
	v_pk_add_f32 v[88:89], v[94:95], v[78:79]
	v_pk_add_f32 v[78:79], v[94:95], v[78:79] neg_lo:[0,1] neg_hi:[0,1]
	v_pk_add_f32 v[94:95], v[66:67], v[86:87] op_sel:[0,1] op_sel_hi:[1,0] neg_hi:[0,1]
	v_pk_add_f32 v[66:67], v[66:67], v[86:87] op_sel:[0,1] op_sel_hi:[1,0] neg_lo:[0,1]
	v_pk_add_f32 v[86:87], v[70:71], v[76:77] op_sel:[0,1] op_sel_hi:[1,0] neg_hi:[0,1]
	v_pk_add_f32 v[70:71], v[70:71], v[76:77] op_sel:[0,1] op_sel_hi:[1,0] neg_lo:[0,1]
	v_pk_add_f32 v[76:77], v[74:75], v[72:73]
	v_pk_add_f32 v[72:73], v[74:75], v[72:73] neg_lo:[0,1] neg_hi:[0,1]
	v_pk_add_f32 v[74:75], v[76:77], v[86:87]
	v_pk_add_f32 v[76:77], v[86:87], v[76:77] neg_lo:[0,1] neg_hi:[0,1]
	v_pk_add_f32 v[86:87], v[70:71], v[72:73] op_sel:[0,1] op_sel_hi:[1,0] neg_hi:[0,1]
	v_pk_add_f32 v[70:71], v[70:71], v[72:73] op_sel:[0,1] op_sel_hi:[1,0] neg_lo:[0,1]
	v_pk_add_f32 v[72:73], v[64:65], v[68:69]
	v_pk_add_f32 v[64:65], v[64:65], v[68:69] neg_lo:[0,1] neg_hi:[0,1]
	v_pk_add_f32 v[68:69], v[90:91], v[92:93]
	v_pk_add_f32 v[90:91], v[90:91], v[92:93] neg_lo:[0,1] neg_hi:[0,1]
	v_pk_add_f32 v[92:93], v[72:73], v[68:69]
	v_pk_add_f32 v[68:69], v[72:73], v[68:69] neg_lo:[0,1] neg_hi:[0,1]
	v_pk_add_f32 v[72:73], v[64:65], v[90:91] op_sel:[0,1] op_sel_hi:[1,0] neg_hi:[0,1]
	v_pk_add_f32 v[64:65], v[64:65], v[90:91] op_sel:[0,1] op_sel_hi:[1,0] neg_lo:[0,1]
	v_pk_mul_f32 v[90:91], v[88:89], v[30:31] op_sel:[0,0] op_sel_hi:[0,1]
	v_pk_fma_f32 v[90:91], v[88:89], v[30:31], v[90:91] op_sel:[1,1,0] op_sel_hi:[1,0,1] neg_lo:[0,1,0]
	v_pk_mul_f32 v[88:89], v[74:75], v[28:29] op_sel:[0,0] op_sel_hi:[0,1]
	v_pk_fma_f32 v[88:89], v[74:75], v[28:29], v[88:89] op_sel:[1,1,0] op_sel_hi:[1,0,1] neg_lo:[0,1,0]
	v_pk_mul_f32 v[74:75], v[92:93], v[26:27] op_sel:[0,0] op_sel_hi:[0,1]
	v_pk_fma_f32 v[74:75], v[92:93], v[26:27], v[74:75] op_sel:[1,1,0] op_sel_hi:[1,0,1] neg_lo:[0,1,0]
	s_barrier
	ds_write_b64 v1, v[74:75] offset:6552
	v_pk_mul_f32 v[74:75], v[84:85], v[24:25] op_sel:[0,0] op_sel_hi:[0,1]
	v_pk_fma_f32 v[74:75], v[84:85], v[24:25], v[74:75] op_sel:[1,1,0] op_sel_hi:[1,0,1] neg_lo:[0,1,0]
	ds_write_b64 v1, v[74:75] offset:8736
	v_pk_mul_f32 v[74:75], v[94:95], v[20:21] op_sel:[0,0] op_sel_hi:[0,1]
	v_pk_fma_f32 v[74:75], v[94:95], v[20:21], v[74:75] op_sel:[1,1,0] op_sel_hi:[1,0,1] neg_lo:[0,1,0]
	ds_write_b64 v1, v[74:75] offset:10920
	v_pk_mul_f32 v[74:75], v[86:87], v[16:17] op_sel:[0,0] op_sel_hi:[0,1]
	v_pk_fma_f32 v[74:75], v[86:87], v[16:17], v[74:75] op_sel:[1,1,0] op_sel_hi:[1,0,1] neg_lo:[0,1,0]
	ds_write_b64 v1, v[74:75] offset:13104
	v_pk_mul_f32 v[74:75], v[72:73], v[10:11] op_sel:[0,0] op_sel_hi:[0,1]
	v_pk_fma_f32 v[74:75], v[72:73], v[10:11], v[74:75] op_sel:[1,1,0] op_sel_hi:[1,0,1] neg_lo:[0,1,0]
	v_pk_mul_f32 v[72:73], v[82:83], v[22:23] op_sel:[0,0] op_sel_hi:[0,1]
	v_pk_fma_f32 v[72:73], v[82:83], v[22:23], v[72:73] op_sel:[1,1,0] op_sel_hi:[1,0,1] neg_lo:[0,1,0]
	ds_write_b64 v1, v[72:73] offset:17472
	v_pk_mul_f32 v[72:73], v[78:79], v[18:19] op_sel:[0,0] op_sel_hi:[0,1]
	v_pk_fma_f32 v[72:73], v[78:79], v[18:19], v[72:73] op_sel:[1,1,0] op_sel_hi:[1,0,1] neg_lo:[0,1,0]
	ds_write_b64 v1, v[72:73] offset:19656
	v_pk_mul_f32 v[72:73], v[76:77], v[12:13] op_sel:[0,0] op_sel_hi:[0,1]
	v_pk_fma_f32 v[72:73], v[76:77], v[12:13], v[72:73] op_sel:[1,1,0] op_sel_hi:[1,0,1] neg_lo:[0,1,0]
	ds_write_b64 v1, v[72:73] offset:21840
	v_pk_mul_f32 v[72:73], v[68:69], v[14:15] op_sel:[0,0] op_sel_hi:[0,1]
	v_pk_fma_f32 v[72:73], v[68:69], v[14:15], v[72:73] op_sel:[1,1,0] op_sel_hi:[1,0,1] neg_lo:[0,1,0]
	v_pk_mul_f32 v[68:69], v[80:81], v[6:7] op_sel:[0,0] op_sel_hi:[0,1]
	v_pk_fma_f32 v[68:69], v[80:81], v[6:7], v[68:69] op_sel:[1,1,0] op_sel_hi:[1,0,1] neg_lo:[0,1,0]
	ds_write_b64 v1, v[68:69] offset:26208
	v_pk_mul_f32 v[68:69], v[66:67], v[8:9] op_sel:[0,0] op_sel_hi:[0,1]
	v_pk_fma_f32 v[68:69], v[66:67], v[8:9], v[68:69] op_sel:[1,1,0] op_sel_hi:[1,0,1] neg_lo:[0,1,0]
	v_pk_mul_f32 v[66:67], v[70:71], v[4:5] op_sel:[0,0] op_sel_hi:[0,1]
	v_pk_fma_f32 v[66:67], v[70:71], v[4:5], v[66:67] op_sel:[1,1,0] op_sel_hi:[1,0,1] neg_lo:[0,1,0]
	ds_write_b64 v1, v[66:67] offset:30576
	v_pk_mul_f32 v[66:67], v[64:65], v[2:3] op_sel:[0,0] op_sel_hi:[0,1]
	v_pk_fma_f32 v[66:67], v[64:65], v[2:3], v[66:67] op_sel:[1,1,0] op_sel_hi:[1,0,1] neg_lo:[0,1,0]
	ds_write_b64 v1, v[98:99]
	ds_write_b64 v1, v[90:91] offset:2184
	ds_write_b64 v1, v[88:89] offset:4368
	ds_write_b64 v1, v[74:75] offset:15288
	ds_write_b64 v1, v[72:73] offset:24024
	ds_write_b64 v1, v[68:69] offset:28392
	ds_write_b64 v1, v[66:67] offset:32760
	s_waitcnt lgkmcnt(0)
	s_barrier
	ds_read2_b64 v[64:67], v96 offset1:16
	ds_read2_b64 v[68:71], v96 offset0:32 offset1:48
	ds_read2_b64 v[72:75], v96 offset0:64 offset1:80
	ds_read2_b64 v[76:79], v96 offset0:128 offset1:144
	ds_read2_b64 v[80:83], v96 offset0:96 offset1:112
	ds_read2_b64 v[84:87], v96 offset0:192 offset1:208
	ds_read2_b64 v[88:91], v96 offset0:160 offset1:176
	ds_read2_b64 v[92:95], v96 offset0:224 offset1:240
	s_waitcnt lgkmcnt(4)
	v_pk_add_f32 v[98:99], v[64:65], v[76:77]
	v_pk_add_f32 v[64:65], v[64:65], v[76:77] neg_lo:[0,1] neg_hi:[0,1]
	s_waitcnt lgkmcnt(2)
	v_pk_add_f32 v[76:77], v[72:73], v[84:85]
	v_pk_add_f32 v[72:73], v[72:73], v[84:85] neg_lo:[0,1] neg_hi:[0,1]
	v_pk_add_f32 v[84:85], v[98:99], v[76:77]
	v_pk_add_f32 v[76:77], v[98:99], v[76:77] neg_lo:[0,1] neg_hi:[0,1]
	v_pk_add_f32 v[98:99], v[64:65], v[72:73] op_sel:[0,1] op_sel_hi:[1,0] neg_hi:[0,1]
	v_pk_add_f32 v[64:65], v[64:65], v[72:73] op_sel:[0,1] op_sel_hi:[1,0] neg_lo:[0,1]
	v_pk_add_f32 v[72:73], v[66:67], v[78:79]
	v_pk_add_f32 v[66:67], v[66:67], v[78:79] neg_lo:[0,1] neg_hi:[0,1]
	v_pk_add_f32 v[78:79], v[74:75], v[86:87]
	v_pk_add_f32 v[74:75], v[74:75], v[86:87] neg_lo:[0,1] neg_hi:[0,1]
	v_pk_add_f32 v[86:87], v[72:73], v[78:79]
	v_pk_add_f32 v[72:73], v[72:73], v[78:79] neg_lo:[0,1] neg_hi:[0,1]
	v_pk_add_f32 v[78:79], v[66:67], v[74:75] op_sel:[0,1] op_sel_hi:[1,0] neg_hi:[0,1]
	v_pk_add_f32 v[66:67], v[66:67], v[74:75] op_sel:[0,1] op_sel_hi:[1,0] neg_lo:[0,1]
	s_waitcnt lgkmcnt(1)
	v_pk_add_f32 v[74:75], v[68:69], v[88:89]
	v_pk_add_f32 v[68:69], v[68:69], v[88:89] neg_lo:[0,1] neg_hi:[0,1]
	s_waitcnt lgkmcnt(0)
	v_pk_add_f32 v[88:89], v[80:81], v[92:93]
	v_pk_add_f32 v[80:81], v[80:81], v[92:93] neg_lo:[0,1] neg_hi:[0,1]
	v_pk_add_f32 v[92:93], v[74:75], v[88:89]
	v_pk_add_f32 v[74:75], v[74:75], v[88:89] neg_lo:[0,1] neg_hi:[0,1]
	v_pk_add_f32 v[88:89], v[68:69], v[80:81] op_sel:[0,1] op_sel_hi:[1,0] neg_hi:[0,1]
	v_pk_add_f32 v[68:69], v[68:69], v[80:81] op_sel:[0,1] op_sel_hi:[1,0] neg_lo:[0,1]
	v_pk_add_f32 v[80:81], v[70:71], v[90:91]
	v_pk_add_f32 v[70:71], v[70:71], v[90:91] neg_lo:[0,1] neg_hi:[0,1]
	v_pk_add_f32 v[90:91], v[82:83], v[94:95]
	v_pk_add_f32 v[82:83], v[82:83], v[94:95] neg_lo:[0,1] neg_hi:[0,1]
	v_pk_add_f32 v[94:95], v[80:81], v[90:91]
	v_pk_add_f32 v[80:81], v[80:81], v[90:91] neg_lo:[0,1] neg_hi:[0,1]
	v_pk_add_f32 v[90:91], v[70:71], v[82:83] op_sel:[0,1] op_sel_hi:[1,0] neg_hi:[0,1]
	v_pk_add_f32 v[70:71], v[70:71], v[82:83] op_sel:[0,1] op_sel_hi:[1,0] neg_lo:[0,1]
	v_pk_mul_f32 v[82:83], v[78:79], s[6:7] op_sel:[0,0] op_sel_hi:[0,1]
	v_pk_fma_f32 v[82:83], v[78:79], s[6:7], v[82:83] op_sel:[1,1,0] op_sel_hi:[1,0,1] neg_lo:[0,1,0]
	v_pk_mul_f32 v[78:79], v[66:67], s[10:11] op_sel:[0,0] op_sel_hi:[0,1]
	v_pk_fma_f32 v[78:79], v[66:67], s[10:11], v[78:79] op_sel:[1,1,0] op_sel_hi:[1,0,1] neg_lo:[0,1,0]
	v_pk_add_f32 v[66:67], v[88:89], v[88:89] op_sel:[0,1] op_sel_hi:[1,0] neg_hi:[0,1]
	v_pk_add_f32 v[72:73], v[72:73], v[72:73] op_sel:[0,1] op_sel_hi:[1,0] neg_hi:[0,1]
	s_nop 0
	v_pk_mul_f32 v[88:89], v[90:91], s[10:11] op_sel:[0,0] op_sel_hi:[0,1]
	v_pk_fma_f32 v[88:89], v[90:91], s[10:11], v[88:89] op_sel:[1,1,0] op_sel_hi:[1,0,1] neg_lo:[0,1,0]
	v_pk_mul_f32 v[90:91], v[70:71], s[14:15] op_sel:[0,0] op_sel_hi:[0,1]
	v_pk_fma_f32 v[90:91], v[70:71], s[14:15], v[90:91] op_sel:[1,1,0] op_sel_hi:[1,0,1] neg_lo:[0,1,0]
	v_pk_add_f32 v[70:71], v[84:85], v[92:93]
	v_pk_mul_f32 v[66:67], v[66:67], s[8:9]
	v_pk_add_f32 v[84:85], v[84:85], v[92:93] neg_lo:[0,1] neg_hi:[0,1]
	v_pk_add_f32 v[92:93], v[86:87], v[94:95]
	v_pk_add_f32 v[86:87], v[86:87], v[94:95] neg_lo:[0,1] neg_hi:[0,1]
	v_pk_add_f32 v[68:69], v[68:69], v[68:69] op_sel:[0,1] op_sel_hi:[1,0] neg_lo:[0,1]
	v_pk_add_f32 v[80:81], v[80:81], v[80:81] op_sel:[0,1] op_sel_hi:[1,0] neg_lo:[0,1]
	v_pk_add_f32 v[94:95], v[70:71], v[92:93]
	v_pk_add_f32 v[92:93], v[70:71], v[92:93] neg_lo:[0,1] neg_hi:[0,1]
	v_pk_add_f32 v[100:101], v[84:85], v[86:87] op_sel:[0,1] op_sel_hi:[1,0] neg_hi:[0,1]
	v_pk_add_f32 v[84:85], v[84:85], v[86:87] op_sel:[0,1] op_sel_hi:[1,0] neg_lo:[0,1]
	v_pk_add_f32 v[70:71], v[98:99], v[66:67]
	v_pk_add_f32 v[66:67], v[98:99], v[66:67] neg_lo:[0,1] neg_hi:[0,1]
	v_pk_add_f32 v[86:87], v[82:83], v[88:89]
	v_pk_add_f32 v[82:83], v[82:83], v[88:89] neg_lo:[0,1] neg_hi:[0,1]
	v_pk_mul_f32 v[72:73], v[72:73], s[8:9]
	v_pk_mul_f32 v[68:69], v[68:69], s[12:13]
	v_pk_mul_f32 v[80:81], v[80:81], s[12:13]
	v_pk_add_f32 v[88:89], v[70:71], v[86:87]
	v_pk_add_f32 v[86:87], v[70:71], v[86:87] neg_lo:[0,1] neg_hi:[0,1]
	v_pk_add_f32 v[98:99], v[66:67], v[82:83] op_sel:[0,1] op_sel_hi:[1,0] neg_hi:[0,1]
	v_pk_add_f32 v[82:83], v[66:67], v[82:83] op_sel:[0,1] op_sel_hi:[1,0] neg_lo:[0,1]
	v_pk_add_f32 v[66:67], v[76:77], v[74:75] op_sel:[0,1] op_sel_hi:[1,0] neg_hi:[0,1]
	v_pk_add_f32 v[70:71], v[76:77], v[74:75] op_sel:[0,1] op_sel_hi:[1,0] neg_lo:[0,1]
	v_pk_add_f32 v[74:75], v[72:73], v[80:81]
	v_pk_add_f32 v[72:73], v[72:73], v[80:81] neg_lo:[0,1] neg_hi:[0,1]
	v_pk_add_f32 v[76:77], v[74:75], v[66:67]
	v_pk_add_f32 v[74:75], v[66:67], v[74:75] neg_lo:[0,1] neg_hi:[0,1]
	v_pk_add_f32 v[66:67], v[64:65], v[68:69]
	v_pk_add_f32 v[64:65], v[64:65], v[68:69] neg_lo:[0,1] neg_hi:[0,1]
	v_pk_add_f32 v[68:69], v[78:79], v[90:91]
	v_pk_add_f32 v[80:81], v[70:71], v[72:73] op_sel:[0,1] op_sel_hi:[1,0] neg_hi:[0,1]
	v_pk_add_f32 v[72:73], v[70:71], v[72:73] op_sel:[0,1] op_sel_hi:[1,0] neg_lo:[0,1]
	v_pk_add_f32 v[70:71], v[78:79], v[90:91] neg_lo:[0,1] neg_hi:[0,1]
	v_pk_add_f32 v[78:79], v[66:67], v[68:69]
	v_pk_add_f32 v[90:91], v[66:67], v[68:69] neg_lo:[0,1] neg_hi:[0,1]
	v_mov_b32_e32 v68, v0
	v_pk_add_f32 v[102:103], v[64:65], v[70:71] op_sel:[0,1] op_sel_hi:[1,0] neg_hi:[0,1]
	v_pk_add_f32 v[104:105], v[64:65], v[70:71] op_sel:[0,1] op_sel_hi:[1,0] neg_lo:[0,1]
	s_nop 0
	v_ashrrev_i32_e32 v64, 4, v68
	v_lshlrev_b32_e32 v97, 3, v64
	v_add_u32_e32 v108, 0x8800, v97
	v_and_b32_e32 v68, 15, v68
	ds_read2_b64 v[64:67], v108 offset0:16 offset1:32
	v_mad_u32_u24 v109, v68, s5, v97
	ds_read2_b64 v[68:71], v108 offset0:48 offset1:64
	s_waitcnt lgkmcnt(1)
	v_pk_mul_f32 v[106:107], v[88:89], v[64:65] op_sel:[0,0] op_sel_hi:[0,1]
	v_pk_fma_f32 v[106:107], v[88:89], v[64:65], v[106:107] op_sel:[1,1,0] op_sel_hi:[1,0,1] neg_lo:[0,1,0]
	v_pk_mul_f32 v[88:89], v[76:77], v[66:67] op_sel:[0,0] op_sel_hi:[0,1]
	v_pk_fma_f32 v[88:89], v[76:77], v[66:67], v[88:89] op_sel:[1,1,0] op_sel_hi:[1,0,1] neg_lo:[0,1,0]
	s_waitcnt lgkmcnt(0)
	v_pk_mul_f32 v[76:77], v[78:79], v[68:69] op_sel:[0,0] op_sel_hi:[0,1]
	v_pk_fma_f32 v[76:77], v[78:79], v[68:69], v[76:77] op_sel:[1,1,0] op_sel_hi:[1,0,1] neg_lo:[0,1,0]
	ds_write2_b64 v109, v[88:89], v[76:77] offset0:32 offset1:48
	v_pk_mul_f32 v[76:77], v[100:101], v[70:71] op_sel:[0,0] op_sel_hi:[0,1]
	v_pk_fma_f32 v[76:77], v[100:101], v[70:71], v[76:77] op_sel:[1,1,0] op_sel_hi:[1,0,1] neg_lo:[0,1,0]
	ds_read2_b64 v[64:67], v108 offset0:80 offset1:96
	s_waitcnt lgkmcnt(0)
	v_pk_mul_f32 v[78:79], v[98:99], v[64:65] op_sel:[0,0] op_sel_hi:[0,1]
	v_pk_fma_f32 v[78:79], v[98:99], v[64:65], v[78:79] op_sel:[1,1,0] op_sel_hi:[1,0,1] neg_lo:[0,1,0]
	ds_write2_b64 v109, v[76:77], v[78:79] offset0:64 offset1:80
	v_pk_mul_f32 v[76:77], v[80:81], v[66:67] op_sel:[0,0] op_sel_hi:[0,1]
	v_pk_fma_f32 v[76:77], v[80:81], v[66:67], v[76:77] op_sel:[1,1,0] op_sel_hi:[1,0,1] neg_lo:[0,1,0]
	ds_read2_b64 v[68:71], v108 offset0:112 offset1:128
	ds_read2_b64 v[64:67], v108 offset0:144 offset1:160
	s_waitcnt lgkmcnt(1)
	v_pk_mul_f32 v[78:79], v[102:103], v[68:69] op_sel:[0,0] op_sel_hi:[0,1]
	v_pk_fma_f32 v[78:79], v[102:103], v[68:69], v[78:79] op_sel:[1,1,0] op_sel_hi:[1,0,1] neg_lo:[0,1,0]
	ds_write2_b64 v109, v[76:77], v[78:79] offset0:96 offset1:112
	v_pk_mul_f32 v[76:77], v[92:93], v[70:71] op_sel:[0,0] op_sel_hi:[0,1]
	v_pk_fma_f32 v[76:77], v[92:93], v[70:71], v[76:77] op_sel:[1,1,0] op_sel_hi:[1,0,1] neg_lo:[0,1,0]
	ds_read2_b64 v[68:71], v108 offset0:176 offset1:192
	s_waitcnt lgkmcnt(2)
	v_pk_mul_f32 v[78:79], v[86:87], v[64:65] op_sel:[0,0] op_sel_hi:[0,1]
	v_pk_fma_f32 v[78:79], v[86:87], v[64:65], v[78:79] op_sel:[1,1,0] op_sel_hi:[1,0,1] neg_lo:[0,1,0]
	ds_write2_b64 v109, v[76:77], v[78:79] offset0:128 offset1:144
	v_pk_mul_f32 v[76:77], v[74:75], v[66:67] op_sel:[0,0] op_sel_hi:[0,1]
	v_pk_fma_f32 v[76:77], v[74:75], v[66:67], v[76:77] op_sel:[1,1,0] op_sel_hi:[1,0,1] neg_lo:[0,1,0]
	ds_read2_b64 v[64:67], v108 offset0:208 offset1:224
	s_waitcnt lgkmcnt(2)
	v_pk_mul_f32 v[74:75], v[90:91], v[68:69] op_sel:[0,0] op_sel_hi:[0,1]
	v_pk_fma_f32 v[74:75], v[90:91], v[68:69], v[74:75] op_sel:[1,1,0] op_sel_hi:[1,0,1] neg_lo:[0,1,0]
	ds_write2_b64 v109, v[76:77], v[74:75] offset0:160 offset1:176
	v_pk_mul_f32 v[74:75], v[84:85], v[70:71] op_sel:[0,0] op_sel_hi:[0,1]
	v_pk_fma_f32 v[74:75], v[84:85], v[70:71], v[74:75] op_sel:[1,1,0] op_sel_hi:[1,0,1] neg_lo:[0,1,0]
	s_waitcnt lgkmcnt(1)
	v_pk_mul_f32 v[70:71], v[82:83], v[64:65] op_sel:[0,0] op_sel_hi:[0,1]
	v_pk_fma_f32 v[70:71], v[82:83], v[64:65], v[70:71] op_sel:[1,1,0] op_sel_hi:[1,0,1] neg_lo:[0,1,0]
	v_pk_mul_f32 v[64:65], v[72:73], v[66:67] op_sel:[0,0] op_sel_hi:[0,1]
	v_pk_fma_f32 v[64:65], v[72:73], v[66:67], v[64:65] op_sel:[1,1,0] op_sel_hi:[1,0,1] neg_lo:[0,1,0]
	ds_read_b64 v[68:69], v97 offset:36736
	s_waitcnt lgkmcnt(0)
	v_pk_mul_f32 v[66:67], v[104:105], v[68:69] op_sel:[0,0] op_sel_hi:[0,1]
	v_pk_fma_f32 v[66:67], v[104:105], v[68:69], v[66:67] op_sel:[1,1,0] op_sel_hi:[1,0,1] neg_lo:[0,1,0]
	ds_write2_b64 v109, v[64:65], v[66:67] offset0:224 offset1:240
	v_mov_b32_e32 v64, v0
	ds_write2_b64 v109, v[94:95], v[106:107] offset1:16
	ds_write2_b64 v109, v[74:75], v[70:71] offset0:192 offset1:208
	s_waitcnt lgkmcnt(0)
	s_barrier
	s_nop 0
	v_and_b32_e32 v65, 15, v64
	v_and_b32_e32 v64, 0x1ffffff0, v64
	v_lshlrev_b32_e32 v64, 3, v64
	v_mad_u32_u24 v92, v65, s5, v64
	ds_read2_b64 v[64:67], v92 offset1:1
	ds_read2_b64 v[68:71], v92 offset0:2 offset1:3
	ds_read2_b64 v[72:75], v92 offset0:8 offset1:9
	ds_read2_b64 v[76:79], v92 offset0:4 offset1:5
	ds_read2_b64 v[80:83], v92 offset0:6 offset1:7
	ds_read2_b64 v[84:87], v92 offset0:12 offset1:13
	ds_read2_b64 v[88:91], v92 offset0:10 offset1:11
	ds_read2_b64 v[92:95], v92 offset0:14 offset1:15
	s_waitcnt lgkmcnt(5)
	v_pk_add_f32 v[98:99], v[64:65], v[72:73]
	v_pk_add_f32 v[64:65], v[64:65], v[72:73] neg_lo:[0,1] neg_hi:[0,1]
	s_waitcnt lgkmcnt(2)
	v_pk_add_f32 v[72:73], v[76:77], v[84:85]
	v_pk_add_f32 v[76:77], v[76:77], v[84:85] neg_lo:[0,1] neg_hi:[0,1]
	v_pk_add_f32 v[84:85], v[98:99], v[72:73]
	v_pk_add_f32 v[98:99], v[98:99], v[72:73] neg_lo:[0,1] neg_hi:[0,1]
	v_pk_add_f32 v[100:101], v[64:65], v[76:77] op_sel:[0,1] op_sel_hi:[1,0] neg_hi:[0,1]
	v_pk_add_f32 v[102:103], v[64:65], v[76:77] op_sel:[0,1] op_sel_hi:[1,0] neg_lo:[0,1]
	v_pk_add_f32 v[64:65], v[66:67], v[74:75]
	v_pk_add_f32 v[72:73], v[78:79], v[86:87]
	v_pk_add_f32 v[66:67], v[66:67], v[74:75] neg_lo:[0,1] neg_hi:[0,1]
	v_pk_add_f32 v[74:75], v[78:79], v[86:87] neg_lo:[0,1] neg_hi:[0,1]
	v_pk_add_f32 v[76:77], v[64:65], v[72:73]
	v_pk_add_f32 v[64:65], v[64:65], v[72:73] neg_lo:[0,1] neg_hi:[0,1]
	v_pk_add_f32 v[72:73], v[66:67], v[74:75] op_sel:[0,1] op_sel_hi:[1,0] neg_hi:[0,1]
	v_pk_add_f32 v[66:67], v[66:67], v[74:75] op_sel:[0,1] op_sel_hi:[1,0] neg_lo:[0,1]
	s_waitcnt lgkmcnt(1)
	v_pk_add_f32 v[74:75], v[68:69], v[88:89]
	s_waitcnt lgkmcnt(0)
	v_pk_add_f32 v[78:79], v[80:81], v[92:93]
	v_pk_add_f32 v[64:65], v[64:65], v[64:65] op_sel:[0,1] op_sel_hi:[1,0] neg_hi:[0,1]
	v_pk_add_f32 v[68:69], v[68:69], v[88:89] neg_lo:[0,1] neg_hi:[0,1]
	v_pk_add_f32 v[80:81], v[80:81], v[92:93] neg_lo:[0,1] neg_hi:[0,1]
	v_pk_add_f32 v[86:87], v[74:75], v[78:79]
	v_pk_add_f32 v[78:79], v[74:75], v[78:79] neg_lo:[0,1] neg_hi:[0,1]
	v_pk_add_f32 v[74:75], v[68:69], v[80:81] op_sel:[0,1] op_sel_hi:[1,0] neg_hi:[0,1]
	v_pk_mul_f32 v[92:93], v[64:65], s[8:9]
	v_pk_add_f32 v[68:69], v[68:69], v[80:81] op_sel:[0,1] op_sel_hi:[1,0] neg_lo:[0,1]
	v_pk_add_f32 v[80:81], v[70:71], v[90:91]
	v_pk_add_f32 v[64:65], v[74:75], v[74:75] op_sel:[0,1] op_sel_hi:[1,0] neg_hi:[0,1]
	v_pk_add_f32 v[70:71], v[70:71], v[90:91] neg_lo:[0,1] neg_hi:[0,1]
	v_pk_add_f32 v[88:89], v[82:83], v[94:95]
	v_pk_add_f32 v[82:83], v[82:83], v[94:95] neg_lo:[0,1] neg_hi:[0,1]
	v_pk_mul_f32 v[94:95], v[66:67], s[10:11] op_sel:[0,0] op_sel_hi:[0,1]
	v_pk_fma_f32 v[94:95], v[66:67], s[10:11], v[94:95] op_sel:[1,1,0] op_sel_hi:[1,0,1] neg_lo:[0,1,0]
	v_pk_mul_f32 v[66:67], v[64:65], s[8:9]
	v_pk_add_f32 v[64:65], v[68:69], v[68:69] op_sel:[0,1] op_sel_hi:[1,0] neg_lo:[0,1]
	v_pk_add_f32 v[90:91], v[80:81], v[88:89]
	v_pk_add_f32 v[80:81], v[80:81], v[88:89] neg_lo:[0,1] neg_hi:[0,1]
	v_pk_add_f32 v[88:89], v[70:71], v[82:83] op_sel:[0,1] op_sel_hi:[1,0] neg_hi:[0,1]
	v_pk_add_f32 v[70:71], v[70:71], v[82:83] op_sel:[0,1] op_sel_hi:[1,0] neg_lo:[0,1]
	v_pk_mul_f32 v[104:105], v[64:65], s[12:13]
	v_pk_mul_f32 v[82:83], v[72:73], s[6:7] op_sel:[0,0] op_sel_hi:[0,1]
	v_pk_fma_f32 v[82:83], v[72:73], s[6:7], v[82:83] op_sel:[1,1,0] op_sel_hi:[1,0,1] neg_lo:[0,1,0]
	v_pk_add_f32 v[72:73], v[76:77], v[90:91]
	v_pk_add_f32 v[64:65], v[80:81], v[80:81] op_sel:[0,1] op_sel_hi:[1,0] neg_lo:[0,1]
	v_pk_mul_f32 v[68:69], v[88:89], s[10:11] op_sel:[0,0] op_sel_hi:[0,1]
	v_pk_fma_f32 v[68:69], v[88:89], s[10:11], v[68:69] op_sel:[1,1,0] op_sel_hi:[1,0,1] neg_lo:[0,1,0]
	v_pk_mul_f32 v[108:109], v[70:71], s[14:15] op_sel:[0,0] op_sel_hi:[0,1]
	v_pk_fma_f32 v[108:109], v[70:71], s[14:15], v[108:109] op_sel:[1,1,0] op_sel_hi:[1,0,1] neg_lo:[0,1,0]
	v_pk_add_f32 v[70:71], v[84:85], v[86:87] neg_lo:[0,1] neg_hi:[0,1]
	v_pk_mul_f32 v[106:107], v[64:65], s[12:13]
	v_pk_add_f32 v[64:65], v[84:85], v[86:87]
	v_pk_add_f32 v[74:75], v[76:77], v[90:91] neg_lo:[0,1] neg_hi:[0,1]
	v_pk_add_f32 v[88:89], v[64:65], v[72:73]
	v_pk_add_f32 v[72:73], v[64:65], v[72:73] neg_lo:[0,1] neg_hi:[0,1]
	v_pk_add_f32 v[80:81], v[70:71], v[74:75] op_sel:[0,1] op_sel_hi:[1,0] neg_hi:[0,1]
	v_pk_add_f32 v[64:65], v[70:71], v[74:75] op_sel:[0,1] op_sel_hi:[1,0] neg_lo:[0,1]
	v_pk_add_f32 v[70:71], v[100:101], v[66:67]
	v_pk_add_f32 v[66:67], v[100:101], v[66:67] neg_lo:[0,1] neg_hi:[0,1]
	v_pk_add_f32 v[74:75], v[82:83], v[68:69]
	v_pk_add_f32 v[68:69], v[82:83], v[68:69] neg_lo:[0,1] neg_hi:[0,1]
	v_pk_add_f32 v[90:91], v[70:71], v[74:75]
	v_pk_add_f32 v[74:75], v[70:71], v[74:75] neg_lo:[0,1] neg_hi:[0,1]
	v_pk_add_f32 v[82:83], v[66:67], v[68:69] op_sel:[0,1] op_sel_hi:[1,0] neg_hi:[0,1]
	v_pk_add_f32 v[66:67], v[66:67], v[68:69] op_sel:[0,1] op_sel_hi:[1,0] neg_lo:[0,1]
	v_pk_add_f32 v[68:69], v[98:99], v[78:79] op_sel:[0,1] op_sel_hi:[1,0] neg_hi:[0,1]
	v_pk_add_f32 v[70:71], v[98:99], v[78:79] op_sel:[0,1] op_sel_hi:[1,0] neg_lo:[0,1]
	v_pk_add_f32 v[76:77], v[92:93], v[106:107]
	v_pk_add_f32 v[78:79], v[92:93], v[106:107] neg_lo:[0,1] neg_hi:[0,1]
	v_pk_add_f32 v[92:93], v[76:77], v[68:69]
	v_pk_add_f32 v[76:77], v[68:69], v[76:77] neg_lo:[0,1] neg_hi:[0,1]
	v_pk_add_f32 v[86:87], v[70:71], v[78:79] op_sel:[0,1] op_sel_hi:[1,0] neg_hi:[0,1]
	v_pk_add_f32 v[68:69], v[70:71], v[78:79] op_sel:[0,1] op_sel_hi:[1,0] neg_lo:[0,1]
	v_pk_add_f32 v[70:71], v[102:103], v[104:105]
	v_pk_add_f32 v[98:99], v[102:103], v[104:105] neg_lo:[0,1] neg_hi:[0,1]
	v_pk_add_f32 v[78:79], v[94:95], v[108:109]
	v_pk_add_f32 v[100:101], v[94:95], v[108:109] neg_lo:[0,1] neg_hi:[0,1]
	v_pk_add_f32 v[94:95], v[70:71], v[78:79]
	v_pk_add_f32 v[78:79], v[70:71], v[78:79] neg_lo:[0,1] neg_hi:[0,1]
	v_pk_add_f32 v[84:85], v[98:99], v[100:101] op_sel:[0,1] op_sel_hi:[1,0] neg_hi:[0,1]
	v_pk_add_f32 v[70:71], v[98:99], v[100:101] op_sel:[0,1] op_sel_hi:[1,0] neg_lo:[0,1]
	v_mov_b32_e32 v98, v0
	s_nop 0
	v_and_b32_e32 v97, -16, v98
	v_and_b32_e32 v99, 15, v98
	v_lshlrev_b32_e32 v100, 3, v97
	v_mad_u32_u24 v100, v99, s5, v100
	v_cmp_ne_u32_e32 vcc, 0, v99
	ds_write2_b64 v100, v[88:89], v[90:91] offset1:1
	ds_write2_b64 v100, v[92:93], v[94:95] offset0:2 offset1:3
	ds_write2_b64 v100, v[80:81], v[82:83] offset0:4 offset1:5
	ds_write2_b64 v100, v[86:87], v[84:85] offset0:6 offset1:7
	ds_write2_b64 v100, v[72:73], v[74:75] offset0:8 offset1:9
	ds_write2_b64 v100, v[76:77], v[78:79] offset0:10 offset1:11
	ds_write2_b64 v100, v[64:65], v[66:67] offset0:12 offset1:13
	ds_write2_b64 v100, v[68:69], v[70:71] offset0:14 offset1:15
	s_waitcnt lgkmcnt(0)
	s_barrier
	s_and_saveexec_b64 s[6:7], vcc
	s_xor_b64 s[6:7], exec, s[6:7]
	v_sub_u32_e32 v99, 16, v99
	v_mul_u32_u24_e32 v99, 0x111, v99
	v_sub_u32_e32 v97, v99, v97
	v_add_u32_e32 v100, 0xf0, v97
	s_andn2_saveexec_b64 s[6:7], s[6:7]
	v_sub_u32_e32 v97, 0x100, v98
	v_cmp_lt_u32_e32 vcc, 15, v98
	s_nop 1
	v_cndmask_b32_e32 v100, 1, v97, vcc
	s_or_b64 exec, exec, s[6:7]
	v_mov_b32_e32 v97, 0
	v_lshlrev_b32_e32 v110, 3, v100
	ds_read_b64 v[108:109], v97
	ds_read2_b64 v[100:103], v110 offset0:14 offset1:15
	v_cmp_eq_u32_e32 vcc, 0, v98
	ds_read2_b64 v[104:107], v110 offset0:12 offset1:13
	s_mov_b32 s6, 0x3f6c835e
	s_mov_b32 s7, 0xbec3ef15
	s_waitcnt lgkmcnt(1)
	v_cndmask_b32_e32 v99, v103, v109, vcc
	v_cndmask_b32_e32 v98, v102, v108, vcc
	v_pk_add_f32 v[102:103], v[88:89], v[98:99] neg_hi:[0,1]
	v_pk_add_f32 v[88:89], v[88:89], v[98:99] neg_lo:[0,1]
	s_mov_b32 s9, s8
	v_pk_mul_f32 v[98:99], v[102:103], v[88:89] op_sel:[0,0] op_sel_hi:[0,1]
	v_pk_fma_f32 v[98:99], v[102:103], v[88:89], v[98:99] op_sel:[1,1,0] op_sel_hi:[1,0,1] neg_hi:[0,1,0]
	v_pk_add_f32 v[88:89], v[90:91], v[100:101] neg_hi:[0,1]
	v_pk_add_f32 v[90:91], v[90:91], v[100:101] neg_lo:[0,1]
	s_mov_b32 s14, s11
	v_pk_add_f32 v[62:63], v[62:63], v[98:99] op_sel:[1,0] op_sel_hi:[0,1] neg_lo:[0,1] neg_hi:[1,1]
	v_pk_mul_f32 v[98:99], v[88:89], v[90:91] op_sel:[0,0] op_sel_hi:[0,1]
	v_pk_fma_f32 v[98:99], v[88:89], v[90:91], v[98:99] op_sel:[1,1,0] op_sel_hi:[1,0,1] neg_hi:[0,1,0]
	s_waitcnt lgkmcnt(0)
	v_pk_add_f32 v[88:89], v[92:93], v[106:107] neg_hi:[0,1]
	v_pk_add_f32 v[90:91], v[92:93], v[106:107] neg_lo:[0,1]
	s_mov_b32 s15, s10
	v_pk_mul_f32 v[92:93], v[88:89], v[90:91] op_sel:[0,0] op_sel_hi:[0,1]
	v_pk_fma_f32 v[92:93], v[88:89], v[90:91], v[92:93] op_sel:[1,1,0] op_sel_hi:[1,0,1] neg_hi:[0,1,0]
	v_pk_add_f32 v[60:61], v[60:61], v[98:99] op_sel:[1,0] op_sel_hi:[0,1] neg_lo:[0,1] neg_hi:[1,1]
	ds_read2_b64 v[88:91], v110 offset0:10 offset1:11
	v_pk_add_f32 v[58:59], v[58:59], v[92:93] op_sel:[1,0] op_sel_hi:[0,1] neg_lo:[0,1] neg_hi:[1,1]
	v_pk_add_f32 v[92:93], v[94:95], v[104:105] neg_hi:[0,1]
	v_pk_add_f32 v[94:95], v[94:95], v[104:105] neg_lo:[0,1]
	s_mov_b32 s13, s12
	v_pk_mul_f32 v[98:99], v[92:93], v[94:95] op_sel:[0,0] op_sel_hi:[0,1]
	v_pk_fma_f32 v[98:99], v[92:93], v[94:95], v[98:99] op_sel:[1,1,0] op_sel_hi:[1,0,1] neg_hi:[0,1,0]
	ds_read2_b64 v[92:95], v110 offset0:8 offset1:9
	v_pk_add_f32 v[56:57], v[56:57], v[98:99] op_sel:[1,0] op_sel_hi:[0,1] neg_lo:[0,1] neg_hi:[1,1]
	s_waitcnt lgkmcnt(1)
	v_pk_add_f32 v[98:99], v[80:81], v[90:91] neg_hi:[0,1]
	v_pk_add_f32 v[80:81], v[80:81], v[90:91] neg_lo:[0,1]
	s_add_u32 s2, s2, 0x2000000
	v_pk_mul_f32 v[90:91], v[98:99], v[80:81] op_sel:[0,0] op_sel_hi:[0,1]
	v_pk_fma_f32 v[90:91], v[98:99], v[80:81], v[90:91] op_sel:[1,1,0] op_sel_hi:[1,0,1] neg_hi:[0,1,0]
	v_pk_add_f32 v[80:81], v[82:83], v[88:89] neg_hi:[0,1]
	v_pk_add_f32 v[82:83], v[82:83], v[88:89] neg_lo:[0,1]
	s_addc_u32 s3, s3, 0
	v_pk_mul_f32 v[88:89], v[80:81], v[82:83] op_sel:[0,0] op_sel_hi:[0,1]
	v_pk_fma_f32 v[88:89], v[80:81], v[82:83], v[88:89] op_sel:[1,1,0] op_sel_hi:[1,0,1] neg_hi:[0,1,0]
	s_waitcnt lgkmcnt(0)
	v_pk_add_f32 v[80:81], v[86:87], v[94:95] neg_lo:[0,1]
	v_pk_add_f32 v[54:55], v[54:55], v[90:91] op_sel:[1,0] op_sel_hi:[0,1] neg_lo:[0,1] neg_hi:[1,1]
	s_load_dwordx2 s[0:1], s[0:1], 0x8
	v_pk_add_f32 v[88:89], v[52:53], v[88:89] op_sel:[1,0] op_sel_hi:[0,1] neg_lo:[0,1] neg_hi:[1,1]
	v_pk_add_f32 v[52:53], v[86:87], v[94:95] neg_hi:[0,1]
	s_nop 0
	v_pk_mul_f32 v[82:83], v[52:53], v[80:81] op_sel:[0,0] op_sel_hi:[0,1]
	v_pk_fma_f32 v[82:83], v[52:53], v[80:81], v[82:83] op_sel:[1,1,0] op_sel_hi:[1,0,1] neg_hi:[0,1,0]
	v_pk_add_f32 v[80:81], v[84:85], v[92:93] neg_hi:[0,1]
	s_nop 0
	v_pk_add_f32 v[86:87], v[50:51], v[82:83] op_sel:[1,0] op_sel_hi:[0,1] neg_lo:[0,1] neg_hi:[1,1]
	ds_read2_b64 v[50:53], v110 offset0:6 offset1:7
	v_pk_add_f32 v[82:83], v[84:85], v[92:93] neg_lo:[0,1]
	s_nop 0
	v_pk_mul_f32 v[84:85], v[80:81], v[82:83] op_sel:[0,0] op_sel_hi:[0,1]
	v_pk_fma_f32 v[84:85], v[80:81], v[82:83], v[84:85] op_sel:[1,1,0] op_sel_hi:[1,0,1] neg_hi:[0,1,0]
	ds_read2_b64 v[80:83], v110 offset0:4 offset1:5
	v_pk_add_f32 v[84:85], v[48:49], v[84:85] op_sel:[1,0] op_sel_hi:[0,1] neg_lo:[0,1] neg_hi:[1,1]
	s_waitcnt lgkmcnt(0)
	v_pk_add_f32 v[48:49], v[72:73], v[52:53] neg_hi:[0,1]
	v_pk_add_f32 v[52:53], v[72:73], v[52:53] neg_lo:[0,1]
	s_nop 0
	v_pk_mul_f32 v[72:73], v[48:49], v[52:53] op_sel:[0,0] op_sel_hi:[0,1]
	v_pk_fma_f32 v[72:73], v[48:49], v[52:53], v[72:73] op_sel:[1,1,0] op_sel_hi:[1,0,1] neg_hi:[0,1,0]
	v_pk_add_f32 v[48:49], v[74:75], v[50:51] neg_lo:[0,1]
	s_nop 0
	v_pk_add_f32 v[52:53], v[46:47], v[72:73] op_sel:[1,0] op_sel_hi:[0,1] neg_lo:[0,1] neg_hi:[1,1]
	v_pk_add_f32 v[46:47], v[74:75], v[50:51] neg_hi:[0,1]
	s_nop 0
	v_pk_mul_f32 v[50:51], v[46:47], v[48:49] op_sel:[0,0] op_sel_hi:[0,1]
	v_pk_fma_f32 v[50:51], v[46:47], v[48:49], v[50:51] op_sel:[1,1,0] op_sel_hi:[1,0,1] neg_hi:[0,1,0]
	v_pk_add_f32 v[46:47], v[76:77], v[82:83] neg_lo:[0,1]
	s_nop 0
	v_pk_add_f32 v[50:51], v[44:45], v[50:51] op_sel:[1,0] op_sel_hi:[0,1] neg_lo:[0,1] neg_hi:[1,1]
	v_pk_add_f32 v[44:45], v[76:77], v[82:83] neg_hi:[0,1]
	s_nop 0
	v_pk_mul_f32 v[48:49], v[44:45], v[46:47] op_sel:[0,0] op_sel_hi:[0,1]
	v_pk_fma_f32 v[48:49], v[44:45], v[46:47], v[48:49] op_sel:[1,1,0] op_sel_hi:[1,0,1] neg_hi:[0,1,0]
	v_pk_add_f32 v[46:47], v[78:79], v[80:81] neg_hi:[0,1]
	s_nop 0
	v_pk_add_f32 v[72:73], v[42:43], v[48:49] op_sel:[1,0] op_sel_hi:[0,1] neg_lo:[0,1] neg_hi:[1,1]
	ds_read2_b64 v[42:45], v110 offset0:2 offset1:3
	v_pk_add_f32 v[48:49], v[78:79], v[80:81] neg_lo:[0,1]
	s_nop 0
	v_pk_mul_f32 v[74:75], v[46:47], v[48:49] op_sel:[0,0] op_sel_hi:[0,1]
	v_pk_fma_f32 v[74:75], v[46:47], v[48:49], v[74:75] op_sel:[1,1,0] op_sel_hi:[1,0,1] neg_hi:[0,1,0]
	ds_read2_b64 v[46:49], v110 offset1:1
	v_pk_add_f32 v[40:41], v[40:41], v[74:75] op_sel:[1,0] op_sel_hi:[0,1] neg_lo:[0,1] neg_hi:[1,1]
	s_waitcnt lgkmcnt(1)
	v_pk_add_f32 v[74:75], v[64:65], v[44:45] neg_hi:[0,1]
	v_pk_add_f32 v[44:45], v[64:65], v[44:45] neg_lo:[0,1]
	s_waitcnt lgkmcnt(0)
	v_pk_mul_f32 v[64:65], v[74:75], v[44:45] op_sel:[0,0] op_sel_hi:[0,1]
	v_pk_fma_f32 v[64:65], v[74:75], v[44:45], v[64:65] op_sel:[1,1,0] op_sel_hi:[1,0,1] neg_hi:[0,1,0]
	v_pk_add_f32 v[44:45], v[66:67], v[42:43] neg_hi:[0,1]
	v_pk_add_f32 v[42:43], v[66:67], v[42:43] neg_lo:[0,1]
	s_barrier
	v_pk_add_f32 v[38:39], v[38:39], v[64:65] op_sel:[1,0] op_sel_hi:[0,1] neg_lo:[0,1] neg_hi:[1,1]
	v_pk_mul_f32 v[64:65], v[44:45], v[42:43] op_sel:[0,0] op_sel_hi:[0,1]
	v_pk_fma_f32 v[64:65], v[44:45], v[42:43], v[64:65] op_sel:[1,1,0] op_sel_hi:[1,0,1] neg_hi:[0,1,0]
	v_pk_add_f32 v[42:43], v[68:69], v[48:49] neg_hi:[0,1]
	v_pk_add_f32 v[44:45], v[68:69], v[48:49] neg_lo:[0,1]
	s_nop 0
	v_pk_mul_f32 v[48:49], v[42:43], v[44:45] op_sel:[0,0] op_sel_hi:[0,1]
	v_pk_fma_f32 v[48:49], v[42:43], v[44:45], v[48:49] op_sel:[1,1,0] op_sel_hi:[1,0,1] neg_hi:[0,1,0]
	v_pk_add_f32 v[42:43], v[70:71], v[46:47] neg_hi:[0,1]
	v_pk_add_f32 v[44:45], v[70:71], v[46:47] neg_lo:[0,1]
	v_pk_add_f32 v[36:37], v[36:37], v[64:65] op_sel:[1,0] op_sel_hi:[0,1] neg_lo:[0,1] neg_hi:[1,1]
	s_nop 0
	v_pk_mul_f32 v[46:47], v[42:43], v[44:45] op_sel:[0,0] op_sel_hi:[0,1]
	v_pk_fma_f32 v[46:47], v[42:43], v[44:45], v[46:47] op_sel:[1,1,0] op_sel_hi:[1,0,1] neg_hi:[0,1,0]
	v_pk_add_f32 v[42:43], v[62:63], v[52:53]
	v_pk_add_f32 v[32:33], v[32:33], v[46:47] op_sel:[1,0] op_sel_hi:[0,1] neg_lo:[0,1] neg_hi:[1,1]
	v_pk_add_f32 v[44:45], v[62:63], v[52:53] neg_lo:[0,1] neg_hi:[0,1]
	v_pk_add_f32 v[46:47], v[54:55], v[38:39]
	v_pk_add_f32 v[38:39], v[54:55], v[38:39] neg_lo:[0,1] neg_hi:[0,1]
	v_pk_add_f32 v[34:35], v[34:35], v[48:49] op_sel:[1,0] op_sel_hi:[0,1] neg_lo:[0,1] neg_hi:[1,1]
	v_pk_add_f32 v[48:49], v[42:43], v[46:47]
	v_pk_add_f32 v[42:43], v[42:43], v[46:47] neg_lo:[0,1] neg_hi:[0,1]
	v_pk_add_f32 v[46:47], v[44:45], v[38:39] op_sel:[0,1] op_sel_hi:[1,0] neg_hi:[0,1]
	v_pk_add_f32 v[38:39], v[44:45], v[38:39] op_sel:[0,1] op_sel_hi:[1,0] neg_lo:[0,1]
	v_pk_add_f32 v[44:45], v[60:61], v[50:51]
	v_pk_add_f32 v[50:51], v[60:61], v[50:51] neg_lo:[0,1] neg_hi:[0,1]
	v_pk_add_f32 v[52:53], v[88:89], v[36:37]
	v_pk_add_f32 v[36:37], v[88:89], v[36:37] neg_lo:[0,1] neg_hi:[0,1]
	v_pk_add_f32 v[54:55], v[44:45], v[52:53]
	v_pk_add_f32 v[44:45], v[44:45], v[52:53] neg_lo:[0,1] neg_hi:[0,1]
	v_pk_add_f32 v[52:53], v[50:51], v[36:37] op_sel:[0,1] op_sel_hi:[1,0] neg_hi:[0,1]
	v_pk_add_f32 v[36:37], v[50:51], v[36:37] op_sel:[0,1] op_sel_hi:[1,0] neg_lo:[0,1]
	v_pk_add_f32 v[50:51], v[58:59], v[72:73]
	v_pk_add_f32 v[58:59], v[58:59], v[72:73] neg_lo:[0,1] neg_hi:[0,1]
	v_pk_add_f32 v[60:61], v[86:87], v[34:35]
	v_pk_add_f32 v[34:35], v[86:87], v[34:35] neg_lo:[0,1] neg_hi:[0,1]
	v_pk_add_f32 v[62:63], v[50:51], v[60:61]
	v_pk_add_f32 v[50:51], v[50:51], v[60:61] neg_lo:[0,1] neg_hi:[0,1]
	v_pk_add_f32 v[60:61], v[58:59], v[34:35] op_sel:[0,1] op_sel_hi:[1,0] neg_hi:[0,1]
	v_pk_add_f32 v[34:35], v[58:59], v[34:35] op_sel:[0,1] op_sel_hi:[1,0] neg_lo:[0,1]
	v_pk_add_f32 v[58:59], v[56:57], v[40:41]
	v_pk_add_f32 v[40:41], v[56:57], v[40:41] neg_lo:[0,1] neg_hi:[0,1]
	v_pk_add_f32 v[56:57], v[84:85], v[32:33]
	v_pk_add_f32 v[32:33], v[84:85], v[32:33] neg_lo:[0,1] neg_hi:[0,1]
	v_pk_add_f32 v[64:65], v[58:59], v[56:57]
	v_pk_add_f32 v[56:57], v[58:59], v[56:57] neg_lo:[0,1] neg_hi:[0,1]
	v_pk_add_f32 v[58:59], v[40:41], v[32:33] op_sel:[0,1] op_sel_hi:[1,0] neg_hi:[0,1]
	v_pk_add_f32 v[32:33], v[40:41], v[32:33] op_sel:[0,1] op_sel_hi:[1,0] neg_lo:[0,1]
	v_pk_mul_f32 v[40:41], v[52:53], s[6:7] op_sel:[0,0] op_sel_hi:[0,1]
	v_pk_fma_f32 v[40:41], v[52:53], s[6:7], v[40:41] op_sel:[1,1,0] op_sel_hi:[1,0,1] neg_lo:[0,1,0]
	v_pk_mul_f32 v[52:53], v[36:37], s[10:11] op_sel:[0,0] op_sel_hi:[0,1]
	v_pk_fma_f32 v[52:53], v[36:37], s[10:11], v[52:53] op_sel:[1,1,0] op_sel_hi:[1,0,1] neg_lo:[0,1,0]
	v_pk_add_f32 v[36:37], v[60:61], v[60:61] op_sel:[0,1] op_sel_hi:[1,0] neg_hi:[0,1]
	v_pk_add_f32 v[44:45], v[44:45], v[44:45] op_sel:[0,1] op_sel_hi:[1,0] neg_hi:[0,1]
	s_nop 0
	v_pk_mul_f32 v[60:61], v[58:59], s[10:11] op_sel:[0,0] op_sel_hi:[0,1]
	v_pk_fma_f32 v[60:61], v[58:59], s[10:11], v[60:61] op_sel:[1,1,0] op_sel_hi:[1,0,1] neg_lo:[0,1,0]
	v_pk_mul_f32 v[58:59], v[32:33], s[14:15] op_sel:[0,0] op_sel_hi:[0,1]
	v_pk_fma_f32 v[58:59], v[32:33], s[14:15], v[58:59] op_sel:[1,1,0] op_sel_hi:[1,0,1] neg_lo:[0,1,0]
	v_pk_add_f32 v[32:33], v[48:49], v[62:63]
	v_pk_mul_f32 v[36:37], v[36:37], s[8:9]
	v_pk_add_f32 v[48:49], v[48:49], v[62:63] neg_lo:[0,1] neg_hi:[0,1]
	v_pk_add_f32 v[62:63], v[54:55], v[64:65]
	v_pk_add_f32 v[54:55], v[54:55], v[64:65] neg_lo:[0,1] neg_hi:[0,1]
	v_pk_mul_f32 v[44:45], v[44:45], s[8:9]
	v_pk_add_f32 v[34:35], v[34:35], v[34:35] op_sel:[0,1] op_sel_hi:[1,0] neg_lo:[0,1]
	v_pk_add_f32 v[56:57], v[56:57], v[56:57] op_sel:[0,1] op_sel_hi:[1,0] neg_lo:[0,1]
	v_pk_add_f32 v[64:65], v[32:33], v[62:63]
	v_pk_add_f32 v[32:33], v[32:33], v[62:63] neg_lo:[0,1] neg_hi:[0,1]
	v_pk_add_f32 v[62:63], v[48:49], v[54:55] op_sel:[0,1] op_sel_hi:[1,0] neg_hi:[0,1]
	v_pk_add_f32 v[48:49], v[48:49], v[54:55] op_sel:[0,1] op_sel_hi:[1,0] neg_lo:[0,1]
	v_pk_add_f32 v[54:55], v[46:47], v[36:37]
	v_pk_add_f32 v[36:37], v[46:47], v[36:37] neg_lo:[0,1] neg_hi:[0,1]
	v_pk_add_f32 v[46:47], v[40:41], v[60:61]
	v_pk_add_f32 v[40:41], v[40:41], v[60:61] neg_lo:[0,1] neg_hi:[0,1]
	v_pk_mul_f32 v[34:35], v[34:35], s[12:13]
	v_pk_mul_f32 v[56:57], v[56:57], s[12:13]
	v_pk_add_f32 v[60:61], v[54:55], v[46:47]
	v_pk_add_f32 v[46:47], v[54:55], v[46:47] neg_lo:[0,1] neg_hi:[0,1]
	v_pk_add_f32 v[54:55], v[36:37], v[40:41] op_sel:[0,1] op_sel_hi:[1,0] neg_hi:[0,1]
	v_pk_add_f32 v[36:37], v[36:37], v[40:41] op_sel:[0,1] op_sel_hi:[1,0] neg_lo:[0,1]
	v_pk_add_f32 v[40:41], v[42:43], v[50:51] op_sel:[0,1] op_sel_hi:[1,0] neg_hi:[0,1]
	v_pk_add_f32 v[42:43], v[42:43], v[50:51] op_sel:[0,1] op_sel_hi:[1,0] neg_lo:[0,1]
	v_pk_add_f32 v[50:51], v[44:45], v[56:57]
	v_pk_add_f32 v[44:45], v[44:45], v[56:57] neg_lo:[0,1] neg_hi:[0,1]
	v_pk_add_f32 v[56:57], v[50:51], v[40:41]
	v_pk_add_f32 v[40:41], v[40:41], v[50:51] neg_lo:[0,1] neg_hi:[0,1]
	v_pk_add_f32 v[50:51], v[42:43], v[44:45] op_sel:[0,1] op_sel_hi:[1,0] neg_hi:[0,1]
	v_pk_add_f32 v[42:43], v[42:43], v[44:45] op_sel:[0,1] op_sel_hi:[1,0] neg_lo:[0,1]
	v_pk_add_f32 v[44:45], v[38:39], v[34:35]
	v_pk_add_f32 v[34:35], v[38:39], v[34:35] neg_lo:[0,1] neg_hi:[0,1]
	v_pk_add_f32 v[38:39], v[52:53], v[58:59]
	v_pk_add_f32 v[52:53], v[52:53], v[58:59] neg_lo:[0,1] neg_hi:[0,1]
	v_pk_add_f32 v[58:59], v[44:45], v[38:39]
	v_pk_add_f32 v[38:39], v[44:45], v[38:39] neg_lo:[0,1] neg_hi:[0,1]
	v_pk_add_f32 v[44:45], v[34:35], v[52:53] op_sel:[0,1] op_sel_hi:[1,0] neg_hi:[0,1]
	v_pk_add_f32 v[34:35], v[34:35], v[52:53] op_sel:[0,1] op_sel_hi:[1,0] neg_lo:[0,1]
	v_pk_mul_f32 v[52:53], v[60:61], v[30:31] op_sel:[0,0] op_sel_hi:[0,1]
	v_pk_fma_f32 v[52:53], v[60:61], v[30:31], v[52:53] op_sel:[1,1,0] op_sel_hi:[1,0,1] neg_lo:[0,1,0]
	v_pk_mul_f32 v[30:31], v[56:57], v[28:29] op_sel:[0,0] op_sel_hi:[0,1]
	v_pk_fma_f32 v[30:31], v[56:57], v[28:29], v[30:31] op_sel:[1,1,0] op_sel_hi:[1,0,1] neg_lo:[0,1,0]
	v_pk_mul_f32 v[28:29], v[58:59], v[26:27] op_sel:[0,0] op_sel_hi:[0,1]
	v_pk_fma_f32 v[28:29], v[58:59], v[26:27], v[28:29] op_sel:[1,1,0] op_sel_hi:[1,0,1] neg_lo:[0,1,0]
	v_pk_mul_f32 v[26:27], v[62:63], v[24:25] op_sel:[0,0] op_sel_hi:[0,1]
	v_pk_fma_f32 v[26:27], v[62:63], v[24:25], v[26:27] op_sel:[1,1,0] op_sel_hi:[1,0,1] neg_lo:[0,1,0]
	v_pk_mul_f32 v[24:25], v[54:55], v[20:21] op_sel:[0,0] op_sel_hi:[0,1]
	v_pk_fma_f32 v[24:25], v[54:55], v[20:21], v[24:25] op_sel:[1,1,0] op_sel_hi:[1,0,1] neg_lo:[0,1,0]
	v_pk_mul_f32 v[20:21], v[50:51], v[16:17] op_sel:[0,0] op_sel_hi:[0,1]
	v_pk_fma_f32 v[20:21], v[50:51], v[16:17], v[20:21] op_sel:[1,1,0] op_sel_hi:[1,0,1] neg_lo:[0,1,0]
	s_nop 0
	v_pk_mul_f32 v[16:17], v[44:45], v[10:11] op_sel:[0,0] op_sel_hi:[0,1]
	v_pk_fma_f32 v[16:17], v[44:45], v[10:11], v[16:17] op_sel:[1,1,0] op_sel_hi:[1,0,1] neg_lo:[0,1,0]
	v_pk_mul_f32 v[10:11], v[32:33], v[22:23] op_sel:[0,0] op_sel_hi:[0,1]
	v_pk_fma_f32 v[10:11], v[32:33], v[22:23], v[10:11] op_sel:[1,1,0] op_sel_hi:[1,0,1] neg_lo:[0,1,0]
	ds_write_b64 v1, v[10:11] offset:17472
	v_pk_mul_f32 v[10:11], v[46:47], v[18:19] op_sel:[0,0] op_sel_hi:[0,1]
	v_pk_fma_f32 v[10:11], v[46:47], v[18:19], v[10:11] op_sel:[1,1,0] op_sel_hi:[1,0,1] neg_lo:[0,1,0]
	ds_write_b64 v1, v[10:11] offset:19656
	v_pk_mul_f32 v[10:11], v[40:41], v[12:13] op_sel:[0,0] op_sel_hi:[0,1]
	v_pk_fma_f32 v[10:11], v[40:41], v[12:13], v[10:11] op_sel:[1,1,0] op_sel_hi:[1,0,1] neg_lo:[0,1,0]
	ds_write_b64 v1, v[10:11] offset:21840
	v_pk_mul_f32 v[10:11], v[38:39], v[14:15] op_sel:[0,0] op_sel_hi:[0,1]
	v_pk_fma_f32 v[10:11], v[38:39], v[14:15], v[10:11] op_sel:[1,1,0] op_sel_hi:[1,0,1] neg_lo:[0,1,0]
	ds_write_b64 v1, v[10:11] offset:24024
	v_pk_mul_f32 v[10:11], v[48:49], v[6:7] op_sel:[0,0] op_sel_hi:[0,1]
	v_pk_fma_f32 v[10:11], v[48:49], v[6:7], v[10:11] op_sel:[1,1,0] op_sel_hi:[1,0,1] neg_lo:[0,1,0]
	v_pk_mul_f32 v[6:7], v[36:37], v[8:9] op_sel:[0,0] op_sel_hi:[0,1]
	v_pk_fma_f32 v[6:7], v[36:37], v[8:9], v[6:7] op_sel:[1,1,0] op_sel_hi:[1,0,1] neg_lo:[0,1,0]
	ds_write_b64 v1, v[6:7] offset:28392
	v_pk_mul_f32 v[6:7], v[42:43], v[4:5] op_sel:[0,0] op_sel_hi:[0,1]
	v_pk_fma_f32 v[6:7], v[42:43], v[4:5], v[6:7] op_sel:[1,1,0] op_sel_hi:[1,0,1] neg_lo:[0,1,0]
	v_pk_mul_f32 v[4:5], v[34:35], v[2:3] op_sel:[0,0] op_sel_hi:[0,1]
	v_pk_fma_f32 v[4:5], v[34:35], v[2:3], v[4:5] op_sel:[1,1,0] op_sel_hi:[1,0,1] neg_lo:[0,1,0]
	ds_write_b64 v1, v[64:65]
	ds_write_b64 v1, v[52:53] offset:2184
	ds_write_b64 v1, v[30:31] offset:4368
	ds_write_b64 v1, v[28:29] offset:6552
	ds_write_b64 v1, v[26:27] offset:8736
	ds_write_b64 v1, v[24:25] offset:10920
	ds_write_b64 v1, v[20:21] offset:13104
	ds_write_b64 v1, v[16:17] offset:15288
	ds_write_b64 v1, v[10:11] offset:26208
	ds_write_b64 v1, v[6:7] offset:30576
	ds_write_b64 v1, v[4:5] offset:32760
	s_waitcnt lgkmcnt(0)
	s_barrier
	ds_read2_b64 v[2:5], v96 offset1:16
	ds_read2_b64 v[6:9], v96 offset0:32 offset1:48
	ds_read2_b64 v[10:13], v96 offset0:64 offset1:80
	ds_read2_b64 v[14:17], v96 offset0:128 offset1:144
	ds_read2_b64 v[18:21], v96 offset0:96 offset1:112
	ds_read2_b64 v[22:25], v96 offset0:192 offset1:208
	ds_read2_b64 v[26:29], v96 offset0:160 offset1:176
	ds_read2_b64 v[30:33], v96 offset0:224 offset1:240
	s_waitcnt lgkmcnt(4)
	v_pk_add_f32 v[34:35], v[2:3], v[14:15]
	v_pk_add_f32 v[2:3], v[2:3], v[14:15] neg_lo:[0,1] neg_hi:[0,1]
	s_waitcnt lgkmcnt(2)
	v_pk_add_f32 v[14:15], v[10:11], v[22:23]
	v_pk_add_f32 v[10:11], v[10:11], v[22:23] neg_lo:[0,1] neg_hi:[0,1]
	v_pk_add_f32 v[22:23], v[34:35], v[14:15]
	v_pk_add_f32 v[14:15], v[34:35], v[14:15] neg_lo:[0,1] neg_hi:[0,1]
	v_pk_add_f32 v[34:35], v[2:3], v[10:11] op_sel:[0,1] op_sel_hi:[1,0] neg_hi:[0,1]
	v_pk_add_f32 v[2:3], v[2:3], v[10:11] op_sel:[0,1] op_sel_hi:[1,0] neg_lo:[0,1]
	v_pk_add_f32 v[10:11], v[4:5], v[16:17]
	v_pk_add_f32 v[4:5], v[4:5], v[16:17] neg_lo:[0,1] neg_hi:[0,1]
	v_pk_add_f32 v[16:17], v[12:13], v[24:25]
	v_pk_add_f32 v[12:13], v[12:13], v[24:25] neg_lo:[0,1] neg_hi:[0,1]
	v_pk_add_f32 v[24:25], v[10:11], v[16:17]
	v_pk_add_f32 v[10:11], v[10:11], v[16:17] neg_lo:[0,1] neg_hi:[0,1]
	v_pk_add_f32 v[16:17], v[4:5], v[12:13] op_sel:[0,1] op_sel_hi:[1,0] neg_hi:[0,1]
	v_pk_add_f32 v[4:5], v[4:5], v[12:13] op_sel:[0,1] op_sel_hi:[1,0] neg_lo:[0,1]
	s_waitcnt lgkmcnt(1)
	v_pk_add_f32 v[12:13], v[6:7], v[26:27]
	v_pk_add_f32 v[6:7], v[6:7], v[26:27] neg_lo:[0,1] neg_hi:[0,1]
	s_waitcnt lgkmcnt(0)
	v_pk_add_f32 v[26:27], v[18:19], v[30:31]
	v_pk_add_f32 v[18:19], v[18:19], v[30:31] neg_lo:[0,1] neg_hi:[0,1]
	v_pk_add_f32 v[30:31], v[12:13], v[26:27]
	v_pk_add_f32 v[12:13], v[12:13], v[26:27] neg_lo:[0,1] neg_hi:[0,1]
	v_pk_add_f32 v[26:27], v[6:7], v[18:19] op_sel:[0,1] op_sel_hi:[1,0] neg_hi:[0,1]
	v_pk_add_f32 v[6:7], v[6:7], v[18:19] op_sel:[0,1] op_sel_hi:[1,0] neg_lo:[0,1]
	v_pk_add_f32 v[18:19], v[8:9], v[28:29]
	v_pk_add_f32 v[8:9], v[8:9], v[28:29] neg_lo:[0,1] neg_hi:[0,1]
	v_pk_add_f32 v[28:29], v[20:21], v[32:33]
	v_pk_add_f32 v[20:21], v[20:21], v[32:33] neg_lo:[0,1] neg_hi:[0,1]
	v_pk_add_f32 v[32:33], v[18:19], v[28:29]
	v_pk_add_f32 v[18:19], v[18:19], v[28:29] neg_lo:[0,1] neg_hi:[0,1]
	v_pk_add_f32 v[28:29], v[8:9], v[20:21] op_sel:[0,1] op_sel_hi:[1,0] neg_hi:[0,1]
	v_pk_add_f32 v[8:9], v[8:9], v[20:21] op_sel:[0,1] op_sel_hi:[1,0] neg_lo:[0,1]
	v_pk_mul_f32 v[20:21], v[16:17], s[6:7] op_sel:[0,0] op_sel_hi:[0,1]
	v_pk_fma_f32 v[20:21], v[16:17], s[6:7], v[20:21] op_sel:[1,1,0] op_sel_hi:[1,0,1] neg_lo:[0,1,0]
	v_pk_mul_f32 v[16:17], v[4:5], s[10:11] op_sel:[0,0] op_sel_hi:[0,1]
	v_pk_fma_f32 v[16:17], v[4:5], s[10:11], v[16:17] op_sel:[1,1,0] op_sel_hi:[1,0,1] neg_lo:[0,1,0]
	v_pk_add_f32 v[4:5], v[26:27], v[26:27] op_sel:[0,1] op_sel_hi:[1,0] neg_hi:[0,1]
	v_pk_add_f32 v[10:11], v[10:11], v[10:11] op_sel:[0,1] op_sel_hi:[1,0] neg_hi:[0,1]
	s_nop 0
	v_pk_mul_f32 v[26:27], v[28:29], s[10:11] op_sel:[0,0] op_sel_hi:[0,1]
	v_pk_fma_f32 v[26:27], v[28:29], s[10:11], v[26:27] op_sel:[1,1,0] op_sel_hi:[1,0,1] neg_lo:[0,1,0]
	v_pk_mul_f32 v[28:29], v[8:9], s[14:15] op_sel:[0,0] op_sel_hi:[0,1]
	v_pk_fma_f32 v[28:29], v[8:9], s[14:15], v[28:29] op_sel:[1,1,0] op_sel_hi:[1,0,1] neg_lo:[0,1,0]
	v_pk_add_f32 v[8:9], v[22:23], v[30:31]
	v_pk_mul_f32 v[4:5], v[4:5], s[8:9]
	v_pk_add_f32 v[22:23], v[22:23], v[30:31] neg_lo:[0,1] neg_hi:[0,1]
	v_pk_add_f32 v[30:31], v[24:25], v[32:33]
	v_pk_add_f32 v[24:25], v[24:25], v[32:33] neg_lo:[0,1] neg_hi:[0,1]
	v_pk_add_f32 v[18:19], v[18:19], v[18:19] op_sel:[0,1] op_sel_hi:[1,0] neg_lo:[0,1]
	v_pk_add_f32 v[32:33], v[8:9], v[30:31]
	v_pk_add_f32 v[30:31], v[8:9], v[30:31] neg_lo:[0,1] neg_hi:[0,1]
	v_pk_add_f32 v[36:37], v[22:23], v[24:25] op_sel:[0,1] op_sel_hi:[1,0] neg_hi:[0,1]
	v_pk_add_f32 v[22:23], v[22:23], v[24:25] op_sel:[0,1] op_sel_hi:[1,0] neg_lo:[0,1]
	v_pk_add_f32 v[8:9], v[34:35], v[4:5]
	v_pk_add_f32 v[4:5], v[34:35], v[4:5] neg_lo:[0,1] neg_hi:[0,1]
	v_pk_add_f32 v[24:25], v[20:21], v[26:27]
	v_pk_add_f32 v[20:21], v[20:21], v[26:27] neg_lo:[0,1] neg_hi:[0,1]
	v_pk_mul_f32 v[10:11], v[10:11], s[8:9]
	v_pk_add_f32 v[6:7], v[6:7], v[6:7] op_sel:[0,1] op_sel_hi:[1,0] neg_lo:[0,1]
	v_pk_mul_f32 v[18:19], v[18:19], s[12:13]
	v_pk_add_f32 v[26:27], v[8:9], v[24:25]
	v_pk_add_f32 v[24:25], v[8:9], v[24:25] neg_lo:[0,1] neg_hi:[0,1]
	v_pk_add_f32 v[34:35], v[4:5], v[20:21] op_sel:[0,1] op_sel_hi:[1,0] neg_hi:[0,1]
	v_pk_add_f32 v[20:21], v[4:5], v[20:21] op_sel:[0,1] op_sel_hi:[1,0] neg_lo:[0,1]
	v_pk_add_f32 v[4:5], v[14:15], v[12:13] op_sel:[0,1] op_sel_hi:[1,0] neg_hi:[0,1]
	v_pk_add_f32 v[8:9], v[14:15], v[12:13] op_sel:[0,1] op_sel_hi:[1,0] neg_lo:[0,1]
	v_pk_add_f32 v[12:13], v[10:11], v[18:19]
	v_pk_mul_f32 v[6:7], v[6:7], s[12:13]
	v_pk_add_f32 v[10:11], v[10:11], v[18:19] neg_lo:[0,1] neg_hi:[0,1]
	v_pk_add_f32 v[14:15], v[12:13], v[4:5]
	v_pk_add_f32 v[12:13], v[4:5], v[12:13] neg_lo:[0,1] neg_hi:[0,1]
	v_pk_add_f32 v[4:5], v[2:3], v[6:7]
	v_pk_add_f32 v[2:3], v[2:3], v[6:7] neg_lo:[0,1] neg_hi:[0,1]
	v_mov_b32_e32 v1, v0
	v_pk_add_f32 v[18:19], v[8:9], v[10:11] op_sel:[0,1] op_sel_hi:[1,0] neg_hi:[0,1]
	v_pk_add_f32 v[10:11], v[8:9], v[10:11] op_sel:[0,1] op_sel_hi:[1,0] neg_lo:[0,1]
	v_pk_add_f32 v[8:9], v[16:17], v[28:29] neg_lo:[0,1] neg_hi:[0,1]
	v_pk_add_f32 v[6:7], v[16:17], v[28:29]
	v_pk_add_f32 v[38:39], v[2:3], v[8:9] op_sel:[0,1] op_sel_hi:[1,0] neg_hi:[0,1]
	v_pk_add_f32 v[40:41], v[2:3], v[8:9] op_sel:[0,1] op_sel_hi:[1,0] neg_lo:[0,1]
	v_ashrrev_i32_e32 v2, 4, v1
	v_lshlrev_b32_e32 v44, 3, v2
	v_add_u32_e32 v45, 0x8800, v44
	v_and_b32_e32 v1, 15, v1
	v_pk_add_f32 v[16:17], v[4:5], v[6:7]
	v_pk_add_f32 v[28:29], v[4:5], v[6:7] neg_lo:[0,1] neg_hi:[0,1]
	ds_read2_b64 v[2:5], v45 offset0:16 offset1:32
	v_mad_u32_u24 v1, v1, s5, v44
	ds_read2_b64 v[6:9], v45 offset0:48 offset1:64
	s_waitcnt lgkmcnt(1)
	v_pk_mul_f32 v[42:43], v[26:27], v[2:3] op_sel:[0,0] op_sel_hi:[0,1]
	v_pk_fma_f32 v[42:43], v[26:27], v[2:3], v[42:43] op_sel:[1,1,0] op_sel_hi:[1,0,1] neg_lo:[0,1,0]
	v_pk_mul_f32 v[26:27], v[14:15], v[4:5] op_sel:[0,0] op_sel_hi:[0,1]
	v_pk_fma_f32 v[26:27], v[14:15], v[4:5], v[26:27] op_sel:[1,1,0] op_sel_hi:[1,0,1] neg_lo:[0,1,0]
	s_waitcnt lgkmcnt(0)
	v_pk_mul_f32 v[14:15], v[16:17], v[6:7] op_sel:[0,0] op_sel_hi:[0,1]
	v_pk_fma_f32 v[14:15], v[16:17], v[6:7], v[14:15] op_sel:[1,1,0] op_sel_hi:[1,0,1] neg_lo:[0,1,0]
	ds_write2_b64 v1, v[26:27], v[14:15] offset0:32 offset1:48
	v_pk_mul_f32 v[14:15], v[36:37], v[8:9] op_sel:[0,0] op_sel_hi:[0,1]
	v_pk_fma_f32 v[14:15], v[36:37], v[8:9], v[14:15] op_sel:[1,1,0] op_sel_hi:[1,0,1] neg_lo:[0,1,0]
	ds_read2_b64 v[2:5], v45 offset0:80 offset1:96
	s_waitcnt lgkmcnt(0)
	v_pk_mul_f32 v[16:17], v[34:35], v[2:3] op_sel:[0,0] op_sel_hi:[0,1]
	v_pk_fma_f32 v[16:17], v[34:35], v[2:3], v[16:17] op_sel:[1,1,0] op_sel_hi:[1,0,1] neg_lo:[0,1,0]
	ds_write2_b64 v1, v[14:15], v[16:17] offset0:64 offset1:80
	v_pk_mul_f32 v[14:15], v[18:19], v[4:5] op_sel:[0,0] op_sel_hi:[0,1]
	v_pk_fma_f32 v[14:15], v[18:19], v[4:5], v[14:15] op_sel:[1,1,0] op_sel_hi:[1,0,1] neg_lo:[0,1,0]
	ds_read2_b64 v[6:9], v45 offset0:112 offset1:128
	ds_read2_b64 v[2:5], v45 offset0:144 offset1:160
	s_waitcnt lgkmcnt(1)
	v_pk_mul_f32 v[16:17], v[38:39], v[6:7] op_sel:[0,0] op_sel_hi:[0,1]
	v_pk_fma_f32 v[16:17], v[38:39], v[6:7], v[16:17] op_sel:[1,1,0] op_sel_hi:[1,0,1] neg_lo:[0,1,0]
	ds_write2_b64 v1, v[14:15], v[16:17] offset0:96 offset1:112
	v_pk_mul_f32 v[14:15], v[30:31], v[8:9] op_sel:[0,0] op_sel_hi:[0,1]
	v_pk_fma_f32 v[14:15], v[30:31], v[8:9], v[14:15] op_sel:[1,1,0] op_sel_hi:[1,0,1] neg_lo:[0,1,0]
	ds_read2_b64 v[6:9], v45 offset0:176 offset1:192
	s_waitcnt lgkmcnt(2)
	v_pk_mul_f32 v[16:17], v[24:25], v[2:3] op_sel:[0,0] op_sel_hi:[0,1]
	v_pk_fma_f32 v[16:17], v[24:25], v[2:3], v[16:17] op_sel:[1,1,0] op_sel_hi:[1,0,1] neg_lo:[0,1,0]
	ds_write2_b64 v1, v[14:15], v[16:17] offset0:128 offset1:144
	v_pk_mul_f32 v[14:15], v[12:13], v[4:5] op_sel:[0,0] op_sel_hi:[0,1]
	v_pk_fma_f32 v[14:15], v[12:13], v[4:5], v[14:15] op_sel:[1,1,0] op_sel_hi:[1,0,1] neg_lo:[0,1,0]
	ds_read2_b64 v[2:5], v45 offset0:208 offset1:224
	s_waitcnt lgkmcnt(2)
	v_pk_mul_f32 v[12:13], v[28:29], v[6:7] op_sel:[0,0] op_sel_hi:[0,1]
	v_pk_fma_f32 v[12:13], v[28:29], v[6:7], v[12:13] op_sel:[1,1,0] op_sel_hi:[1,0,1] neg_lo:[0,1,0]
	ds_write2_b64 v1, v[32:33], v[42:43] offset1:16
	ds_write2_b64 v1, v[14:15], v[12:13] offset0:160 offset1:176
	ds_read_b64 v[6:7], v44 offset:36736
	v_pk_mul_f32 v[12:13], v[22:23], v[8:9] op_sel:[0,0] op_sel_hi:[0,1]
	v_pk_fma_f32 v[12:13], v[22:23], v[8:9], v[12:13] op_sel:[1,1,0] op_sel_hi:[1,0,1] neg_lo:[0,1,0]
	s_waitcnt lgkmcnt(3)
	v_pk_mul_f32 v[8:9], v[20:21], v[2:3] op_sel:[0,0] op_sel_hi:[0,1]
	v_pk_fma_f32 v[8:9], v[20:21], v[2:3], v[8:9] op_sel:[1,1,0] op_sel_hi:[1,0,1] neg_lo:[0,1,0]
	ds_write2_b64 v1, v[12:13], v[8:9] offset0:192 offset1:208
	v_pk_mul_f32 v[2:3], v[10:11], v[4:5] op_sel:[0,0] op_sel_hi:[0,1]
	v_pk_fma_f32 v[2:3], v[10:11], v[4:5], v[2:3] op_sel:[1,1,0] op_sel_hi:[1,0,1] neg_lo:[0,1,0]
	s_waitcnt lgkmcnt(1)
	v_pk_mul_f32 v[4:5], v[40:41], v[6:7] op_sel:[0,0] op_sel_hi:[0,1]
	v_pk_fma_f32 v[4:5], v[40:41], v[6:7], v[4:5] op_sel:[1,1,0] op_sel_hi:[1,0,1] neg_lo:[0,1,0]
	ds_write2_b64 v1, v[2:3], v[4:5] offset0:224 offset1:240
	v_mov_b32_e32 v1, v0
	s_waitcnt lgkmcnt(0)
	s_barrier
	v_mov_b32_e32 v53, 0
	v_and_b32_e32 v2, 15, v1
	v_and_b32_e32 v1, 0x1ffffff0, v1
	v_lshlrev_b32_e32 v1, 3, v1
	v_mad_u32_u24 v1, v2, s5, v1
	ds_read2_b64 v[2:5], v1 offset1:1
	ds_read2_b64 v[6:9], v1 offset0:2 offset1:3
	ds_read2_b64 v[10:13], v1 offset0:8 offset1:9
	ds_read2_b64 v[18:21], v1 offset0:4 offset1:5
	ds_read2_b64 v[22:25], v1 offset0:6 offset1:7
	ds_read2_b64 v[26:29], v1 offset0:12 offset1:13
	ds_read2_b64 v[30:33], v1 offset0:10 offset1:11
	ds_read2_b64 v[34:37], v1 offset0:14 offset1:15
	s_waitcnt lgkmcnt(5)
	v_pk_add_f32 v[14:15], v[2:3], v[10:11]
	v_pk_add_f32 v[2:3], v[2:3], v[10:11] neg_lo:[0,1] neg_hi:[0,1]
	s_waitcnt lgkmcnt(2)
	v_pk_add_f32 v[10:11], v[18:19], v[26:27]
	v_pk_add_f32 v[18:19], v[18:19], v[26:27] neg_lo:[0,1] neg_hi:[0,1]
	v_pk_add_f32 v[26:27], v[14:15], v[10:11]
	v_pk_add_f32 v[16:17], v[14:15], v[10:11] neg_lo:[0,1] neg_hi:[0,1]
	v_pk_add_f32 v[14:15], v[2:3], v[18:19] op_sel:[0,1] op_sel_hi:[1,0] neg_hi:[0,1]
	v_pk_add_f32 v[18:19], v[2:3], v[18:19] op_sel:[0,1] op_sel_hi:[1,0] neg_lo:[0,1]
	v_pk_add_f32 v[2:3], v[4:5], v[12:13]
	v_pk_add_f32 v[10:11], v[20:21], v[28:29]
	v_pk_add_f32 v[4:5], v[4:5], v[12:13] neg_lo:[0,1] neg_hi:[0,1]
	v_pk_add_f32 v[12:13], v[20:21], v[28:29] neg_lo:[0,1] neg_hi:[0,1]
	v_pk_add_f32 v[28:29], v[2:3], v[10:11]
	v_pk_add_f32 v[2:3], v[2:3], v[10:11] neg_lo:[0,1] neg_hi:[0,1]
	v_pk_add_f32 v[10:11], v[4:5], v[12:13] op_sel:[0,1] op_sel_hi:[1,0] neg_hi:[0,1]
	v_pk_add_f32 v[4:5], v[4:5], v[12:13] op_sel:[0,1] op_sel_hi:[1,0] neg_lo:[0,1]
	s_waitcnt lgkmcnt(1)
	v_pk_add_f32 v[12:13], v[6:7], v[30:31]
	s_waitcnt lgkmcnt(0)
	v_pk_add_f32 v[20:21], v[22:23], v[34:35]
	v_pk_add_f32 v[2:3], v[2:3], v[2:3] op_sel:[0,1] op_sel_hi:[1,0] neg_hi:[0,1]
	v_pk_add_f32 v[6:7], v[6:7], v[30:31] neg_lo:[0,1] neg_hi:[0,1]
	v_pk_add_f32 v[22:23], v[22:23], v[34:35] neg_lo:[0,1] neg_hi:[0,1]
	v_pk_add_f32 v[30:31], v[12:13], v[20:21]
	v_pk_add_f32 v[20:21], v[12:13], v[20:21] neg_lo:[0,1] neg_hi:[0,1]
	v_pk_add_f32 v[12:13], v[6:7], v[22:23] op_sel:[0,1] op_sel_hi:[1,0] neg_hi:[0,1]
	v_pk_mul_f32 v[44:45], v[2:3], s[8:9]
	v_pk_add_f32 v[6:7], v[6:7], v[22:23] op_sel:[0,1] op_sel_hi:[1,0] neg_lo:[0,1]
	v_pk_add_f32 v[22:23], v[8:9], v[32:33]
	v_pk_add_f32 v[2:3], v[12:13], v[12:13] op_sel:[0,1] op_sel_hi:[1,0] neg_hi:[0,1]
	v_pk_add_f32 v[8:9], v[8:9], v[32:33] neg_lo:[0,1] neg_hi:[0,1]
	v_pk_add_f32 v[32:33], v[24:25], v[36:37]
	v_pk_mul_f32 v[12:13], v[2:3], s[8:9]
	v_pk_add_f32 v[2:3], v[6:7], v[6:7] op_sel:[0,1] op_sel_hi:[1,0] neg_lo:[0,1]
	v_pk_add_f32 v[24:25], v[24:25], v[36:37] neg_lo:[0,1] neg_hi:[0,1]
	v_pk_add_f32 v[34:35], v[22:23], v[32:33]
	v_pk_add_f32 v[32:33], v[22:23], v[32:33] neg_lo:[0,1] neg_hi:[0,1]
	v_pk_mul_f32 v[54:55], v[2:3], s[12:13]
	v_pk_add_f32 v[36:37], v[8:9], v[24:25] op_sel:[0,1] op_sel_hi:[1,0] neg_hi:[0,1]
	v_pk_add_f32 v[8:9], v[8:9], v[24:25] op_sel:[0,1] op_sel_hi:[1,0] neg_lo:[0,1]
	v_pk_mul_f32 v[22:23], v[4:5], s[10:11] op_sel:[0,0] op_sel_hi:[0,1]
	v_pk_fma_f32 v[22:23], v[4:5], s[10:11], v[22:23] op_sel:[1,1,0] op_sel_hi:[1,0,1] neg_lo:[0,1,0]
	v_pk_add_f32 v[4:5], v[28:29], v[34:35]
	v_pk_add_f32 v[2:3], v[32:33], v[32:33] op_sel:[0,1] op_sel_hi:[1,0] neg_lo:[0,1]
	v_pk_add_f32 v[28:29], v[28:29], v[34:35] neg_lo:[0,1] neg_hi:[0,1]
	v_pk_mul_f32 v[32:33], v[2:3], s[12:13]
	v_pk_add_f32 v[2:3], v[26:27], v[30:31]
	v_pk_add_f32 v[26:27], v[26:27], v[30:31] neg_lo:[0,1] neg_hi:[0,1]
	v_pk_mul_f32 v[24:25], v[10:11], s[6:7] op_sel:[0,0] op_sel_hi:[0,1]
	v_pk_fma_f32 v[24:25], v[10:11], s[6:7], v[24:25] op_sel:[1,1,0] op_sel_hi:[1,0,1] neg_lo:[0,1,0]
	v_pk_mul_f32 v[6:7], v[36:37], s[10:11] op_sel:[0,0] op_sel_hi:[0,1]
	v_pk_fma_f32 v[6:7], v[36:37], s[10:11], v[6:7] op_sel:[1,1,0] op_sel_hi:[1,0,1] neg_lo:[0,1,0]
	v_pk_mul_f32 v[56:57], v[8:9], s[14:15] op_sel:[0,0] op_sel_hi:[0,1]
	v_pk_fma_f32 v[56:57], v[8:9], s[14:15], v[56:57] op_sel:[1,1,0] op_sel_hi:[1,0,1] neg_lo:[0,1,0]
	v_pk_add_f32 v[10:11], v[2:3], v[4:5]
	v_lshlrev_b32_e32 v34, 2, v0
	v_pk_add_f32 v[4:5], v[2:3], v[4:5] neg_lo:[0,1] neg_hi:[0,1]
	v_pk_add_f32 v[8:9], v[26:27], v[28:29] op_sel:[0,1] op_sel_hi:[1,0] neg_hi:[0,1]
	v_pk_add_f32 v[2:3], v[26:27], v[28:29] op_sel:[0,1] op_sel_hi:[1,0] neg_lo:[0,1]
	v_pk_add_f32 v[26:27], v[14:15], v[12:13]
	v_pk_add_f32 v[28:29], v[24:25], v[6:7]
	v_add_u32_e32 v1, 0x400, v34
	v_pk_add_f32 v[14:15], v[14:15], v[12:13] neg_lo:[0,1] neg_hi:[0,1]
	v_pk_add_f32 v[30:31], v[24:25], v[6:7] neg_lo:[0,1] neg_hi:[0,1]
	v_pk_add_f32 v[12:13], v[26:27], v[28:29]
	v_pk_add_f32 v[6:7], v[26:27], v[28:29] neg_lo:[0,1] neg_hi:[0,1]
	v_add_u32_e32 v24, 0x800, v34
	v_add_u32_e32 v25, 0xc00, v34
	v_add_u32_e32 v26, 0x1000, v34
	v_add_u32_e32 v27, 0x1400, v34
	v_add_u32_e32 v28, 0x1800, v34
	v_add_u32_e32 v29, 0x1c00, v34
	v_add_u32_e32 v35, 0x2000, v34
	s_waitcnt vmcnt(0)
	v_mov_b32_e32 v1, v113
	s_nop 0
	v_mov_b32_e32 v36, v114
	v_mov_b32_e32 v37, v115
	v_mov_b32_e32 v38, v116
	v_mov_b32_e32 v39, v117
	v_mov_b32_e32 v40, v118
	v_mov_b32_e32 v41, v119
	v_mov_b32_e32 v42, v120
	v_add_u32_e32 v24, 0x2400, v34
	v_add_u32_e32 v25, 0x2800, v34
	v_add_u32_e32 v26, 0x2c00, v34
	v_add_u32_e32 v27, 0x3000, v34
	v_add_u32_e32 v28, 0x3400, v34
	v_add_u32_e32 v35, 0x3800, v34
	v_mov_b32_e32 v52, v112
	v_mov_b32_e32 v43, v126
	v_add_u32_e32 v29, 0x3c00, v34
	v_mov_b32_e32 v47, v121
	v_mov_b32_e32 v48, v122
	v_mov_b32_e32 v49, v123
	v_mov_b32_e32 v50, v124
	v_mov_b32_e32 v51, v125
	v_mov_b32_e32 v46, v127
	v_pk_add_f32 v[26:27], v[16:17], v[20:21] op_sel:[0,1] op_sel_hi:[1,0] neg_hi:[0,1]
	v_pk_add_f32 v[16:17], v[16:17], v[20:21] op_sel:[0,1] op_sel_hi:[1,0] neg_lo:[0,1]
	v_pk_add_f32 v[20:21], v[44:45], v[32:33]
	v_pk_add_f32 v[28:29], v[44:45], v[32:33] neg_lo:[0,1] neg_hi:[0,1]
	v_pk_add_f32 v[24:25], v[14:15], v[30:31] op_sel:[0,1] op_sel_hi:[1,0] neg_hi:[0,1]
	v_pk_add_f32 v[14:15], v[14:15], v[30:31] op_sel:[0,1] op_sel_hi:[1,0] neg_lo:[0,1]
	v_pk_add_f32 v[30:31], v[20:21], v[26:27]
	v_pk_add_f32 v[20:21], v[26:27], v[20:21] neg_lo:[0,1] neg_hi:[0,1]
	v_pk_add_f32 v[26:27], v[16:17], v[28:29] op_sel:[0,1] op_sel_hi:[1,0] neg_hi:[0,1]
	v_pk_add_f32 v[16:17], v[16:17], v[28:29] op_sel:[0,1] op_sel_hi:[1,0] neg_lo:[0,1]
	v_pk_add_f32 v[28:29], v[18:19], v[54:55]
	v_pk_add_f32 v[44:45], v[22:23], v[56:57]
	s_mov_b32 s2, 0xff61b1e6
	v_pk_add_f32 v[18:19], v[18:19], v[54:55] neg_lo:[0,1] neg_hi:[0,1]
	v_pk_add_f32 v[54:55], v[22:23], v[56:57] neg_lo:[0,1] neg_hi:[0,1]
	v_pk_add_f32 v[32:33], v[28:29], v[44:45]
	v_pk_add_f32 v[22:23], v[28:29], v[44:45] neg_lo:[0,1] neg_hi:[0,1]
	v_max3_f32 v44, v10, s2, v12
	v_max3_f32 v44, v44, v30, v32
	v_max3_f32 v44, v44, v8, v24
	v_pk_add_f32 v[28:29], v[18:19], v[54:55] op_sel:[0,1] op_sel_hi:[1,0] neg_hi:[0,1]
	v_pk_add_f32 v[18:19], v[18:19], v[54:55] op_sel:[0,1] op_sel_hi:[1,0] neg_lo:[0,1]
	v_max3_f32 v45, -v11, s2, -v13
	v_max3_f32 v44, v44, v26, v28
	v_max3_f32 v44, v44, v4, v6
	v_max3_f32 v44, v44, v20, v22
	v_max3_f32 v44, v44, v2, v14
	v_max3_f32 v44, v44, v16, v18
	v_max3_f32 v45, v45, -v31, -v33
	v_max3_f32 v45, v45, -v9, -v25
	v_mov_b32_dpp v53, v44 quad_perm:[1,0,3,2] row_mask:0xf bank_mask:0xf
	v_max_f32_e32 v53, v53, v53
	v_max_f32_e32 v44, v44, v53
	v_mov_b32_e32 v53, 0
	v_max3_f32 v45, v45, -v27, -v29
	v_max3_f32 v45, v45, -v5, -v7
	v_mov_b32_dpp v53, v44 quad_perm:[2,3,0,1] row_mask:0xf bank_mask:0xf
	v_max_f32_e32 v53, v53, v53
	v_max_f32_e32 v44, v44, v53
	v_mov_b32_e32 v53, 0
	v_max3_f32 v45, v45, -v21, -v23
	v_max3_f32 v45, v45, -v3, -v15
	v_mov_b32_dpp v53, v44 row_half_mirror row_mask:0xf bank_mask:0xf
	v_max_f32_e32 v53, v53, v53
	v_max_f32_e32 v44, v44, v53
	v_mov_b32_e32 v53, 0
	v_max3_f32 v45, v45, -v17, -v19
	s_nop 0
	v_mov_b32_dpp v53, v44 row_mirror row_mask:0xf bank_mask:0xf
	v_max_f32_e32 v53, v53, v53
	v_max_f32_e32 v44, v44, v53
	s_nop 0
	v_readlane_b32 s5, v44, 0
	v_readlane_b32 s6, v44, 16
	v_readlane_b32 s7, v44, 32
	v_readlane_b32 s8, v44, 48
	v_mov_b32_e32 v44, 0
	s_nop 1
	v_mov_b32_dpp v44, v45 quad_perm:[1,0,3,2] row_mask:0xf bank_mask:0xf
	v_max_f32_e32 v44, v44, v44
	v_max_f32_e32 v44, v45, v44
	v_mov_b32_e32 v45, 0
	s_nop 1
	v_mov_b32_dpp v45, v44 quad_perm:[2,3,0,1] row_mask:0xf bank_mask:0xf
	v_max_f32_e32 v45, v45, v45
	v_max_f32_e32 v44, v44, v45
	v_mov_b32_e32 v45, 0
	s_nop 1
	v_mov_b32_dpp v45, v44 row_half_mirror row_mask:0xf bank_mask:0xf
	v_max_f32_e32 v45, v45, v45
	v_max_f32_e32 v44, v44, v45
	v_mov_b32_e32 v45, 0
	s_nop 1
	v_mov_b32_dpp v45, v44 row_mirror row_mask:0xf bank_mask:0xf
	v_max_f32_e32 v45, v45, v45
	v_max_f32_e32 v44, v44, v45
	v_and_b32_e32 v45, 63, v0
	v_readlane_b32 s9, v44, 0
	v_readlane_b32 s10, v44, 16
	v_readlane_b32 s11, v44, 32
	v_readlane_b32 s12, v44, 48
	v_ashrrev_i32_e32 v44, 6, v0
	v_cmp_eq_u32_e32 vcc, 0, v45
	v_lshlrev_b32_e32 v61, 3, v44
	s_and_saveexec_b64 s[2:3], vcc
	s_cbranch_execz .LBB1_10
	v_max_f32_e64 v44, s12, s12
	v_max_f32_e64 v45, s11, s11
	v_max_f32_e32 v44, v45, v44
	v_mov_b32_e32 v45, s10
	v_max3_f32 v45, s9, v45, v44
	v_max_f32_e64 v44, s8, s8
	v_max_f32_e64 v53, s7, s7
	v_max_f32_e32 v44, v53, v44
	v_mov_b32_e32 v53, s6
	v_max3_f32 v44, s5, v53, v44
	ds_write_b64 v61, v[44:45] offset:36864

.LBB1_12:
	s_or_b64 exec, exec, s[8:9]
	s_waitcnt vmcnt(7)
	v_and_b32_e32 v23, 0xffff, v52
	v_and_b32_e32 v52, 0xffff, v1
	v_mov_b32_e32 v1, 0
	v_and_b32_e32 v61, 0xffff, v36
	v_and_b32_e32 v62, 0xffff, v37
	v_and_b32_e32 v63, 0xffff, v38
	v_and_b32_e32 v64, 0xffff, v39
	v_and_b32_e32 v65, 0xffff, v40
	v_and_b32_e32 v66, 0xffff, v41
	v_and_b32_e32 v67, 0xffff, v42
	s_waitcnt vmcnt(6)
	v_and_b32_e32 v14, 0xffff, v43
	s_waitcnt lgkmcnt(0)
	s_barrier
	ds_read_b128 v[36:39], v1 offset:36896
	ds_read_b128 v[40:43], v1 offset:36912
	s_mov_b32 s5, 0
	s_lshl_b64 s[2:3], s[4:5], 16
	s_add_u32 s0, s0, s2
	s_waitcnt lgkmcnt(1)
	v_add_f32_e32 v16, v36, v38
	s_waitcnt lgkmcnt(0)
	v_add_f32_e32 v18, v40, v42
	s_addc_u32 s1, s1, s3
	s_lshl_b32 s2, s16, 1
	v_add_f32_e32 v16, v16, v18
	s_mov_b32 s4, 0x45800000
	s_add_u32 s0, s0, s2
	v_div_scale_f32 v18, s[2:3], v16, v16, s4
	v_rcp_f32_e32 v36, v18
	v_add_f32_e32 v37, v37, v39
	v_add_f32_e32 v38, v41, v43
	v_add_f32_e32 v37, v37, v38
	v_fma_f32 v38, -v18, v36, 1.0
	v_fmac_f32_e32 v36, v38, v36
	v_div_scale_f32 v38, vcc, s4, v16, s4
	v_mul_f32_e32 v39, v38, v36
	v_fma_f32 v40, -v18, v39, v38
	v_fmac_f32_e32 v39, v40, v36
	v_fma_f32 v18, -v18, v39, v38
	v_div_scale_f32 v38, s[2:3], v37, v37, s4
	v_rcp_f32_e32 v40, v38
	v_div_fmas_f32 v18, v18, v36, v39
	v_div_fixup_f32 v16, v18, v16, s4
	s_addc_u32 s1, s1, 0
	v_fma_f32 v18, -v38, v40, 1.0
	v_fmac_f32_e32 v40, v18, v40
	v_div_scale_f32 v18, vcc, s4, v37, s4
	v_mul_f32_e32 v36, v18, v40
	v_fma_f32 v39, -v38, v36, v18
	v_fmac_f32_e32 v36, v39, v40
	v_fma_f32 v18, -v38, v36, v18
	v_div_fmas_f32 v18, v18, v40, v36
	v_cvt_f32_fp8_e32 v36, v23
	v_cvt_f32_fp8_sdwa v23, v23 src0_sel:BYTE_1
	v_div_fixup_f32 v18, v18, v37, s4
	v_mul_f32_e32 v37, v16, v59
	v_mul_f32_e32 v36, v37, v36
	v_mul_f32_e32 v37, v18, v60
	v_mul_f32_e32 v23, v37, v23
	v_mov_b32_e32 v38, 0
	v_cvt_pk_fp8_f32 v38, v36, v23
	v_cvt_f32_fp8_e32 v23, v52
	v_cvt_f32_fp8_sdwa v36, v52 src0_sel:BYTE_1
	v_mul_f32_e32 v37, v16, v57
	v_cvt_pk_fp8_f32 v38, 0, 0 op_sel:[0,0,1]
	v_mul_f32_e32 v23, v37, v23
	v_mul_f32_e32 v37, v18, v58
	v_lshlrev_b32_e32 v0, 3, v0
	v_mul_f32_e32 v36, v37, v36
	v_mov_b32_e32 v39, v1
	v_cvt_pk_fp8_f32 v39, v23, v36
	v_lshl_add_u64 v[36:37], v[0:1], 1, s[0:1]
	v_cvt_f32_fp8_e32 v23, v61
	global_store_short v[36:37], v38, off
	v_cvt_f32_fp8_sdwa v38, v61 src0_sel:BYTE_1
	v_mul_f32_e32 v40, v16, v55
	v_mul_f32_e32 v23, v40, v23
	v_mul_f32_e32 v40, v18, v56
	v_cvt_pk_fp8_f32 v39, 0, 0 op_sel:[0,0,1]
	v_mul_f32_e32 v38, v40, v38
	v_mov_b32_e32 v40, v1
	v_cvt_pk_fp8_f32 v40, v23, v38
	v_cvt_f32_fp8_e32 v23, v62
	v_add_u32_e32 v36, 0x800, v0
	v_mov_b32_e32 v37, v1
	v_cvt_f32_fp8_sdwa v38, v62 src0_sel:BYTE_1
	v_lshl_add_u64 v[36:37], v[36:37], 1, s[0:1]
	global_store_short v[36:37], v39, off
	v_mul_f32_e32 v39, v16, v53
	v_mul_f32_e32 v23, v39, v23
	v_mul_f32_e32 v39, v18, v54
	v_cvt_pk_fp8_f32 v40, 0, 0 op_sel:[0,0,1]
	v_mul_f32_e32 v38, v39, v38
	v_mov_b32_e32 v39, v1
	v_cvt_pk_fp8_f32 v39, v23, v38
	v_cvt_f32_fp8_e32 v23, v63
	v_add_u32_e32 v36, 0x1000, v0
	v_mov_b32_e32 v37, v1
	v_cvt_f32_fp8_sdwa v38, v63 src0_sel:BYTE_1
	v_lshl_add_u64 v[36:37], v[36:37], 1, s[0:1]
	global_store_short v[36:37], v40, off
	v_mul_f32_e32 v40, v16, v44
	v_mul_f32_e32 v23, v40, v23
	v_mul_f32_e32 v40, v18, v45
	v_mul_f32_e32 v38, v40, v38
	v_mov_b32_e32 v40, v1
	v_cvt_pk_fp8_f32 v40, v23, v38
	v_cvt_f32_fp8_e32 v23, v64
	v_cvt_f32_fp8_sdwa v38, v64 src0_sel:BYTE_1
	v_cvt_pk_fp8_f32 v39, 0, 0 op_sel:[0,0,1]
	v_mul_f32_e32 v32, v16, v32
	v_add_u32_e32 v36, 0x1800, v0
	v_mov_b32_e32 v37, v1
	v_mul_f32_e32 v23, v32, v23
	v_mul_f32_e32 v32, v18, v33
	v_lshl_add_u64 v[36:37], v[36:37], 1, s[0:1]
	v_mul_f32_e32 v32, v32, v38
	v_mov_b32_e32 v38, v1
	global_store_short v[36:37], v39, off
	v_add_u32_e32 v36, 0x2000, v0
	v_mov_b32_e32 v37, v1
	v_cvt_pk_fp8_f32 v38, v23, v32
	v_cvt_f32_fp8_e32 v23, v65
	v_lshl_add_u64 v[32:33], v[36:37], 1, s[0:1]
	v_cvt_f32_fp8_sdwa v36, v65 src0_sel:BYTE_1
	v_cvt_pk_fp8_f32 v40, 0, 0 op_sel:[0,0,1]
	v_mul_f32_e32 v30, v16, v30
	v_mul_f32_e32 v23, v30, v23
	v_mul_f32_e32 v30, v18, v31
	v_mul_f32_e32 v30, v30, v36
	v_mov_b32_e32 v36, v1
	global_store_short v[32:33], v40, off
	v_add_u32_e32 v32, 0x2800, v0
	v_mov_b32_e32 v33, v1
	v_cvt_pk_fp8_f32 v36, v23, v30
	v_cvt_f32_fp8_e32 v23, v66
	v_lshl_add_u64 v[30:31], v[32:33], 1, s[0:1]
	v_cvt_f32_fp8_sdwa v32, v66 src0_sel:BYTE_1
	v_cvt_pk_fp8_f32 v38, 0, 0 op_sel:[0,0,1]
	v_mul_f32_e32 v28, v16, v28
	v_mul_f32_e32 v23, v28, v23
	v_mul_f32_e32 v28, v18, v29
	v_mul_f32_e32 v28, v28, v32
	v_mov_b32_e32 v32, v1
	global_store_short v[30:31], v38, off
	v_add_u32_e32 v30, 0x3000, v0
	v_mov_b32_e32 v31, v1
	v_cvt_pk_fp8_f32 v32, v23, v28
	v_cvt_f32_fp8_e32 v23, v67
	v_lshl_add_u64 v[28:29], v[30:31], 1, s[0:1]
	v_cvt_f32_fp8_sdwa v30, v67 src0_sel:BYTE_1
	v_mul_f32_e32 v26, v16, v26
	v_mul_f32_e32 v23, v26, v23
	v_mul_f32_e32 v26, v18, v27
	s_waitcnt vmcnt(11)
	v_and_b32_e32 v22, 0xffff, v47
	v_mul_f32_e32 v26, v26, v30
	v_mov_b32_e32 v30, v1
	v_cvt_pk_fp8_f32 v30, v23, v26
	v_cvt_f32_fp8_e32 v23, v22
	s_waitcnt vmcnt(10)
	v_and_b32_e32 v21, 0xffff, v48
	v_mul_f32_e32 v24, v16, v24
	v_cvt_f32_fp8_sdwa v22, v22 src0_sel:BYTE_1
	v_mul_f32_e32 v23, v24, v23
	v_mul_f32_e32 v24, v18, v25
	v_cvt_f32_fp8_e32 v25, v21
	v_cvt_f32_fp8_sdwa v21, v21 src0_sel:BYTE_1
	v_mul_f32_e32 v13, v16, v13
	v_mul_f32_e32 v20, v18, v20
	s_waitcnt vmcnt(9)
	v_and_b32_e32 v19, 0xffff, v49
	v_cvt_pk_fp8_f32 v36, 0, 0 op_sel:[0,0,1]
	v_mul_f32_e32 v13, v13, v25
	v_mul_f32_e32 v20, v20, v21
	v_mov_b32_e32 v25, v1
	v_mul_f32_e32 v22, v24, v22
	v_mov_b32_e32 v24, v1
	v_cvt_pk_fp8_f32 v25, v13, v20
	v_cvt_f32_fp8_e32 v13, v19
	v_cvt_f32_fp8_sdwa v19, v19 src0_sel:BYTE_1
	v_cvt_pk_fp8_f32 v32, 0, 0 op_sel:[0,0,1]
	v_cvt_pk_fp8_f32 v24, v23, v22
	global_store_short v[28:29], v36, off
	v_add_u32_e32 v28, v35, v34
	v_mov_b32_e32 v29, v1
	v_cvt_pk_fp8_f32 v30, 0, 0 op_sel:[0,0,1]
	v_mul_f32_e32 v10, v16, v10
	v_mul_f32_e32 v11, v18, v11
	v_lshl_add_u64 v[26:27], v[28:29], 1, s[0:1]
	v_mul_f32_e32 v10, v10, v13
	v_mul_f32_e32 v11, v11, v19
	v_mov_b32_e32 v13, v1
	global_store_short v[26:27], v32, off
	v_add_u32_e32 v26, 0x4000, v0
	v_mov_b32_e32 v27, v1
	v_cvt_pk_fp8_f32 v24, 0, 0 op_sel:[0,0,1]
	v_cvt_pk_fp8_f32 v13, v10, v11
	v_lshl_add_u64 v[22:23], v[26:27], 1, s[0:1]
	s_waitcnt vmcnt(10)
	v_and_b32_e32 v17, 0xffff, v50
	global_store_short v[22:23], v30, off
	v_add_u32_e32 v22, 0x4800, v0
	v_mov_b32_e32 v23, v1
	v_cvt_pk_fp8_f32 v25, 0, 0 op_sel:[0,0,1]
	v_lshl_add_u64 v[20:21], v[22:23], 1, s[0:1]
	v_cvt_f32_fp8_e32 v19, v17
	v_cvt_f32_fp8_sdwa v17, v17 src0_sel:BYTE_1
	global_store_short v[20:21], v24, off
	v_add_u32_e32 v20, 0x5000, v0
	v_mov_b32_e32 v21, v1
	v_cvt_pk_fp8_f32 v13, 0, 0 op_sel:[0,0,1]
	v_lshl_add_u64 v[10:11], v[20:21], 1, s[0:1]
	global_store_short v[10:11], v25, off
	v_add_u32_e32 v10, 0x5800, v0
	v_mov_b32_e32 v11, v1
	v_mul_f32_e32 v8, v16, v8
	v_mul_f32_e32 v9, v18, v9
	s_waitcnt vmcnt(12)
	v_and_b32_e32 v15, 0xffff, v51
	v_lshl_add_u64 v[10:11], v[10:11], 1, s[0:1]
	v_mul_f32_e32 v8, v8, v19
	v_mul_f32_e32 v9, v9, v17
	v_mov_b32_e32 v17, v1
	v_cvt_pk_fp8_f32 v17, v8, v9
	global_store_short v[10:11], v13, off
	v_cvt_f32_fp8_e32 v9, v15
	v_cvt_f32_fp8_sdwa v10, v15 src0_sel:BYTE_1
	v_mul_f32_e32 v6, v16, v6
	v_mul_f32_e32 v7, v18, v7
	v_mul_f32_e32 v6, v6, v9
	v_mul_f32_e32 v7, v7, v10
	v_mov_b32_e32 v10, v1
	v_cvt_pk_fp8_f32 v10, v6, v7
	v_cvt_pk_fp8_f32 v17, 0, 0 op_sel:[0,0,1]
	v_add_u32_e32 v8, 0x6000, v0
	v_mov_b32_e32 v9, v1
	v_cvt_pk_fp8_f32 v10, 0, 0 op_sel:[0,0,1]
	v_lshl_add_u64 v[6:7], v[8:9], 1, s[0:1]
	global_store_short v[6:7], v17, off
	v_add_u32_e32 v6, 0x6800, v0
	v_mov_b32_e32 v7, v1
	v_lshl_add_u64 v[6:7], v[6:7], 1, s[0:1]
	global_store_short v[6:7], v10, off
	v_cvt_f32_fp8_e32 v7, v14
	v_cvt_f32_fp8_sdwa v8, v14 src0_sel:BYTE_1
	v_mul_f32_e32 v4, v16, v4
	v_mul_f32_e32 v5, v18, v5
	s_waitcnt vmcnt(14)
	v_and_b32_e32 v12, 0xffff, v46
	v_mul_f32_e32 v4, v4, v7
	v_mul_f32_e32 v5, v5, v8
	v_mov_b32_e32 v8, v1
	v_cvt_f32_fp8_e32 v7, v12
	v_cvt_pk_fp8_f32 v8, v4, v5
	v_cvt_f32_fp8_sdwa v4, v12 src0_sel:BYTE_1
	v_mul_f32_e32 v2, v16, v2
	v_mul_f32_e32 v3, v18, v3
	v_mul_f32_e32 v2, v2, v7
	v_mul_f32_e32 v3, v3, v4
	v_mov_b32_e32 v4, v1
	v_cvt_pk_fp8_f32 v4, v2, v3
	v_cvt_pk_fp8_f32 v8, 0, 0 op_sel:[0,0,1]
	v_add_u32_e32 v6, 0x7000, v0
	v_mov_b32_e32 v7, v1
	v_cvt_pk_fp8_f32 v4, 0, 0 op_sel:[0,0,1]
	v_add_u32_e32 v0, 0x7800, v0
	v_lshl_add_u64 v[2:3], v[6:7], 1, s[0:1]
	v_lshl_add_u64 v[0:1], v[0:1], 1, s[0:1]
	global_store_short v[2:3], v8, off
	global_store_short v[0:1], v4, off
	s_endpgm
	s_nop 0
	s_nop 0
	s_nop 0
	s_nop 0
	s_nop 0
	s_nop 0
	s_nop 0
	s_nop 0
	s_nop 0
	s_nop 0
	s_nop 0
	s_nop 0
	s_nop 0
	s_nop 0
	s_nop 0
	s_endpgm

	.amdhsa_kernel _Z5k_fftPKtPtPKDv2_f
		.amdhsa_group_segment_fixed_size 36928
		.amdhsa_private_segment_fixed_size 0
		.amdhsa_kernarg_size 24
		.amdhsa_user_sgpr_count 2
		.amdhsa_user_sgpr_dispatch_ptr 0
		.amdhsa_user_sgpr_queue_ptr 0
		.amdhsa_user_sgpr_kernarg_segment_ptr 1
		.amdhsa_user_sgpr_dispatch_id 0
		.amdhsa_user_sgpr_kernarg_preload_length 0
		.amdhsa_user_sgpr_kernarg_preload_offset 0
		.amdhsa_user_sgpr_private_segment_size 0
		.amdhsa_uses_dynamic_stack 0
		.amdhsa_enable_private_segment 0
		.amdhsa_system_sgpr_workgroup_id_x 1
		.amdhsa_system_sgpr_workgroup_id_y 0
		.amdhsa_system_sgpr_workgroup_id_z 0
		.amdhsa_system_sgpr_workgroup_info 0
		.amdhsa_system_vgpr_workitem_id 0
		.amdhsa_next_free_vgpr 128
		.amdhsa_next_free_sgpr 96
		.amdhsa_accum_offset 128
		.amdhsa_reserve_vcc 1
		.amdhsa_float_round_mode_32 0
		.amdhsa_float_round_mode_16_64 0
		.amdhsa_float_denorm_mode_32 3
		.amdhsa_float_denorm_mode_16_64 3
		.amdhsa_dx10_clamp 1
		.amdhsa_ieee_mode 1
		.amdhsa_fp16_overflow 0
		.amdhsa_tg_split 0
		.amdhsa_exception_fp_ieee_invalid_op 0
		.amdhsa_exception_fp_denorm_src 0
		.amdhsa_exception_fp_ieee_div_zero 0
		.amdhsa_exception_fp_ieee_overflow 0
		.amdhsa_exception_fp_ieee_underflow 0
		.amdhsa_exception_fp_ieee_inexact 0
		.amdhsa_exception_int_div_zero 0
	.end_amdhsa_kernel

amdhsa.kernels:
  - .agpr_count:     0
    .args:
      - .actual_access:  read_only
        .address_space:  global
        .offset:         0
        .size:           8
        .value_kind:     global_buffer
      - .actual_access:  write_only
        .address_space:  global
        .offset:         8
        .size:           8
        .value_kind:     global_buffer
      - .offset:         16
        .size:           4
        .value_kind:     by_value
      - .actual_access:  read_only
        .address_space:  global
        .offset:         24
        .size:           8
        .value_kind:     global_buffer
      - .actual_access:  read_only
        .address_space:  global
        .offset:         32
        .size:           8
        .value_kind:     global_buffer
      - .actual_access:  read_only
        .address_space:  global
        .offset:         40
        .size:           8
        .value_kind:     global_buffer
      - .actual_access:  read_only
        .address_space:  global
        .offset:         48
        .size:           8
        .value_kind:     global_buffer
      - .actual_access:  write_only
        .address_space:  global
        .offset:         56
        .size:           8
        .value_kind:     global_buffer
      - .actual_access:  write_only
        .address_space:  global
        .offset:         64
        .size:           8
        .value_kind:     global_buffer
      - .actual_access:  write_only
        .address_space:  global
        .offset:         72
        .size:           8
        .value_kind:     global_buffer
    .group_segment_fixed_size: 16640
    .kernarg_segment_align: 8
    .kernarg_segment_size: 80
    .language:       OpenCL C
    .language_version:
      - 2
      - 0
    .max_flat_workgroup_size: 256
    .name:           _Z6k_prepPK15HIP_vector_typeIfLj4EEPS_IjLj4EEiPKfS6_S6_S6_PtS7_PS_IfLj2EE
    .private_segment_fixed_size: 0
    .sgpr_count:     22
    .sgpr_spill_count: 0
    .symbol:         _Z6k_prepPK15HIP_vector_typeIfLj4EEPS_IjLj4EEiPKfS6_S6_S6_PtS7_PS_IfLj2EE.kd
    .uniform_work_group_size: 1
    .uses_dynamic_stack: false
    .vgpr_count:     45
    .vgpr_spill_count: 0
    .wavefront_size: 64
  - .agpr_count:     0
    .args:
      - .actual_access:  read_only
        .address_space:  global
        .offset:         0
        .size:           8
        .value_kind:     global_buffer
      - .actual_access:  write_only
        .address_space:  global
        .offset:         8
        .size:           8
        .value_kind:     global_buffer
      - .actual_access:  read_only
        .address_space:  global
        .offset:         16
        .size:           8
        .value_kind:     global_buffer
    .group_segment_fixed_size: 36928
    .kernarg_segment_align: 8
    .kernarg_segment_size: 24
    .language:       OpenCL C
    .language_version:
      - 2
      - 0
    .max_flat_workgroup_size: 256
    .name:           _Z5k_fftPKtPtPKDv2_f
    .private_segment_fixed_size: 0
    .sgpr_count:     23
    .sgpr_spill_count: 0
    .symbol:         _Z5k_fftPKtPtPKDv2_f.kd
    .uniform_work_group_size: 1
    .uses_dynamic_stack: false
    .vgpr_count:     128
    .vgpr_spill_count: 0
    .wavefront_size: 64
  - .agpr_count:     0
    .args:
      - .address_space:  global
        .offset:         0
        .size:           8
        .value_kind:     global_buffer
      - .address_space:  global
        .offset:         8
        .size:           8
        .value_kind:     global_buffer
      - .actual_access:  write_only
        .address_space:  global
        .offset:         16
        .size:           8
        .value_kind:     global_buffer
      - .actual_access:  read_only
        .address_space:  global
        .offset:         24
        .size:           8
        .value_kind:     global_buffer
      - .actual_access:  read_only
        .address_space:  global
        .offset:         32
        .size:           8
        .value_kind:     global_buffer
      - .actual_access:  read_only
        .address_space:  global
        .offset:         40
        .size:           8
        .value_kind:     global_buffer
      - .offset:         48
        .size:           4
        .value_kind:     by_value
      - .offset:         52
        .size:           4
        .value_kind:     by_value
    .group_segment_fixed_size: 0
    .kernarg_segment_align: 8
    .kernarg_segment_size: 56
    .language:       OpenCL C
    .language_version:
      - 2
      - 0
    .max_flat_workgroup_size: 512
    .name:           _Z6k_gemmILi2EEvPKtS1_PvPKfS4_S4_ii
    .private_segment_fixed_size: 0
    .sgpr_count:     92
    .sgpr_spill_count: 0
    .symbol:         _Z6k_gemmILi2EEvPKtS1_PvPKfS4_S4_ii.kd
    .uniform_work_group_size: 1
    .uses_dynamic_stack: false
    .vgpr_count:     256
    .vgpr_spill_count: 0
    .wavefront_size: 64
  - .agpr_count:     0
    .args:
      - .address_space:  global
        .offset:         0
        .size:           8
        .value_kind:     global_buffer
      - .address_space:  global
        .offset:         8
        .size:           8
        .value_kind:     global_buffer
      - .actual_access:  write_only
        .address_space:  global
        .offset:         16
        .size:           8
        .value_kind:     global_buffer
      - .actual_access:  read_only
        .address_space:  global
        .offset:         24
        .size:           8
        .value_kind:     global_buffer
      - .actual_access:  read_only
        .address_space:  global
        .offset:         32
        .size:           8
        .value_kind:     global_buffer
      - .actual_access:  read_only
        .address_space:  global
        .offset:         40
        .size:           8
        .value_kind:     global_buffer
      - .offset:         48
        .size:           4
        .value_kind:     by_value
      - .offset:         52
        .size:           4
        .value_kind:     by_value
    .group_segment_fixed_size: 0
    .kernarg_segment_align: 8
    .kernarg_segment_size: 56
    .language:       OpenCL C
    .language_version:
      - 2
      - 0
    .max_flat_workgroup_size: 512
    .name:           _Z6k_gemmILi4EEvPKtS1_PvPKfS4_S4_ii
    .private_segment_fixed_size: 0
    .sgpr_count:     62
    .sgpr_spill_count: 0
    .symbol:         _Z6k_gemmILi4EEvPKtS1_PvPKfS4_S4_ii.kd
    .uniform_work_group_size: 1
    .uses_dynamic_stack: false
    .vgpr_count:     254
    .vgpr_spill_count: 0
    .wavefront_size: 64
